# peel first K-loop iteration in all 25 GEMM loops: first MFMA per accumulator takes C=0, 128-register preheader clear removed
# speedup vs baseline: 1.0118x; 1.0055x over previous
; #define PG8_STAGE(bufoff, gbase, voff) do { _Pragma("unroll") for (int _i = 0; _i < 2; ++_i) \
;         __builtin_amdgcn_global_load_lds((const unsigned*)((const char*)(gbase) + (voff)[_i]), (PG8_LAS unsigned*)(lds + (bufoff) + ldsw + _i * 8192), 16, 0, 0); } while (0)
; #define PG8_LDA(dst, b, h) do { if constexpr (DT != 1) { _Pragma("unroll") for (int m = 0; m < 4; ++m) _Pragma("unroll") for (int k = 0; k < 2; ++k) dst[m][k] = *(const PG8_LAS bf16x8*)(lds + PG8_SA(b, h) + aoff + m * 2048 + k * 1024); } \
;         else { _Pragma("unroll") for (int m = 0; m < 4; ++m) dst##8[m] = ld32(lds + PG8_SA(b, h) + aoff + m * 2048); } } while (0)
; #define PG8_LDB(dst, b, h) do { if constexpr (DT != 1) { _Pragma("unroll") for (int n = 0; n < 2; ++n) _Pragma("unroll") for (int k = 0; k < 2; ++k) dst[n][k] = *(const PG8_LAS bf16x8*)(lds + PG8_SB(b, h) + boff + n * 2048 + k * 1024); } \
;         else { _Pragma("unroll") for (int n = 0; n < 2; ++n) dst##8[n] = ld32(lds + PG8_SB(b, h) + boff + n * 2048); } } while (0)
; #define PG8_WAIT_V(n) asm volatile("s_waitcnt vmcnt(" #n ")" ::: "memory")
; #define PG8_WAIT_L(n) asm volatile("s_waitcnt lgkmcnt(" #n ")" ::: "memory")
; #define PG8_BAR __builtin_amdgcn_s_barrier()
; #define PG8_SCHED __builtin_amdgcn_sched_barrier(0)
;     ...
;         const char* nA = has_next ? (const char*)g.A + (size_t)nxt.pm * tstepA : cA; const char* nB = has_next ? (const char*)g.Bt + (size_t)nxt.pn * tstepB : cB;
;         for (int t = 0; t < nt; t += 2) {
;             const bool last = (t == nt - 2);
;             const char* a1 = cA + (size_t)(t + 1) * kstep;
;             const char* a2 = last ? nA : cA + (size_t)(t + 2) * kstep; const char* b2 = last ? nB : cB + (size_t)(t + 2) * kstep;
;             const char* a3 = a2 + kstep; const char* b3 = b2 + kstep;
;             if (last && has_next) S.a_ready(nxt);
;             if constexpr (SP2) {
;             PG8_LDB(B0, 0, 0); PG8_LDB(B1, 0, 1); PG8_SCHED; PG8_LDA(At, 0, 0); PG8_STAGE(PG8_SA(1, 1), a1 + hstepA, voffA);
;             PG8_WAIT_V(8); PG8_WAIT_L(0); PG8_BAR; PG8_MMA(0, 0, At, B0); PG8_MMA(0, 1, At, B1); PG8_BAR; PG8_SCHED;
.Lzs_1:
	s_cbranch_vccnz .LBB0_228
	s_and_b64 s[28:29], s[0:1], exec
	s_cselect_b32 s15, s19, s27
	s_cselect_b32 s17, s18, s26
	s_cselect_b32 s64, s21, s25
	s_cselect_b32 s65, s20, s24
	s_add_u32 s66, s24, 0x100
	s_addc_u32 s67, s25, 0
	s_add_u32 s24, s26, 0x40080
	s_addc_u32 s25, s27, 0
	s_mov_b32 s26, 0
	s_lshl_b32 s98, s63, 8
	s_ashr_i32 s99, s98, 31
	v_lshl_add_u64 v[242:243], s[98:99], 2, v[154:155]
	global_load_dwordx4 v[226:229], v[242:243], off
	global_load_dwordx4 v[230:233], v[242:243], off offset:512
	global_load_dwordx4 v[234:237], v[242:243], off offset:16
	global_load_dwordx4 v[238:241], v[242:243], off offset:528
	v_add_u32_e32 v142, s35, v164
	v_add_u32_e32 v180, s36, v164
	ds_read_b128 v[130:133], v142
	ds_read_b128 v[134:137], v142 offset:1024
	ds_read_b128 v[138:141], v142 offset:2048
	ds_read_b128 v[142:145], v142 offset:3072
	ds_read_b128 v[168:171], v180
	ds_read_b128 v[172:175], v180 offset:1024
	ds_read_b128 v[176:179], v180 offset:2048
	ds_read_b128 v[180:183], v180 offset:3072
	s_add_i32 s68, s26, 2
	s_add_u32 s27, s24, 0xfffc0080
	s_addc_u32 s28, s25, -1
	s_cmp_eq_u32 s61, s26
	s_cselect_b32 s26, s65, s66
	s_cselect_b32 s29, s15, s28
	s_cselect_b32 s28, s17, s27
	s_cselect_b32 s27, s64, s67
	s_add_i32 m0, s46, 0xc000
	ds_read_b128 v[184:187], v167
	ds_read_b128 v[188:191], v167 offset:1024
	ds_read_b128 v[192:195], v167 offset:2048
	ds_read_b128 v[196:199], v167 offset:3072
	ds_read_b128 v[200:203], v167 offset:4096
	ds_read_b128 v[204:207], v167 offset:5120
	ds_read_b128 v[208:211], v167 offset:6144
	ds_read_b128 v[212:215], v167 offset:7168
	global_load_lds_dwordx4 v158, s[24:25]
	s_add_i32 m0, s46, 0xe000
	s_nop 0
	global_load_lds_dwordx4 v156, s[24:25]
	s_waitcnt vmcnt(8) lgkmcnt(0)
	s_barrier
	s_setprio 1
	v_mfma_i32_16x16x64_i8 v[126:129], v[130:133], v[184:187], 0
	v_mfma_i32_16x16x64_i8 v[118:121], v[138:141], v[184:187], 0
	v_mfma_i32_16x16x64_i8 v[110:113], v[130:133], v[192:195], 0
	v_mfma_i32_16x16x64_i8 v[102:105], v[138:141], v[192:195], 0
	v_mfma_i32_16x16x64_i8 v[94:97], v[130:133], v[200:203], 0
	v_mfma_i32_16x16x64_i8 v[86:89], v[138:141], v[200:203], 0
	v_mfma_i32_16x16x64_i8 v[78:81], v[130:133], v[208:211], 0
	v_mfma_i32_16x16x64_i8 v[70:73], v[138:141], v[208:211], 0
	v_mfma_i32_16x16x64_i8 v[126:129], v[134:137], v[188:191], v[126:129]
	v_mfma_i32_16x16x64_i8 v[118:121], v[142:145], v[188:191], v[118:121]
	v_mfma_i32_16x16x64_i8 v[110:113], v[134:137], v[196:199], v[110:113]
	v_mfma_i32_16x16x64_i8 v[102:105], v[142:145], v[196:199], v[102:105]
	v_mfma_i32_16x16x64_i8 v[94:97], v[134:137], v[204:207], v[94:97]
	v_mfma_i32_16x16x64_i8 v[86:89], v[142:145], v[204:207], v[86:89]
	v_mfma_i32_16x16x64_i8 v[78:81], v[134:137], v[212:215], v[78:81]
	v_mfma_i32_16x16x64_i8 v[70:73], v[142:145], v[212:215], v[70:73]
	s_setprio 0
	s_setprio 1
	v_mfma_i32_16x16x64_i8 v[122:125], v[168:171], v[184:187], 0
	v_mfma_i32_16x16x64_i8 v[114:117], v[176:179], v[184:187], 0
	v_mfma_i32_16x16x64_i8 v[106:109], v[168:171], v[192:195], 0
	v_mfma_i32_16x16x64_i8 v[98:101], v[176:179], v[192:195], 0
	v_mfma_i32_16x16x64_i8 v[90:93], v[168:171], v[200:203], 0
	v_mfma_i32_16x16x64_i8 v[82:85], v[176:179], v[200:203], 0
	v_mfma_i32_16x16x64_i8 v[74:77], v[168:171], v[208:211], 0
	v_mfma_i32_16x16x64_i8 v[66:69], v[176:179], v[208:211], 0
	v_mfma_i32_16x16x64_i8 v[122:125], v[172:175], v[188:191], v[122:125]
	v_mfma_i32_16x16x64_i8 v[114:117], v[180:183], v[188:191], v[114:117]
	v_mfma_i32_16x16x64_i8 v[106:109], v[172:175], v[196:199], v[106:109]
	v_mfma_i32_16x16x64_i8 v[98:101], v[180:183], v[196:199], v[98:101]
	v_mfma_i32_16x16x64_i8 v[90:93], v[172:175], v[204:207], v[90:93]
	v_mfma_i32_16x16x64_i8 v[82:85], v[180:183], v[204:207], v[82:85]
	v_mfma_i32_16x16x64_i8 v[74:77], v[172:175], v[212:215], v[74:77]
	v_mfma_i32_16x16x64_i8 v[66:69], v[180:183], v[212:215], v[66:69]
	s_setprio 0
	s_barrier
	s_mov_b32 m0, s23
	s_add_u32 s98, s26, 0x80
	s_addc_u32 s99, s27, 0
	s_add_u32 s70, s26, 0x40000
	ds_read_b128 v[184:187], v167 offset:16384
	ds_read_b128 v[188:191], v167 offset:17408
	ds_read_b128 v[192:195], v167 offset:18432
	ds_read_b128 v[196:199], v167 offset:19456
	ds_read_b128 v[200:203], v167 offset:20480
	ds_read_b128 v[204:207], v167 offset:21504
	ds_read_b128 v[208:211], v167 offset:22528
	ds_read_b128 v[212:215], v167 offset:23552
	global_load_lds_dwordx4 v148, s[26:27]
	s_mov_b32 m0, s43
	s_addc_u32 s71, s27, 0
	global_load_lds_dwordx4 v152, s[26:27]
	s_mov_b32 m0, s44
	s_nop 0
	global_load_lds_dwordx4 v148, s[70:71]
	s_mov_b32 m0, s45
	s_nop 0
	global_load_lds_dwordx4 v152, s[70:71]
	s_add_u32 s100, s28, 0x80
	s_addc_u32 s101, s29, 0
	s_mov_b32 m0, s46
	s_nop 0
	global_load_lds_dwordx4 v146, s[28:29]
	s_mov_b32 m0, s47
	s_nop 0
	global_load_lds_dwordx4 v150, s[28:29]
	s_waitcnt vmcnt(8) lgkmcnt(0)
	s_barrier
; #define PG8_STAGE(bufoff, gbase, voff) do { _Pragma("unroll") for (int _i = 0; _i < 2; ++_i) \
;         __builtin_amdgcn_global_load_lds((const unsigned*)((const char*)(gbase) + (voff)[_i]), (PG8_LAS unsigned*)(lds + (bufoff) + ldsw + _i * 8192), 16, 0, 0); } while (0)
; #define PG8_LDA(dst, b, h) do { if constexpr (DT != 1) { _Pragma("unroll") for (int m = 0; m < 4; ++m) _Pragma("unroll") for (int k = 0; k < 2; ++k) dst[m][k] = *(const PG8_LAS bf16x8*)(lds + PG8_SA(b, h) + aoff + m * 2048 + k * 1024); } \
;         else { _Pragma("unroll") for (int m = 0; m < 4; ++m) dst##8[m] = ld32(lds + PG8_SA(b, h) + aoff + m * 2048); } } while (0)
; #define PG8_LDB(dst, b, h) do { if constexpr (DT != 1) { _Pragma("unroll") for (int n = 0; n < 2; ++n) _Pragma("unroll") for (int k = 0; k < 2; ++k) dst[n][k] = *(const PG8_LAS bf16x8*)(lds + PG8_SB(b, h) + boff + n * 2048 + k * 1024); } \
;         else { _Pragma("unroll") for (int n = 0; n < 2; ++n) dst##8[n] = ld32(lds + PG8_SB(b, h) + boff + n * 2048); } } while (0)
; #define PG8_WAIT_V(n) asm volatile("s_waitcnt vmcnt(" #n ")" ::: "memory")
; #define PG8_WAIT_L(n) asm volatile("s_waitcnt lgkmcnt(" #n ")" ::: "memory")
; #define PG8_BAR __builtin_amdgcn_s_barrier()
; #define PG8_SCHED __builtin_amdgcn_sched_barrier(0)
;     ...
;             PG8_LDA(At, 0, 1); PG8_STAGE(PG8_SB(0, 0), b2, voffB); PG8_STAGE(PG8_SB(0, 1), b2 + hstepB, voffB); PG8_STAGE(PG8_SA(0, 0), a2, voffA);
;             PG8_WAIT_V(8); PG8_WAIT_L(0); PG8_BAR; PG8_MMA(1, 0, At, B0); PG8_MMA(1, 1, At, B1); PG8_BAR; PG8_SCHED;
;             PG8_LDB(B0, 1, 0); PG8_LDB(B1, 1, 1); PG8_SCHED; PG8_LDA(At, 1, 0); PG8_STAGE(PG8_SA(0, 1), a2 + hstepA, voffA);
;             PG8_WAIT_V(8); PG8_WAIT_L(0); PG8_BAR; PG8_MMA(0, 0, At, B0); PG8_MMA(0, 1, At, B1); PG8_BAR; PG8_SCHED;
	s_setprio 1
	v_mfma_i32_16x16x64_i8 v[62:65], v[130:133], v[184:187], 0
	v_mfma_i32_16x16x64_i8 v[54:57], v[138:141], v[184:187], 0
	v_mfma_i32_16x16x64_i8 v[46:49], v[130:133], v[192:195], 0
	v_mfma_i32_16x16x64_i8 v[38:41], v[138:141], v[192:195], 0
	v_mfma_i32_16x16x64_i8 v[30:33], v[130:133], v[200:203], 0
	v_mfma_i32_16x16x64_i8 v[22:25], v[138:141], v[200:203], 0
	v_mfma_i32_16x16x64_i8 v[14:17], v[130:133], v[208:211], 0
	v_mfma_i32_16x16x64_i8 v[6:9], v[138:141], v[208:211], 0
	v_mfma_i32_16x16x64_i8 v[62:65], v[134:137], v[188:191], v[62:65]
	v_mfma_i32_16x16x64_i8 v[54:57], v[142:145], v[188:191], v[54:57]
	v_mfma_i32_16x16x64_i8 v[46:49], v[134:137], v[196:199], v[46:49]
	v_mfma_i32_16x16x64_i8 v[38:41], v[142:145], v[196:199], v[38:41]
	v_mfma_i32_16x16x64_i8 v[30:33], v[134:137], v[204:207], v[30:33]
	v_mfma_i32_16x16x64_i8 v[22:25], v[142:145], v[204:207], v[22:25]
	v_mfma_i32_16x16x64_i8 v[14:17], v[134:137], v[212:215], v[14:17]
	v_mfma_i32_16x16x64_i8 v[6:9], v[142:145], v[212:215], v[6:9]
	s_setprio 0
	s_setprio 1
	v_mfma_i32_16x16x64_i8 v[58:61], v[168:171], v[184:187], 0
	v_mfma_i32_16x16x64_i8 v[50:53], v[176:179], v[184:187], 0
	v_mfma_i32_16x16x64_i8 v[42:45], v[168:171], v[192:195], 0
	v_mfma_i32_16x16x64_i8 v[34:37], v[176:179], v[192:195], 0
	v_mfma_i32_16x16x64_i8 v[26:29], v[168:171], v[200:203], 0
	v_mfma_i32_16x16x64_i8 v[18:21], v[176:179], v[200:203], 0
	v_mfma_i32_16x16x64_i8 v[10:13], v[168:171], v[208:211], 0
	v_mfma_i32_16x16x64_i8 v[2:5], v[176:179], v[208:211], 0
	v_mfma_i32_16x16x64_i8 v[58:61], v[172:175], v[188:191], v[58:61]
	v_mfma_i32_16x16x64_i8 v[50:53], v[180:183], v[188:191], v[50:53]
	v_mfma_i32_16x16x64_i8 v[42:45], v[172:175], v[196:199], v[42:45]
	v_mfma_i32_16x16x64_i8 v[34:37], v[180:183], v[196:199], v[34:37]
	v_mfma_i32_16x16x64_i8 v[26:29], v[172:175], v[204:207], v[26:29]
	v_mfma_i32_16x16x64_i8 v[18:21], v[180:183], v[204:207], v[18:21]
	v_mfma_i32_16x16x64_i8 v[10:13], v[172:175], v[212:215], v[10:13]
	v_mfma_i32_16x16x64_i8 v[2:5], v[180:183], v[212:215], v[2:5]
	s_setprio 0
	s_barrier
	v_add_u32_e32 v142, s51, v164
	v_add_u32_e32 v180, s52, v164
	ds_read_b128 v[130:133], v142
	ds_read_b128 v[134:137], v142 offset:1024
	ds_read_b128 v[138:141], v142 offset:2048
	ds_read_b128 v[142:145], v142 offset:3072
	ds_read_b128 v[168:171], v180
	ds_read_b128 v[172:175], v180 offset:1024
	ds_read_b128 v[176:179], v180 offset:2048
	ds_read_b128 v[180:183], v180 offset:3072
	s_add_u32 s28, s28, 0x40000
	s_addc_u32 s29, s29, 0
	s_mov_b32 m0, s48
	ds_read_b128 v[184:187], v167 offset:32768
	ds_read_b128 v[188:191], v167 offset:33792
	ds_read_b128 v[192:195], v167 offset:34816
	ds_read_b128 v[196:199], v167 offset:35840
	ds_read_b128 v[200:203], v167 offset:36864
	ds_read_b128 v[204:207], v167 offset:37888
	ds_read_b128 v[208:211], v167 offset:38912
	ds_read_b128 v[212:215], v167 offset:39936
	global_load_lds_dwordx4 v146, s[28:29]
	s_mov_b32 m0, s49
	s_nop 0
	global_load_lds_dwordx4 v150, s[28:29]
	s_waitcnt vmcnt(8) lgkmcnt(0)
	s_barrier
	s_setprio 1
	v_mfma_i32_16x16x64_i8 v[126:129], v[130:133], v[184:187], v[126:129]
	v_mfma_i32_16x16x64_i8 v[118:121], v[138:141], v[184:187], v[118:121]
	v_mfma_i32_16x16x64_i8 v[110:113], v[130:133], v[192:195], v[110:113]
	v_mfma_i32_16x16x64_i8 v[102:105], v[138:141], v[192:195], v[102:105]
	v_mfma_i32_16x16x64_i8 v[94:97], v[130:133], v[200:203], v[94:97]
	v_mfma_i32_16x16x64_i8 v[86:89], v[138:141], v[200:203], v[86:89]
	v_mfma_i32_16x16x64_i8 v[78:81], v[130:133], v[208:211], v[78:81]
	v_mfma_i32_16x16x64_i8 v[70:73], v[138:141], v[208:211], v[70:73]
	v_mfma_i32_16x16x64_i8 v[126:129], v[134:137], v[188:191], v[126:129]
	v_mfma_i32_16x16x64_i8 v[118:121], v[142:145], v[188:191], v[118:121]
	v_mfma_i32_16x16x64_i8 v[110:113], v[134:137], v[196:199], v[110:113]
	v_mfma_i32_16x16x64_i8 v[102:105], v[142:145], v[196:199], v[102:105]
	v_mfma_i32_16x16x64_i8 v[94:97], v[134:137], v[204:207], v[94:97]
	v_mfma_i32_16x16x64_i8 v[86:89], v[142:145], v[204:207], v[86:89]
	v_mfma_i32_16x16x64_i8 v[78:81], v[134:137], v[212:215], v[78:81]
	v_mfma_i32_16x16x64_i8 v[70:73], v[142:145], v[212:215], v[70:73]
	s_setprio 0
	s_setprio 1
	v_mfma_i32_16x16x64_i8 v[122:125], v[168:171], v[184:187], v[122:125]
	v_mfma_i32_16x16x64_i8 v[114:117], v[176:179], v[184:187], v[114:117]
	v_mfma_i32_16x16x64_i8 v[106:109], v[168:171], v[192:195], v[106:109]
	v_mfma_i32_16x16x64_i8 v[98:101], v[176:179], v[192:195], v[98:101]
	v_mfma_i32_16x16x64_i8 v[90:93], v[168:171], v[200:203], v[90:93]
	v_mfma_i32_16x16x64_i8 v[82:85], v[176:179], v[200:203], v[82:85]
	v_mfma_i32_16x16x64_i8 v[74:77], v[168:171], v[208:211], v[74:77]
	v_mfma_i32_16x16x64_i8 v[66:69], v[176:179], v[208:211], v[66:69]
	v_mfma_i32_16x16x64_i8 v[122:125], v[172:175], v[188:191], v[122:125]
	v_mfma_i32_16x16x64_i8 v[114:117], v[180:183], v[188:191], v[114:117]
	v_mfma_i32_16x16x64_i8 v[106:109], v[172:175], v[196:199], v[106:109]
	v_mfma_i32_16x16x64_i8 v[98:101], v[180:183], v[196:199], v[98:101]
	v_mfma_i32_16x16x64_i8 v[90:93], v[172:175], v[204:207], v[90:93]
	v_mfma_i32_16x16x64_i8 v[82:85], v[180:183], v[204:207], v[82:85]
	v_mfma_i32_16x16x64_i8 v[74:77], v[172:175], v[212:215], v[74:77]
	v_mfma_i32_16x16x64_i8 v[66:69], v[180:183], v[212:215], v[66:69]
	s_setprio 0
	s_barrier
; #define PG8_STAGE(bufoff, gbase, voff) do { _Pragma("unroll") for (int _i = 0; _i < 2; ++_i) \
;         __builtin_amdgcn_global_load_lds((const unsigned*)((const char*)(gbase) + (voff)[_i]), (PG8_LAS unsigned*)(lds + (bufoff) + ldsw + _i * 8192), 16, 0, 0); } while (0)
; #define PG8_LDA(dst, b, h) do { if constexpr (DT != 1) { _Pragma("unroll") for (int m = 0; m < 4; ++m) _Pragma("unroll") for (int k = 0; k < 2; ++k) dst[m][k] = *(const PG8_LAS bf16x8*)(lds + PG8_SA(b, h) + aoff + m * 2048 + k * 1024); } \
;         else { _Pragma("unroll") for (int m = 0; m < 4; ++m) dst##8[m] = ld32(lds + PG8_SA(b, h) + aoff + m * 2048); } } while (0)
; #define PG8_WAIT_V(n) asm volatile("s_waitcnt vmcnt(" #n ")" ::: "memory")
; #define PG8_WAIT_L(n) asm volatile("s_waitcnt lgkmcnt(" #n ")" ::: "memory")
; #define PG8_BAR __builtin_amdgcn_s_barrier()
; #define PG8_SCHED __builtin_amdgcn_sched_barrier(0)
;     ...
;         for (int t = 0; t < nt; t += 2) {
;     ...
;             PG8_LDA(At, 1, 1); PG8_STAGE(PG8_SB(1, 0), b3, voffB); PG8_STAGE(PG8_SB(1, 1), b3 + hstepB, voffB); PG8_STAGE(PG8_SA(1, 0), a3, voffA);
;             PG8_WAIT_V(8); PG8_WAIT_L(0); PG8_BAR; PG8_MMA(1, 0, At, B0); PG8_MMA(1, 1, At, B1); PG8_BAR; PG8_SCHED;
	s_mov_b32 m0, s55
	s_add_u32 s26, s26, 0x40080
	ds_read_b128 v[184:187], v167 offset:49152
	ds_read_b128 v[188:191], v167 offset:50176
	ds_read_b128 v[192:195], v167 offset:51200
	ds_read_b128 v[196:199], v167 offset:52224
	ds_read_b128 v[200:203], v167 offset:53248
	ds_read_b128 v[204:207], v167 offset:54272
	ds_read_b128 v[208:211], v167 offset:55296
	ds_read_b128 v[212:215], v167 offset:56320
	global_load_lds_dwordx4 v148, s[98:99]
	s_mov_b32 m0, s56
	s_addc_u32 s27, s27, 0
	global_load_lds_dwordx4 v152, s[98:99]
	s_mov_b32 m0, s59
	s_nop 0
	global_load_lds_dwordx4 v148, s[26:27]
	s_mov_b32 m0, s60
	s_nop 0
	global_load_lds_dwordx4 v152, s[26:27]
	s_mov_b32 m0, s57
	s_nop 0
	global_load_lds_dwordx4 v146, s[100:101]
	s_mov_b32 m0, s58
	s_nop 0
	global_load_lds_dwordx4 v150, s[100:101]
	s_waitcnt vmcnt(8) lgkmcnt(0)
	s_barrier
	s_setprio 1
	v_mfma_i32_16x16x64_i8 v[62:65], v[130:133], v[184:187], v[62:65]
	v_mfma_i32_16x16x64_i8 v[54:57], v[138:141], v[184:187], v[54:57]
	v_mfma_i32_16x16x64_i8 v[46:49], v[130:133], v[192:195], v[46:49]
	v_mfma_i32_16x16x64_i8 v[38:41], v[138:141], v[192:195], v[38:41]
	v_mfma_i32_16x16x64_i8 v[30:33], v[130:133], v[200:203], v[30:33]
	v_mfma_i32_16x16x64_i8 v[22:25], v[138:141], v[200:203], v[22:25]
	v_mfma_i32_16x16x64_i8 v[14:17], v[130:133], v[208:211], v[14:17]
	v_mfma_i32_16x16x64_i8 v[6:9], v[138:141], v[208:211], v[6:9]
	v_mfma_i32_16x16x64_i8 v[62:65], v[134:137], v[188:191], v[62:65]
	v_mfma_i32_16x16x64_i8 v[54:57], v[142:145], v[188:191], v[54:57]
	v_mfma_i32_16x16x64_i8 v[46:49], v[134:137], v[196:199], v[46:49]
	v_mfma_i32_16x16x64_i8 v[38:41], v[142:145], v[196:199], v[38:41]
	v_mfma_i32_16x16x64_i8 v[30:33], v[134:137], v[204:207], v[30:33]
	v_mfma_i32_16x16x64_i8 v[22:25], v[142:145], v[204:207], v[22:25]
	v_mfma_i32_16x16x64_i8 v[14:17], v[134:137], v[212:215], v[14:17]
	v_mfma_i32_16x16x64_i8 v[6:9], v[142:145], v[212:215], v[6:9]
	s_setprio 0
	s_setprio 1
	v_mfma_i32_16x16x64_i8 v[58:61], v[168:171], v[184:187], v[58:61]
	v_mfma_i32_16x16x64_i8 v[50:53], v[176:179], v[184:187], v[50:53]
	v_mfma_i32_16x16x64_i8 v[42:45], v[168:171], v[192:195], v[42:45]
	v_mfma_i32_16x16x64_i8 v[34:37], v[176:179], v[192:195], v[34:37]
	v_mfma_i32_16x16x64_i8 v[26:29], v[168:171], v[200:203], v[26:29]
	v_mfma_i32_16x16x64_i8 v[18:21], v[176:179], v[200:203], v[18:21]
	v_mfma_i32_16x16x64_i8 v[10:13], v[168:171], v[208:211], v[10:13]
	v_mfma_i32_16x16x64_i8 v[2:5], v[176:179], v[208:211], v[2:5]
	v_mfma_i32_16x16x64_i8 v[58:61], v[172:175], v[188:191], v[58:61]
	v_mfma_i32_16x16x64_i8 v[50:53], v[180:183], v[188:191], v[50:53]
	v_mfma_i32_16x16x64_i8 v[42:45], v[172:175], v[196:199], v[42:45]
	v_mfma_i32_16x16x64_i8 v[34:37], v[180:183], v[196:199], v[34:37]
	v_mfma_i32_16x16x64_i8 v[26:29], v[172:175], v[204:207], v[26:29]
	v_mfma_i32_16x16x64_i8 v[18:21], v[180:183], v[204:207], v[18:21]
	v_mfma_i32_16x16x64_i8 v[10:13], v[172:175], v[212:215], v[10:13]
	v_mfma_i32_16x16x64_i8 v[2:5], v[180:183], v[212:215], v[2:5]
	s_setprio 0
	s_barrier
	s_add_u32 s66, s66, 0x100
	s_addc_u32 s67, s67, 0
	s_add_u32 s24, s24, 0x100
	s_addc_u32 s25, s25, 0
	s_cmp_ge_i32 s68, s54
	s_mov_b32 s26, s68
	s_cbranch_scc0 .LBB0_227
	s_branch .LBB0_228

; #define PG8_STAGE(bufoff, gbase, voff) do { _Pragma("unroll") for (int _i = 0; _i < 2; ++_i) \
;         __builtin_amdgcn_global_load_lds((const unsigned*)((const char*)(gbase) + (voff)[_i]), (PG8_LAS unsigned*)(lds + (bufoff) + ldsw + _i * 8192), 16, 0, 0); } while (0)
; #define PG8_LDA(dst, b, h) do { if constexpr (DT != 1) { _Pragma("unroll") for (int m = 0; m < 4; ++m) _Pragma("unroll") for (int k = 0; k < 2; ++k) dst[m][k] = *(const PG8_LAS bf16x8*)(lds + PG8_SA(b, h) + aoff + m * 2048 + k * 1024); } \
;         else { _Pragma("unroll") for (int m = 0; m < 4; ++m) dst##8[m] = ld32(lds + PG8_SA(b, h) + aoff + m * 2048); } } while (0)
; #define PG8_LDB(dst, b, h) do { if constexpr (DT != 1) { _Pragma("unroll") for (int n = 0; n < 2; ++n) _Pragma("unroll") for (int k = 0; k < 2; ++k) dst[n][k] = *(const PG8_LAS bf16x8*)(lds + PG8_SB(b, h) + boff + n * 2048 + k * 1024); } \
;         else { _Pragma("unroll") for (int n = 0; n < 2; ++n) dst##8[n] = ld32(lds + PG8_SB(b, h) + boff + n * 2048); } } while (0)
; #define PG8_WAIT_V(n) asm volatile("s_waitcnt vmcnt(" #n ")" ::: "memory")
; #define PG8_WAIT_L(n) asm volatile("s_waitcnt lgkmcnt(" #n ")" ::: "memory")
; #define PG8_BAR __builtin_amdgcn_s_barrier()
;     ...
;         const char* nA = has_next ? (const char*)g.A + (size_t)nxt.pm * tstepA : cA; const char* nB = has_next ? (const char*)g.Bt + (size_t)nxt.pn * tstepB : cB;
;         for (int t = 0; t < nt; t += 2) {
;             const bool last = (t == nt - 2);
;             const char* a1 = cA + (size_t)(t + 1) * kstep;
;             const char* a2 = last ? nA : cA + (size_t)(t + 2) * kstep; const char* b2 = last ? nB : cB + (size_t)(t + 2) * kstep;
;             const char* a3 = a2 + kstep; const char* b3 = b2 + kstep;
;             if (last && has_next) S.a_ready(nxt);
;             if constexpr (SP2) {
;             PG8_LDB(B0, 0, 0); PG8_LDB(B1, 0, 1); PG8_SCHED; PG8_LDA(At, 0, 0); PG8_STAGE(PG8_SA(1, 1), a1 + hstepA, voffA);
;             PG8_WAIT_V(8); PG8_WAIT_L(0); PG8_BAR; PG8_MMA(0, 0, At, B0); PG8_MMA(0, 1, At, B1); PG8_BAR; PG8_SCHED;
;             PG8_LDA(At, 0, 1); PG8_STAGE(PG8_SB(0, 0), b2, voffB); PG8_STAGE(PG8_SB(0, 1), b2 + hstepB, voffB); PG8_STAGE(PG8_SA(0, 0), a2, voffA);
;             PG8_WAIT_V(8); PG8_WAIT_L(0); PG8_BAR; PG8_MMA(1, 0, At, B0); PG8_MMA(1, 1, At, B1); PG8_BAR; PG8_SCHED;
.Lzt_1:
	s_cbranch_vccnz .LBB0_305
	s_add_u32 s67, s30, 0x100
	s_addc_u32 s68, s31, 0
	s_mov_b32 s34, 0
	ds_read_b128 v[146:149], v159
	ds_read_b128 v[150:153], v159 offset:1024
	ds_read_b128 v[154:157], v159 offset:2048
	ds_read_b128 v[164:167], v159 offset:3072
	ds_read_b128 v[168:171], v160
	ds_read_b128 v[172:175], v160 offset:1024
	ds_read_b128 v[176:179], v160 offset:2048
	ds_read_b128 v[180:183], v160 offset:3072
	s_add_i32 s69, s34, 2
	s_add_u32 s30, s28, 0x100
	s_addc_u32 s31, s29, 0
	s_cmp_eq_u32 s60, s34
	s_cselect_b32 s34, s26, s67
	s_cselect_b32 s37, s3, s31
	s_cselect_b32 s36, s2, s30
	s_cselect_b32 s35, s27, s68
	v_lshl_add_u64 v[216:217], s[28:29], 0, v[140:141]
	s_add_i32 m0, s48, 0xc000
	ds_read_b128 v[184:187], v161
	ds_read_b128 v[188:191], v161 offset:1024
	ds_read_b128 v[192:195], v161 offset:2048
	ds_read_b128 v[196:199], v161 offset:3072
	ds_read_b128 v[200:203], v161 offset:4096
	ds_read_b128 v[204:207], v161 offset:5120
	ds_read_b128 v[208:211], v161 offset:6144
	ds_read_b128 v[212:215], v161 offset:7168
	global_load_lds_dwordx4 v[216:217], off
	v_lshl_add_u64 v[216:217], s[28:29], 0, v[138:139]
	s_add_i32 m0, s48, 0xe000
	s_nop 0
	global_load_lds_dwordx4 v[216:217], off
	s_waitcnt vmcnt(8) lgkmcnt(0)
	s_barrier
	s_setprio 1
	v_mfma_f32_16x16x32_bf16 v[126:129], v[146:149], v[184:187], 0
	v_mfma_f32_16x16x32_bf16 v[122:125], v[154:157], v[184:187], 0
	v_mfma_f32_16x16x32_bf16 v[118:121], v[146:149], v[192:195], 0
	v_mfma_f32_16x16x32_bf16 v[114:117], v[154:157], v[192:195], 0
	v_mfma_f32_16x16x32_bf16 v[106:109], v[146:149], v[200:203], 0
	v_mfma_f32_16x16x32_bf16 v[98:101], v[154:157], v[200:203], 0
	v_mfma_f32_16x16x32_bf16 v[90:93], v[146:149], v[208:211], 0
	v_mfma_f32_16x16x32_bf16 v[82:85], v[154:157], v[208:211], 0
	v_mfma_f32_16x16x32_bf16 v[126:129], v[150:153], v[188:191], v[126:129]
	v_mfma_f32_16x16x32_bf16 v[122:125], v[164:167], v[188:191], v[122:125]
	v_mfma_f32_16x16x32_bf16 v[118:121], v[150:153], v[196:199], v[118:121]
	v_mfma_f32_16x16x32_bf16 v[114:117], v[164:167], v[196:199], v[114:117]
	v_mfma_f32_16x16x32_bf16 v[106:109], v[150:153], v[204:207], v[106:109]
	v_mfma_f32_16x16x32_bf16 v[98:101], v[164:167], v[204:207], v[98:101]
	v_mfma_f32_16x16x32_bf16 v[90:93], v[150:153], v[212:215], v[90:93]
	v_mfma_f32_16x16x32_bf16 v[82:85], v[164:167], v[212:215], v[82:85]
	s_setprio 0
	s_setprio 1
	v_mfma_f32_16x16x32_bf16 v[110:113], v[168:171], v[184:187], 0
	v_mfma_f32_16x16x32_bf16 v[102:105], v[176:179], v[184:187], 0
	v_mfma_f32_16x16x32_bf16 v[94:97], v[168:171], v[192:195], 0
	v_mfma_f32_16x16x32_bf16 v[86:89], v[176:179], v[192:195], 0
	v_mfma_f32_16x16x32_bf16 v[78:81], v[168:171], v[200:203], 0
	v_mfma_f32_16x16x32_bf16 v[74:77], v[176:179], v[200:203], 0
	v_mfma_f32_16x16x32_bf16 v[70:73], v[168:171], v[208:211], 0
	v_mfma_f32_16x16x32_bf16 v[66:69], v[176:179], v[208:211], 0
	v_mfma_f32_16x16x32_bf16 v[110:113], v[172:175], v[188:191], v[110:113]
	v_mfma_f32_16x16x32_bf16 v[102:105], v[180:183], v[188:191], v[102:105]
	v_mfma_f32_16x16x32_bf16 v[94:97], v[172:175], v[196:199], v[94:97]
	v_mfma_f32_16x16x32_bf16 v[86:89], v[180:183], v[196:199], v[86:89]
	v_mfma_f32_16x16x32_bf16 v[78:81], v[172:175], v[204:207], v[78:81]
	v_mfma_f32_16x16x32_bf16 v[74:77], v[180:183], v[204:207], v[74:77]
	v_mfma_f32_16x16x32_bf16 v[70:73], v[172:175], v[212:215], v[70:73]
	v_mfma_f32_16x16x32_bf16 v[66:69], v[180:183], v[212:215], v[66:69]
	s_setprio 0
	s_barrier
	s_mov_b32 m0, s44
	s_add_u32 s98, s34, 0x80
	s_addc_u32 s99, s35, 0
	s_add_u32 s28, s34, 0x160000
	ds_read_b128 v[184:187], v161 offset:16384
	ds_read_b128 v[188:191], v161 offset:17408
	ds_read_b128 v[192:195], v161 offset:18432
	ds_read_b128 v[196:199], v161 offset:19456
	ds_read_b128 v[200:203], v161 offset:20480
	ds_read_b128 v[204:207], v161 offset:21504
	ds_read_b128 v[208:211], v161 offset:22528
	ds_read_b128 v[212:215], v161 offset:23552
	global_load_lds_dwordx4 v132, s[34:35]
	s_mov_b32 m0, s45
	s_addc_u32 s29, s35, 0
	global_load_lds_dwordx4 v136, s[34:35]
	s_mov_b32 m0, s46
	s_nop 0
	global_load_lds_dwordx4 v132, s[28:29]
	s_mov_b32 m0, s47
	s_nop 0
	global_load_lds_dwordx4 v136, s[28:29]
	s_add_u32 s100, s36, 0x80
	s_addc_u32 s101, s37, 0
	s_mov_b32 m0, s48
	s_nop 0
	global_load_lds_dwordx4 v130, s[36:37]
	s_mov_b32 m0, s49
	s_nop 0
	global_load_lds_dwordx4 v134, s[36:37]
	s_waitcnt vmcnt(8) lgkmcnt(0)
	s_barrier
	s_setprio 1
	v_mfma_f32_16x16x32_bf16 v[62:65], v[146:149], v[184:187], 0
	v_mfma_f32_16x16x32_bf16 v[58:61], v[154:157], v[184:187], 0
	v_mfma_f32_16x16x32_bf16 v[54:57], v[146:149], v[192:195], 0
	v_mfma_f32_16x16x32_bf16 v[50:53], v[154:157], v[192:195], 0
	v_mfma_f32_16x16x32_bf16 v[42:45], v[146:149], v[200:203], 0
	v_mfma_f32_16x16x32_bf16 v[34:37], v[154:157], v[200:203], 0
	v_mfma_f32_16x16x32_bf16 v[26:29], v[146:149], v[208:211], 0
	v_mfma_f32_16x16x32_bf16 v[18:21], v[154:157], v[208:211], 0
	v_mfma_f32_16x16x32_bf16 v[62:65], v[150:153], v[188:191], v[62:65]
	v_mfma_f32_16x16x32_bf16 v[58:61], v[164:167], v[188:191], v[58:61]
	v_mfma_f32_16x16x32_bf16 v[54:57], v[150:153], v[196:199], v[54:57]
	v_mfma_f32_16x16x32_bf16 v[50:53], v[164:167], v[196:199], v[50:53]
	v_mfma_f32_16x16x32_bf16 v[42:45], v[150:153], v[204:207], v[42:45]
	v_mfma_f32_16x16x32_bf16 v[34:37], v[164:167], v[204:207], v[34:37]
	v_mfma_f32_16x16x32_bf16 v[26:29], v[150:153], v[212:215], v[26:29]
	v_mfma_f32_16x16x32_bf16 v[18:21], v[164:167], v[212:215], v[18:21]
	s_setprio 0
	s_setprio 1
	v_mfma_f32_16x16x32_bf16 v[46:49], v[168:171], v[184:187], 0
	v_mfma_f32_16x16x32_bf16 v[38:41], v[176:179], v[184:187], 0
	v_mfma_f32_16x16x32_bf16 v[30:33], v[168:171], v[192:195], 0
	v_mfma_f32_16x16x32_bf16 v[22:25], v[176:179], v[192:195], 0
	v_mfma_f32_16x16x32_bf16 v[14:17], v[168:171], v[200:203], 0
	v_mfma_f32_16x16x32_bf16 v[10:13], v[176:179], v[200:203], 0
	v_mfma_f32_16x16x32_bf16 v[6:9], v[168:171], v[208:211], 0
	v_mfma_f32_16x16x32_bf16 v[2:5], v[176:179], v[208:211], 0
	v_mfma_f32_16x16x32_bf16 v[46:49], v[172:175], v[188:191], v[46:49]
	v_mfma_f32_16x16x32_bf16 v[38:41], v[180:183], v[188:191], v[38:41]
	v_mfma_f32_16x16x32_bf16 v[30:33], v[172:175], v[196:199], v[30:33]
	v_mfma_f32_16x16x32_bf16 v[22:25], v[180:183], v[196:199], v[22:25]
	v_mfma_f32_16x16x32_bf16 v[14:17], v[172:175], v[204:207], v[14:17]
	v_mfma_f32_16x16x32_bf16 v[10:13], v[180:183], v[204:207], v[10:13]
	v_mfma_f32_16x16x32_bf16 v[6:9], v[172:175], v[212:215], v[6:9]
	v_mfma_f32_16x16x32_bf16 v[2:5], v[180:183], v[212:215], v[2:5]
	s_setprio 0
	s_barrier
; #define PG8_STAGE(bufoff, gbase, voff) do { _Pragma("unroll") for (int _i = 0; _i < 2; ++_i) \
;         __builtin_amdgcn_global_load_lds((const unsigned*)((const char*)(gbase) + (voff)[_i]), (PG8_LAS unsigned*)(lds + (bufoff) + ldsw + _i * 8192), 16, 0, 0); } while (0)
; #define PG8_LDA(dst, b, h) do { if constexpr (DT != 1) { _Pragma("unroll") for (int m = 0; m < 4; ++m) _Pragma("unroll") for (int k = 0; k < 2; ++k) dst[m][k] = *(const PG8_LAS bf16x8*)(lds + PG8_SA(b, h) + aoff + m * 2048 + k * 1024); } \
;         else { _Pragma("unroll") for (int m = 0; m < 4; ++m) dst##8[m] = ld32(lds + PG8_SA(b, h) + aoff + m * 2048); } } while (0)
; #define PG8_LDB(dst, b, h) do { if constexpr (DT != 1) { _Pragma("unroll") for (int n = 0; n < 2; ++n) _Pragma("unroll") for (int k = 0; k < 2; ++k) dst[n][k] = *(const PG8_LAS bf16x8*)(lds + PG8_SB(b, h) + boff + n * 2048 + k * 1024); } \
;         else { _Pragma("unroll") for (int n = 0; n < 2; ++n) dst##8[n] = ld32(lds + PG8_SB(b, h) + boff + n * 2048); } } while (0)
; #define PG8_WAIT_V(n) asm volatile("s_waitcnt vmcnt(" #n ")" ::: "memory")
; #define PG8_WAIT_L(n) asm volatile("s_waitcnt lgkmcnt(" #n ")" ::: "memory")
; #define PG8_BAR __builtin_amdgcn_s_barrier()
; #define PG8_SCHED __builtin_amdgcn_sched_barrier(0)
;     ...
;         for (int t = 0; t < nt; t += 2) {
;     ...
;             PG8_LDB(B0, 1, 0); PG8_LDB(B1, 1, 1); PG8_SCHED; PG8_LDA(At, 1, 0); PG8_STAGE(PG8_SA(0, 1), a2 + hstepA, voffA);
;             PG8_WAIT_V(8); PG8_WAIT_L(0); PG8_BAR; PG8_MMA(0, 0, At, B0); PG8_MMA(0, 1, At, B1); PG8_BAR; PG8_SCHED;
;             PG8_LDA(At, 1, 1); PG8_STAGE(PG8_SB(1, 0), b3, voffB); PG8_STAGE(PG8_SB(1, 1), b3 + hstepB, voffB); PG8_STAGE(PG8_SA(1, 0), a3, voffA);
;             PG8_WAIT_V(8); PG8_WAIT_L(0); PG8_BAR; PG8_MMA(1, 0, At, B0); PG8_MMA(1, 1, At, B1); PG8_BAR; PG8_SCHED;
	ds_read_b128 v[146:149], v162
	ds_read_b128 v[150:153], v162 offset:1024
	ds_read_b128 v[154:157], v162 offset:2048
	ds_read_b128 v[164:167], v162 offset:3072
	ds_read_b128 v[168:171], v163
	ds_read_b128 v[172:175], v163 offset:1024
	ds_read_b128 v[176:179], v163 offset:2048
	ds_read_b128 v[180:183], v163 offset:3072
	s_add_u32 s28, s36, 0x160000
	s_addc_u32 s29, s37, 0
	s_mov_b32 m0, s50
	ds_read_b128 v[184:187], v161 offset:32768
	ds_read_b128 v[188:191], v161 offset:33792
	ds_read_b128 v[192:195], v161 offset:34816
	ds_read_b128 v[196:199], v161 offset:35840
	ds_read_b128 v[200:203], v161 offset:36864
	ds_read_b128 v[204:207], v161 offset:37888
	ds_read_b128 v[208:211], v161 offset:38912
	ds_read_b128 v[212:215], v161 offset:39936
	global_load_lds_dwordx4 v130, s[28:29]
	s_mov_b32 m0, s51
	s_nop 0
	global_load_lds_dwordx4 v134, s[28:29]
	s_waitcnt vmcnt(8) lgkmcnt(0)
	s_barrier
	s_setprio 1
	v_mfma_f32_16x16x32_bf16 v[126:129], v[146:149], v[184:187], v[126:129]
	v_mfma_f32_16x16x32_bf16 v[122:125], v[154:157], v[184:187], v[122:125]
	v_mfma_f32_16x16x32_bf16 v[118:121], v[146:149], v[192:195], v[118:121]
	v_mfma_f32_16x16x32_bf16 v[114:117], v[154:157], v[192:195], v[114:117]
	v_mfma_f32_16x16x32_bf16 v[106:109], v[146:149], v[200:203], v[106:109]
	v_mfma_f32_16x16x32_bf16 v[98:101], v[154:157], v[200:203], v[98:101]
	v_mfma_f32_16x16x32_bf16 v[90:93], v[146:149], v[208:211], v[90:93]
	v_mfma_f32_16x16x32_bf16 v[82:85], v[154:157], v[208:211], v[82:85]
	v_mfma_f32_16x16x32_bf16 v[126:129], v[150:153], v[188:191], v[126:129]
	v_mfma_f32_16x16x32_bf16 v[122:125], v[164:167], v[188:191], v[122:125]
	v_mfma_f32_16x16x32_bf16 v[118:121], v[150:153], v[196:199], v[118:121]
	v_mfma_f32_16x16x32_bf16 v[114:117], v[164:167], v[196:199], v[114:117]
	v_mfma_f32_16x16x32_bf16 v[106:109], v[150:153], v[204:207], v[106:109]
	v_mfma_f32_16x16x32_bf16 v[98:101], v[164:167], v[204:207], v[98:101]
	v_mfma_f32_16x16x32_bf16 v[90:93], v[150:153], v[212:215], v[90:93]
	v_mfma_f32_16x16x32_bf16 v[82:85], v[164:167], v[212:215], v[82:85]
	s_setprio 0
	s_setprio 1
	v_mfma_f32_16x16x32_bf16 v[110:113], v[168:171], v[184:187], v[110:113]
	v_mfma_f32_16x16x32_bf16 v[102:105], v[176:179], v[184:187], v[102:105]
	v_mfma_f32_16x16x32_bf16 v[94:97], v[168:171], v[192:195], v[94:97]
	v_mfma_f32_16x16x32_bf16 v[86:89], v[176:179], v[192:195], v[86:89]
	v_mfma_f32_16x16x32_bf16 v[78:81], v[168:171], v[200:203], v[78:81]
	v_mfma_f32_16x16x32_bf16 v[74:77], v[176:179], v[200:203], v[74:77]
	v_mfma_f32_16x16x32_bf16 v[70:73], v[168:171], v[208:211], v[70:73]
	v_mfma_f32_16x16x32_bf16 v[66:69], v[176:179], v[208:211], v[66:69]
	v_mfma_f32_16x16x32_bf16 v[110:113], v[172:175], v[188:191], v[110:113]
	v_mfma_f32_16x16x32_bf16 v[102:105], v[180:183], v[188:191], v[102:105]
	v_mfma_f32_16x16x32_bf16 v[94:97], v[172:175], v[196:199], v[94:97]
	v_mfma_f32_16x16x32_bf16 v[86:89], v[180:183], v[196:199], v[86:89]
	v_mfma_f32_16x16x32_bf16 v[78:81], v[172:175], v[204:207], v[78:81]
	v_mfma_f32_16x16x32_bf16 v[74:77], v[180:183], v[204:207], v[74:77]
	v_mfma_f32_16x16x32_bf16 v[70:73], v[172:175], v[212:215], v[70:73]
	v_mfma_f32_16x16x32_bf16 v[66:69], v[180:183], v[212:215], v[66:69]
	s_setprio 0
	s_barrier
	s_mov_b32 m0, s54
	s_add_u32 s28, s34, 0x160080
	ds_read_b128 v[184:187], v161 offset:49152
	ds_read_b128 v[188:191], v161 offset:50176
	ds_read_b128 v[192:195], v161 offset:51200
	ds_read_b128 v[196:199], v161 offset:52224
	ds_read_b128 v[200:203], v161 offset:53248
	ds_read_b128 v[204:207], v161 offset:54272
	ds_read_b128 v[208:211], v161 offset:55296
	ds_read_b128 v[212:215], v161 offset:56320
	global_load_lds_dwordx4 v132, s[98:99]
	s_mov_b32 m0, s55
	s_addc_u32 s29, s35, 0
	global_load_lds_dwordx4 v136, s[98:99]
	s_mov_b32 m0, s58
	s_nop 0
	global_load_lds_dwordx4 v132, s[28:29]
	s_mov_b32 m0, s59
	s_nop 0
	global_load_lds_dwordx4 v136, s[28:29]
	s_mov_b32 m0, s56
	s_nop 0
	global_load_lds_dwordx4 v130, s[100:101]
	s_mov_b32 m0, s57
	s_nop 0
	global_load_lds_dwordx4 v134, s[100:101]
	s_waitcnt vmcnt(8) lgkmcnt(0)
	s_barrier
	s_setprio 1
	v_mfma_f32_16x16x32_bf16 v[62:65], v[146:149], v[184:187], v[62:65]
	v_mfma_f32_16x16x32_bf16 v[58:61], v[154:157], v[184:187], v[58:61]
	v_mfma_f32_16x16x32_bf16 v[54:57], v[146:149], v[192:195], v[54:57]
	v_mfma_f32_16x16x32_bf16 v[50:53], v[154:157], v[192:195], v[50:53]
	v_mfma_f32_16x16x32_bf16 v[42:45], v[146:149], v[200:203], v[42:45]
	v_mfma_f32_16x16x32_bf16 v[34:37], v[154:157], v[200:203], v[34:37]
	v_mfma_f32_16x16x32_bf16 v[26:29], v[146:149], v[208:211], v[26:29]
	v_mfma_f32_16x16x32_bf16 v[18:21], v[154:157], v[208:211], v[18:21]
	v_mfma_f32_16x16x32_bf16 v[62:65], v[150:153], v[188:191], v[62:65]
	v_mfma_f32_16x16x32_bf16 v[58:61], v[164:167], v[188:191], v[58:61]
	v_mfma_f32_16x16x32_bf16 v[54:57], v[150:153], v[196:199], v[54:57]
	v_mfma_f32_16x16x32_bf16 v[50:53], v[164:167], v[196:199], v[50:53]
	v_mfma_f32_16x16x32_bf16 v[42:45], v[150:153], v[204:207], v[42:45]
	v_mfma_f32_16x16x32_bf16 v[34:37], v[164:167], v[204:207], v[34:37]
	v_mfma_f32_16x16x32_bf16 v[26:29], v[150:153], v[212:215], v[26:29]
	v_mfma_f32_16x16x32_bf16 v[18:21], v[164:167], v[212:215], v[18:21]
	s_setprio 0
	s_setprio 1
	v_mfma_f32_16x16x32_bf16 v[46:49], v[168:171], v[184:187], v[46:49]
	v_mfma_f32_16x16x32_bf16 v[38:41], v[176:179], v[184:187], v[38:41]
	v_mfma_f32_16x16x32_bf16 v[30:33], v[168:171], v[192:195], v[30:33]
	v_mfma_f32_16x16x32_bf16 v[22:25], v[176:179], v[192:195], v[22:25]
	v_mfma_f32_16x16x32_bf16 v[14:17], v[168:171], v[200:203], v[14:17]
	v_mfma_f32_16x16x32_bf16 v[10:13], v[176:179], v[200:203], v[10:13]
	v_mfma_f32_16x16x32_bf16 v[6:9], v[168:171], v[208:211], v[6:9]
	v_mfma_f32_16x16x32_bf16 v[2:5], v[176:179], v[208:211], v[2:5]
	v_mfma_f32_16x16x32_bf16 v[46:49], v[172:175], v[188:191], v[46:49]
	v_mfma_f32_16x16x32_bf16 v[38:41], v[180:183], v[188:191], v[38:41]
	v_mfma_f32_16x16x32_bf16 v[30:33], v[172:175], v[196:199], v[30:33]
	v_mfma_f32_16x16x32_bf16 v[22:25], v[180:183], v[196:199], v[22:25]
	v_mfma_f32_16x16x32_bf16 v[14:17], v[172:175], v[204:207], v[14:17]
	v_mfma_f32_16x16x32_bf16 v[10:13], v[180:183], v[204:207], v[10:13]
	v_mfma_f32_16x16x32_bf16 v[6:9], v[172:175], v[212:215], v[6:9]
	v_mfma_f32_16x16x32_bf16 v[2:5], v[180:183], v[212:215], v[2:5]
	s_setprio 0
	s_barrier
	s_add_u32 s67, s67, 0x100
	s_addc_u32 s68, s68, 0
	s_cmp_ge_i32 s69, s53
	s_mov_b64 s[28:29], s[30:31]
	s_mov_b32 s34, s69
	s_cbranch_scc0 .LBB0_303
	s_branch .Lpx_1

;     __device__ __forceinline__ void operator()(const f32x4 (&acc)[2][2][4][2], const Unit& u, int wr, int wc, int fr, int fq) const {
;     ...
;                 for (int m = 0; m < 4; ++m) { const size_t off = (size_t)(row0 + ai * HALF + m * 16) * ldc + col0;
; #pragma unroll
;                     for (int bj = 0; bj < 2; ++bj) { const h16x8_t w = wv[m][bj];
;                         const f32x4 b0 = (f32x4){(float)w[0], (float)w[1], (float)w[2], (float)w[3]}, b1 = (f32x4){(float)w[4], (float)w[5], (float)w[6], (float)w[7]};
;                         const f32x4 o0 = b0 + acc[ai][bj][m][0] * s, o1 = b1 + acc[ai][bj][m][1] * s;
.Lpx_1:
	v_pk_mul_f32 v[128:129], v[128:129], 0.5 op_sel_hi:[1,0]
	v_pk_mul_f32 v[126:127], v[126:127], 0.5 op_sel_hi:[1,0]
	v_pk_mul_f32 v[146:147], v[124:125], 0.5 op_sel_hi:[1,0]
	v_pk_mul_f32 v[148:149], v[122:123], 0.5 op_sel_hi:[1,0]
	v_pk_mul_f32 v[150:151], v[112:113], 0.5 op_sel_hi:[1,0]
	v_pk_mul_f32 v[152:153], v[110:111], 0.5 op_sel_hi:[1,0]
	v_pk_mul_f32 v[154:155], v[104:105], 0.5 op_sel_hi:[1,0]
	v_pk_mul_f32 v[156:157], v[102:103], 0.5 op_sel_hi:[1,0]
	v_pk_mul_f32 v[110:111], v[120:121], 0.5 op_sel_hi:[1,0]
	v_pk_mul_f32 v[112:113], v[118:119], 0.5 op_sel_hi:[1,0]
	v_pk_mul_f32 v[116:117], v[116:117], 0.5 op_sel_hi:[1,0]
	v_pk_mul_f32 v[114:115], v[114:115], 0.5 op_sel_hi:[1,0]
	v_pk_mul_f32 v[118:119], v[96:97], 0.5 op_sel_hi:[1,0]
	v_pk_mul_f32 v[120:121], v[94:95], 0.5 op_sel_hi:[1,0]
	v_pk_mul_f32 v[122:123], v[88:89], 0.5 op_sel_hi:[1,0]
	v_pk_mul_f32 v[124:125], v[86:87], 0.5 op_sel_hi:[1,0]
	v_pk_mul_f32 v[94:95], v[108:109], 0.5 op_sel_hi:[1,0]
	v_pk_mul_f32 v[96:97], v[106:107], 0.5 op_sel_hi:[1,0]
	v_pk_mul_f32 v[100:101], v[100:101], 0.5 op_sel_hi:[1,0]
	v_pk_mul_f32 v[98:99], v[98:99], 0.5 op_sel_hi:[1,0]
	v_pk_mul_f32 v[102:103], v[80:81], 0.5 op_sel_hi:[1,0]
	v_pk_mul_f32 v[104:105], v[78:79], 0.5 op_sel_hi:[1,0]
	v_pk_mul_f32 v[106:107], v[76:77], 0.5 op_sel_hi:[1,0]
	v_pk_mul_f32 v[108:109], v[74:75], 0.5 op_sel_hi:[1,0]
	v_pk_mul_f32 v[74:75], v[92:93], 0.5 op_sel_hi:[1,0]
	v_pk_mul_f32 v[76:77], v[90:91], 0.5 op_sel_hi:[1,0]
	v_pk_mul_f32 v[78:79], v[84:85], 0.5 op_sel_hi:[1,0]
	v_pk_mul_f32 v[80:81], v[82:83], 0.5 op_sel_hi:[1,0]
	v_pk_mul_f32 v[86:87], v[72:73], 0.5 op_sel_hi:[1,0]
	v_pk_mul_f32 v[88:89], v[70:71], 0.5 op_sel_hi:[1,0]
	v_pk_mul_f32 v[90:91], v[68:69], 0.5 op_sel_hi:[1,0]
	v_pk_mul_f32 v[92:93], v[66:67], 0.5 op_sel_hi:[1,0]
	v_pk_mul_f32 v[64:65], v[64:65], 0.5 op_sel_hi:[1,0]
	v_pk_mul_f32 v[62:63], v[62:63], 0.5 op_sel_hi:[1,0]
	v_pk_mul_f32 v[66:67], v[60:61], 0.5 op_sel_hi:[1,0]
	v_pk_mul_f32 v[68:69], v[58:59], 0.5 op_sel_hi:[1,0]
	v_pk_mul_f32 v[70:71], v[48:49], 0.5 op_sel_hi:[1,0]
	v_pk_mul_f32 v[72:73], v[46:47], 0.5 op_sel_hi:[1,0]
	v_pk_mul_f32 v[82:83], v[40:41], 0.5 op_sel_hi:[1,0]
	v_pk_mul_f32 v[84:85], v[38:39], 0.5 op_sel_hi:[1,0]
	v_pk_mul_f32 v[46:47], v[56:57], 0.5 op_sel_hi:[1,0]
	v_pk_mul_f32 v[48:49], v[54:55], 0.5 op_sel_hi:[1,0]
	v_pk_mul_f32 v[52:53], v[52:53], 0.5 op_sel_hi:[1,0]
	v_pk_mul_f32 v[50:51], v[50:51], 0.5 op_sel_hi:[1,0]
	v_pk_mul_f32 v[54:55], v[32:33], 0.5 op_sel_hi:[1,0]
	v_pk_mul_f32 v[56:57], v[30:31], 0.5 op_sel_hi:[1,0]
	v_pk_mul_f32 v[58:59], v[24:25], 0.5 op_sel_hi:[1,0]
	v_pk_mul_f32 v[60:61], v[22:23], 0.5 op_sel_hi:[1,0]
	v_pk_mul_f32 v[22:23], v[44:45], 0.5 op_sel_hi:[1,0]
	v_pk_mul_f32 v[24:25], v[42:43], 0.5 op_sel_hi:[1,0]
	v_pk_mul_f32 v[30:31], v[36:37], 0.5 op_sel_hi:[1,0]
	v_pk_mul_f32 v[32:33], v[34:35], 0.5 op_sel_hi:[1,0]
	v_pk_mul_f32 v[34:35], v[16:17], 0.5 op_sel_hi:[1,0]
	v_pk_mul_f32 v[36:37], v[14:15], 0.5 op_sel_hi:[1,0]
	v_pk_mul_f32 v[38:39], v[12:13], 0.5 op_sel_hi:[1,0]
	v_pk_mul_f32 v[40:41], v[10:11], 0.5 op_sel_hi:[1,0]
	v_pk_mul_f32 v[10:11], v[28:29], 0.5 op_sel_hi:[1,0]
	v_pk_mul_f32 v[12:13], v[26:27], 0.5 op_sel_hi:[1,0]
	v_pk_mul_f32 v[14:15], v[20:21], 0.5 op_sel_hi:[1,0]
	v_pk_mul_f32 v[16:17], v[18:19], 0.5 op_sel_hi:[1,0]
	v_pk_mul_f32 v[8:9], v[8:9], 0.5 op_sel_hi:[1,0]
	v_pk_mul_f32 v[6:7], v[6:7], 0.5 op_sel_hi:[1,0]
	v_pk_mul_f32 v[4:5], v[4:5], 0.5 op_sel_hi:[1,0]
	v_pk_mul_f32 v[2:3], v[2:3], 0.5 op_sel_hi:[1,0]

; #define PG8_STAGE(bufoff, gbase, voff) do { _Pragma("unroll") for (int _i = 0; _i < 2; ++_i) \
;         __builtin_amdgcn_global_load_lds((const unsigned*)((const char*)(gbase) + (voff)[_i]), (PG8_LAS unsigned*)(lds + (bufoff) + ldsw + _i * 8192), 16, 0, 0); } while (0)
; #define PG8_LDA(dst, b, h) do { if constexpr (DT != 1) { _Pragma("unroll") for (int m = 0; m < 4; ++m) _Pragma("unroll") for (int k = 0; k < 2; ++k) dst[m][k] = *(const PG8_LAS bf16x8*)(lds + PG8_SA(b, h) + aoff + m * 2048 + k * 1024); } \
;         else { _Pragma("unroll") for (int m = 0; m < 4; ++m) dst##8[m] = ld32(lds + PG8_SA(b, h) + aoff + m * 2048); } } while (0)
; #define PG8_LDB(dst, b, h) do { if constexpr (DT != 1) { _Pragma("unroll") for (int n = 0; n < 2; ++n) _Pragma("unroll") for (int k = 0; k < 2; ++k) dst[n][k] = *(const PG8_LAS bf16x8*)(lds + PG8_SB(b, h) + boff + n * 2048 + k * 1024); } \
;         else { _Pragma("unroll") for (int n = 0; n < 2; ++n) dst##8[n] = ld32(lds + PG8_SB(b, h) + boff + n * 2048); } } while (0)
; #define PG8_WAIT_V(n) asm volatile("s_waitcnt vmcnt(" #n ")" ::: "memory")
; #define PG8_WAIT_L(n) asm volatile("s_waitcnt lgkmcnt(" #n ")" ::: "memory")
; #define PG8_BAR __builtin_amdgcn_s_barrier()
;     ...
;         const char* nA = has_next ? (const char*)g.A + (size_t)nxt.pm * tstepA : cA; const char* nB = has_next ? (const char*)g.Bt + (size_t)nxt.pn * tstepB : cB;
;         for (int t = 0; t < nt; t += 2) {
;             const bool last = (t == nt - 2);
;             const char* a1 = cA + (size_t)(t + 1) * kstep;
;             const char* a2 = last ? nA : cA + (size_t)(t + 2) * kstep; const char* b2 = last ? nB : cB + (size_t)(t + 2) * kstep;
;             const char* a3 = a2 + kstep; const char* b3 = b2 + kstep;
;             if (last && has_next) S.a_ready(nxt);
;             if constexpr (SP2) {
;             PG8_LDB(B0, 0, 0); PG8_LDB(B1, 0, 1); PG8_SCHED; PG8_LDA(At, 0, 0); PG8_STAGE(PG8_SA(1, 1), a1 + hstepA, voffA);
;             PG8_WAIT_V(8); PG8_WAIT_L(0); PG8_BAR; PG8_MMA(0, 0, At, B0); PG8_MMA(0, 1, At, B1); PG8_BAR; PG8_SCHED;
;             PG8_LDA(At, 0, 1); PG8_STAGE(PG8_SB(0, 0), b2, voffB); PG8_STAGE(PG8_SB(0, 1), b2 + hstepB, voffB); PG8_STAGE(PG8_SA(0, 0), a2, voffA);
;             PG8_WAIT_V(8); PG8_WAIT_L(0); PG8_BAR; PG8_MMA(1, 0, At, B0); PG8_MMA(1, 1, At, B1); PG8_BAR; PG8_SCHED;
.Lzs_2:
	s_cbranch_vccnz .LBB0_419
	s_and_b64 s[30:31], s[0:1], exec
	s_cselect_b32 s19, s23, s29
	s_cselect_b32 s21, s22, s28
	s_cselect_b32 s61, s25, s27
	s_cselect_b32 s62, s24, s26
	s_add_u32 s63, s26, 0x100
	s_addc_u32 s64, s27, 0
	s_add_u32 s26, s28, 0x80080
	s_addc_u32 s27, s29, 0
	s_mov_b32 s28, 0
	ds_read_b128 v[156:159], v150
	ds_read_b128 v[160:163], v150 offset:1024
	ds_read_b128 v[164:167], v150 offset:2048
	ds_read_b128 v[168:171], v150 offset:3072
	ds_read_b128 v[172:175], v151
	ds_read_b128 v[176:179], v151 offset:1024
	ds_read_b128 v[180:183], v151 offset:2048
	ds_read_b128 v[184:187], v151 offset:3072
	s_add_i32 s65, s28, 2
	s_add_u32 s29, s26, 0xfff80080
	s_addc_u32 s30, s27, -1
	s_cmp_eq_u32 s59, s28
	s_cselect_b32 s28, s62, s63
	s_cselect_b32 s31, s19, s30
	s_cselect_b32 s30, s21, s29
	s_cselect_b32 s29, s61, s64
	s_add_i32 m0, s45, 0xc000
	ds_read_b128 v[188:191], v152
	ds_read_b128 v[192:195], v152 offset:1024
	ds_read_b128 v[196:199], v152 offset:2048
	ds_read_b128 v[200:203], v152 offset:3072
	ds_read_b128 v[204:207], v152 offset:4096
	ds_read_b128 v[208:211], v152 offset:5120
	ds_read_b128 v[212:215], v152 offset:6144
	ds_read_b128 v[216:219], v152 offset:7168
	global_load_lds_dwordx4 v144, s[26:27]
	s_add_i32 m0, s45, 0xe000
	s_nop 0
	global_load_lds_dwordx4 v142, s[26:27]
	s_waitcnt vmcnt(8) lgkmcnt(0)
	s_barrier
	s_setprio 1
	v_mfma_f32_16x16x32_bf16 v[122:125], v[156:159], v[188:191], 0
	v_mfma_f32_16x16x32_bf16 v[126:129], v[164:167], v[188:191], 0
	v_mfma_f32_16x16x32_bf16 v[110:113], v[156:159], v[196:199], 0
	v_mfma_f32_16x16x32_bf16 v[106:109], v[164:167], v[196:199], 0
	v_mfma_f32_16x16x32_bf16 v[94:97], v[156:159], v[204:207], 0
	v_mfma_f32_16x16x32_bf16 v[90:93], v[164:167], v[204:207], 0
	v_mfma_f32_16x16x32_bf16 v[78:81], v[156:159], v[212:215], 0
	v_mfma_f32_16x16x32_bf16 v[74:77], v[164:167], v[212:215], 0
	v_mfma_f32_16x16x32_bf16 v[122:125], v[160:163], v[192:195], v[122:125]
	v_mfma_f32_16x16x32_bf16 v[126:129], v[168:171], v[192:195], v[126:129]
	v_mfma_f32_16x16x32_bf16 v[110:113], v[160:163], v[200:203], v[110:113]
	v_mfma_f32_16x16x32_bf16 v[106:109], v[168:171], v[200:203], v[106:109]
	v_mfma_f32_16x16x32_bf16 v[94:97], v[160:163], v[208:211], v[94:97]
	v_mfma_f32_16x16x32_bf16 v[90:93], v[168:171], v[208:211], v[90:93]
	v_mfma_f32_16x16x32_bf16 v[78:81], v[160:163], v[216:219], v[78:81]
	v_mfma_f32_16x16x32_bf16 v[74:77], v[168:171], v[216:219], v[74:77]
	s_setprio 0
	s_setprio 1
	v_mfma_f32_16x16x32_bf16 v[118:121], v[172:175], v[188:191], 0
	v_mfma_f32_16x16x32_bf16 v[114:117], v[180:183], v[188:191], 0
	v_mfma_f32_16x16x32_bf16 v[102:105], v[172:175], v[196:199], 0
	v_mfma_f32_16x16x32_bf16 v[98:101], v[180:183], v[196:199], 0
	v_mfma_f32_16x16x32_bf16 v[86:89], v[172:175], v[204:207], 0
	v_mfma_f32_16x16x32_bf16 v[82:85], v[180:183], v[204:207], 0
	v_mfma_f32_16x16x32_bf16 v[70:73], v[172:175], v[212:215], 0
	v_mfma_f32_16x16x32_bf16 v[66:69], v[180:183], v[212:215], 0
	v_mfma_f32_16x16x32_bf16 v[118:121], v[176:179], v[192:195], v[118:121]
	v_mfma_f32_16x16x32_bf16 v[114:117], v[184:187], v[192:195], v[114:117]
	v_mfma_f32_16x16x32_bf16 v[102:105], v[176:179], v[200:203], v[102:105]
	v_mfma_f32_16x16x32_bf16 v[98:101], v[184:187], v[200:203], v[98:101]
	v_mfma_f32_16x16x32_bf16 v[86:89], v[176:179], v[208:211], v[86:89]
	v_mfma_f32_16x16x32_bf16 v[82:85], v[184:187], v[208:211], v[82:85]
	v_mfma_f32_16x16x32_bf16 v[70:73], v[176:179], v[216:219], v[70:73]
	v_mfma_f32_16x16x32_bf16 v[66:69], v[184:187], v[216:219], v[66:69]
	s_setprio 0
	s_barrier
	s_mov_b32 m0, s41
	s_add_u32 s98, s28, 0x80
	s_addc_u32 s99, s29, 0
	s_add_u32 s66, s28, 0x80000
	ds_read_b128 v[188:191], v152 offset:16384
	ds_read_b128 v[192:195], v152 offset:17408
	ds_read_b128 v[196:199], v152 offset:18432
	ds_read_b128 v[200:203], v152 offset:19456
	ds_read_b128 v[204:207], v152 offset:20480
	ds_read_b128 v[208:211], v152 offset:21504
	ds_read_b128 v[212:215], v152 offset:22528
	ds_read_b128 v[216:219], v152 offset:23552
	global_load_lds_dwordx4 v132, s[28:29]
	s_mov_b32 m0, s42
	s_addc_u32 s67, s29, 0
	global_load_lds_dwordx4 v136, s[28:29]
	s_mov_b32 m0, s43
	s_nop 0
	global_load_lds_dwordx4 v132, s[66:67]
	s_mov_b32 m0, s44
	s_nop 0
	global_load_lds_dwordx4 v136, s[66:67]
	s_add_u32 s100, s30, 0x80
	s_addc_u32 s101, s31, 0
	s_mov_b32 m0, s45
	s_nop 0
	global_load_lds_dwordx4 v130, s[30:31]
	s_mov_b32 m0, s46
	s_nop 0
	global_load_lds_dwordx4 v134, s[30:31]
	s_waitcnt vmcnt(8) lgkmcnt(0)
	s_barrier
	s_setprio 1
	v_mfma_f32_16x16x32_bf16 v[62:65], v[156:159], v[188:191], 0
	v_mfma_f32_16x16x32_bf16 v[58:61], v[164:167], v[188:191], 0
	v_mfma_f32_16x16x32_bf16 v[46:49], v[156:159], v[196:199], 0
	v_mfma_f32_16x16x32_bf16 v[42:45], v[164:167], v[196:199], 0
	v_mfma_f32_16x16x32_bf16 v[30:33], v[156:159], v[204:207], 0
	v_mfma_f32_16x16x32_bf16 v[26:29], v[164:167], v[204:207], 0
	v_mfma_f32_16x16x32_bf16 v[14:17], v[156:159], v[212:215], 0
	v_mfma_f32_16x16x32_bf16 v[10:13], v[164:167], v[212:215], 0
	v_mfma_f32_16x16x32_bf16 v[62:65], v[160:163], v[192:195], v[62:65]
	v_mfma_f32_16x16x32_bf16 v[58:61], v[168:171], v[192:195], v[58:61]
	v_mfma_f32_16x16x32_bf16 v[46:49], v[160:163], v[200:203], v[46:49]
	v_mfma_f32_16x16x32_bf16 v[42:45], v[168:171], v[200:203], v[42:45]
	v_mfma_f32_16x16x32_bf16 v[30:33], v[160:163], v[208:211], v[30:33]
	v_mfma_f32_16x16x32_bf16 v[26:29], v[168:171], v[208:211], v[26:29]
	v_mfma_f32_16x16x32_bf16 v[14:17], v[160:163], v[216:219], v[14:17]
	v_mfma_f32_16x16x32_bf16 v[10:13], v[168:171], v[216:219], v[10:13]
	s_setprio 0
	s_setprio 1
	v_mfma_f32_16x16x32_bf16 v[54:57], v[172:175], v[188:191], 0
	v_mfma_f32_16x16x32_bf16 v[50:53], v[180:183], v[188:191], 0
	v_mfma_f32_16x16x32_bf16 v[38:41], v[172:175], v[196:199], 0
	v_mfma_f32_16x16x32_bf16 v[34:37], v[180:183], v[196:199], 0
	v_mfma_f32_16x16x32_bf16 v[22:25], v[172:175], v[204:207], 0
	v_mfma_f32_16x16x32_bf16 v[18:21], v[180:183], v[204:207], 0
	v_mfma_f32_16x16x32_bf16 v[6:9], v[172:175], v[212:215], 0
	v_mfma_f32_16x16x32_bf16 v[2:5], v[180:183], v[212:215], 0
	v_mfma_f32_16x16x32_bf16 v[54:57], v[176:179], v[192:195], v[54:57]
	v_mfma_f32_16x16x32_bf16 v[50:53], v[184:187], v[192:195], v[50:53]
	v_mfma_f32_16x16x32_bf16 v[38:41], v[176:179], v[200:203], v[38:41]
	v_mfma_f32_16x16x32_bf16 v[34:37], v[184:187], v[200:203], v[34:37]
	v_mfma_f32_16x16x32_bf16 v[22:25], v[176:179], v[208:211], v[22:25]
	v_mfma_f32_16x16x32_bf16 v[18:21], v[184:187], v[208:211], v[18:21]
	v_mfma_f32_16x16x32_bf16 v[6:9], v[176:179], v[216:219], v[6:9]
	v_mfma_f32_16x16x32_bf16 v[2:5], v[184:187], v[216:219], v[2:5]
	s_setprio 0
	s_barrier
; #define PG8_STAGE(bufoff, gbase, voff) do { _Pragma("unroll") for (int _i = 0; _i < 2; ++_i) \
;         __builtin_amdgcn_global_load_lds((const unsigned*)((const char*)(gbase) + (voff)[_i]), (PG8_LAS unsigned*)(lds + (bufoff) + ldsw + _i * 8192), 16, 0, 0); } while (0)
; #define PG8_LDA(dst, b, h) do { if constexpr (DT != 1) { _Pragma("unroll") for (int m = 0; m < 4; ++m) _Pragma("unroll") for (int k = 0; k < 2; ++k) dst[m][k] = *(const PG8_LAS bf16x8*)(lds + PG8_SA(b, h) + aoff + m * 2048 + k * 1024); } \
;         else { _Pragma("unroll") for (int m = 0; m < 4; ++m) dst##8[m] = ld32(lds + PG8_SA(b, h) + aoff + m * 2048); } } while (0)
; #define PG8_LDB(dst, b, h) do { if constexpr (DT != 1) { _Pragma("unroll") for (int n = 0; n < 2; ++n) _Pragma("unroll") for (int k = 0; k < 2; ++k) dst[n][k] = *(const PG8_LAS bf16x8*)(lds + PG8_SB(b, h) + boff + n * 2048 + k * 1024); } \
;         else { _Pragma("unroll") for (int n = 0; n < 2; ++n) dst##8[n] = ld32(lds + PG8_SB(b, h) + boff + n * 2048); } } while (0)
; #define PG8_WAIT_V(n) asm volatile("s_waitcnt vmcnt(" #n ")" ::: "memory")
; #define PG8_WAIT_L(n) asm volatile("s_waitcnt lgkmcnt(" #n ")" ::: "memory")
; #define PG8_BAR __builtin_amdgcn_s_barrier()
; #define PG8_SCHED __builtin_amdgcn_sched_barrier(0)
;     ...
;         for (int t = 0; t < nt; t += 2) {
;     ...
;             PG8_LDB(B0, 1, 0); PG8_LDB(B1, 1, 1); PG8_SCHED; PG8_LDA(At, 1, 0); PG8_STAGE(PG8_SA(0, 1), a2 + hstepA, voffA);
;             PG8_WAIT_V(8); PG8_WAIT_L(0); PG8_BAR; PG8_MMA(0, 0, At, B0); PG8_MMA(0, 1, At, B1); PG8_BAR; PG8_SCHED;
;             PG8_LDA(At, 1, 1); PG8_STAGE(PG8_SB(1, 0), b3, voffB); PG8_STAGE(PG8_SB(1, 1), b3 + hstepB, voffB); PG8_STAGE(PG8_SA(1, 0), a3, voffA);
;             PG8_WAIT_V(8); PG8_WAIT_L(0); PG8_BAR; PG8_MMA(1, 0, At, B0); PG8_MMA(1, 1, At, B1); PG8_BAR; PG8_SCHED;
	ds_read_b128 v[156:159], v153
	ds_read_b128 v[160:163], v153 offset:1024
	ds_read_b128 v[164:167], v153 offset:2048
	ds_read_b128 v[168:171], v153 offset:3072
	ds_read_b128 v[172:175], v154
	ds_read_b128 v[176:179], v154 offset:1024
	ds_read_b128 v[180:183], v154 offset:2048
	ds_read_b128 v[184:187], v154 offset:3072
	s_add_u32 s30, s30, 0x80000
	s_addc_u32 s31, s31, 0
	s_mov_b32 m0, s47
	ds_read_b128 v[188:191], v152 offset:32768
	ds_read_b128 v[192:195], v152 offset:33792
	ds_read_b128 v[196:199], v152 offset:34816
	ds_read_b128 v[200:203], v152 offset:35840
	ds_read_b128 v[204:207], v152 offset:36864
	ds_read_b128 v[208:211], v152 offset:37888
	ds_read_b128 v[212:215], v152 offset:38912
	ds_read_b128 v[216:219], v152 offset:39936
	global_load_lds_dwordx4 v130, s[30:31]
	s_mov_b32 m0, s48
	s_nop 0
	global_load_lds_dwordx4 v134, s[30:31]
	s_waitcnt vmcnt(8) lgkmcnt(0)
	s_barrier
	s_setprio 1
	v_mfma_f32_16x16x32_bf16 v[122:125], v[156:159], v[188:191], v[122:125]
	v_mfma_f32_16x16x32_bf16 v[126:129], v[164:167], v[188:191], v[126:129]
	v_mfma_f32_16x16x32_bf16 v[110:113], v[156:159], v[196:199], v[110:113]
	v_mfma_f32_16x16x32_bf16 v[106:109], v[164:167], v[196:199], v[106:109]
	v_mfma_f32_16x16x32_bf16 v[94:97], v[156:159], v[204:207], v[94:97]
	v_mfma_f32_16x16x32_bf16 v[90:93], v[164:167], v[204:207], v[90:93]
	v_mfma_f32_16x16x32_bf16 v[78:81], v[156:159], v[212:215], v[78:81]
	v_mfma_f32_16x16x32_bf16 v[74:77], v[164:167], v[212:215], v[74:77]
	v_mfma_f32_16x16x32_bf16 v[122:125], v[160:163], v[192:195], v[122:125]
	v_mfma_f32_16x16x32_bf16 v[126:129], v[168:171], v[192:195], v[126:129]
	v_mfma_f32_16x16x32_bf16 v[110:113], v[160:163], v[200:203], v[110:113]
	v_mfma_f32_16x16x32_bf16 v[106:109], v[168:171], v[200:203], v[106:109]
	v_mfma_f32_16x16x32_bf16 v[94:97], v[160:163], v[208:211], v[94:97]
	v_mfma_f32_16x16x32_bf16 v[90:93], v[168:171], v[208:211], v[90:93]
	v_mfma_f32_16x16x32_bf16 v[78:81], v[160:163], v[216:219], v[78:81]
	v_mfma_f32_16x16x32_bf16 v[74:77], v[168:171], v[216:219], v[74:77]
	s_setprio 0
	s_setprio 1
	v_mfma_f32_16x16x32_bf16 v[118:121], v[172:175], v[188:191], v[118:121]
	v_mfma_f32_16x16x32_bf16 v[114:117], v[180:183], v[188:191], v[114:117]
	v_mfma_f32_16x16x32_bf16 v[102:105], v[172:175], v[196:199], v[102:105]
	v_mfma_f32_16x16x32_bf16 v[98:101], v[180:183], v[196:199], v[98:101]
	v_mfma_f32_16x16x32_bf16 v[86:89], v[172:175], v[204:207], v[86:89]
	v_mfma_f32_16x16x32_bf16 v[82:85], v[180:183], v[204:207], v[82:85]
	v_mfma_f32_16x16x32_bf16 v[70:73], v[172:175], v[212:215], v[70:73]
	v_mfma_f32_16x16x32_bf16 v[66:69], v[180:183], v[212:215], v[66:69]
	v_mfma_f32_16x16x32_bf16 v[118:121], v[176:179], v[192:195], v[118:121]
	v_mfma_f32_16x16x32_bf16 v[114:117], v[184:187], v[192:195], v[114:117]
	v_mfma_f32_16x16x32_bf16 v[102:105], v[176:179], v[200:203], v[102:105]
	v_mfma_f32_16x16x32_bf16 v[98:101], v[184:187], v[200:203], v[98:101]
	v_mfma_f32_16x16x32_bf16 v[86:89], v[176:179], v[208:211], v[86:89]
	v_mfma_f32_16x16x32_bf16 v[82:85], v[184:187], v[208:211], v[82:85]
	v_mfma_f32_16x16x32_bf16 v[70:73], v[176:179], v[216:219], v[70:73]
	v_mfma_f32_16x16x32_bf16 v[66:69], v[184:187], v[216:219], v[66:69]
	s_setprio 0
	s_barrier
	s_mov_b32 m0, s50
	s_add_u32 s28, s28, 0x80080
	ds_read_b128 v[188:191], v152 offset:49152
	ds_read_b128 v[192:195], v152 offset:50176
	ds_read_b128 v[196:199], v152 offset:51200
	ds_read_b128 v[200:203], v152 offset:52224
	ds_read_b128 v[204:207], v152 offset:53248
	ds_read_b128 v[208:211], v152 offset:54272
	ds_read_b128 v[212:215], v152 offset:55296
	ds_read_b128 v[216:219], v152 offset:56320
	global_load_lds_dwordx4 v132, s[98:99]
	s_mov_b32 m0, s51
	s_addc_u32 s29, s29, 0
	global_load_lds_dwordx4 v136, s[98:99]
	s_mov_b32 m0, s54
	s_nop 0
	global_load_lds_dwordx4 v132, s[28:29]
	s_mov_b32 m0, s55
	s_nop 0
	global_load_lds_dwordx4 v136, s[28:29]
	s_mov_b32 m0, s52
	s_nop 0
	global_load_lds_dwordx4 v130, s[100:101]
	s_mov_b32 m0, s53
	s_nop 0
	global_load_lds_dwordx4 v134, s[100:101]
	s_waitcnt vmcnt(8) lgkmcnt(0)
	s_barrier
	s_setprio 1
	v_mfma_f32_16x16x32_bf16 v[62:65], v[156:159], v[188:191], v[62:65]
	v_mfma_f32_16x16x32_bf16 v[58:61], v[164:167], v[188:191], v[58:61]
	v_mfma_f32_16x16x32_bf16 v[46:49], v[156:159], v[196:199], v[46:49]
	v_mfma_f32_16x16x32_bf16 v[42:45], v[164:167], v[196:199], v[42:45]
	v_mfma_f32_16x16x32_bf16 v[30:33], v[156:159], v[204:207], v[30:33]
	v_mfma_f32_16x16x32_bf16 v[26:29], v[164:167], v[204:207], v[26:29]
	v_mfma_f32_16x16x32_bf16 v[14:17], v[156:159], v[212:215], v[14:17]
	v_mfma_f32_16x16x32_bf16 v[10:13], v[164:167], v[212:215], v[10:13]
	v_mfma_f32_16x16x32_bf16 v[62:65], v[160:163], v[192:195], v[62:65]
	v_mfma_f32_16x16x32_bf16 v[58:61], v[168:171], v[192:195], v[58:61]
	v_mfma_f32_16x16x32_bf16 v[46:49], v[160:163], v[200:203], v[46:49]
	v_mfma_f32_16x16x32_bf16 v[42:45], v[168:171], v[200:203], v[42:45]
	v_mfma_f32_16x16x32_bf16 v[30:33], v[160:163], v[208:211], v[30:33]
	v_mfma_f32_16x16x32_bf16 v[26:29], v[168:171], v[208:211], v[26:29]
	v_mfma_f32_16x16x32_bf16 v[14:17], v[160:163], v[216:219], v[14:17]
	v_mfma_f32_16x16x32_bf16 v[10:13], v[168:171], v[216:219], v[10:13]
	s_setprio 0
	s_setprio 1
	v_mfma_f32_16x16x32_bf16 v[54:57], v[172:175], v[188:191], v[54:57]
	v_mfma_f32_16x16x32_bf16 v[50:53], v[180:183], v[188:191], v[50:53]
	v_mfma_f32_16x16x32_bf16 v[38:41], v[172:175], v[196:199], v[38:41]
	v_mfma_f32_16x16x32_bf16 v[34:37], v[180:183], v[196:199], v[34:37]
	v_mfma_f32_16x16x32_bf16 v[22:25], v[172:175], v[204:207], v[22:25]
	v_mfma_f32_16x16x32_bf16 v[18:21], v[180:183], v[204:207], v[18:21]
	v_mfma_f32_16x16x32_bf16 v[6:9], v[172:175], v[212:215], v[6:9]
	v_mfma_f32_16x16x32_bf16 v[2:5], v[180:183], v[212:215], v[2:5]
	v_mfma_f32_16x16x32_bf16 v[54:57], v[176:179], v[192:195], v[54:57]
	v_mfma_f32_16x16x32_bf16 v[50:53], v[184:187], v[192:195], v[50:53]
	v_mfma_f32_16x16x32_bf16 v[38:41], v[176:179], v[200:203], v[38:41]
	v_mfma_f32_16x16x32_bf16 v[34:37], v[184:187], v[200:203], v[34:37]
	v_mfma_f32_16x16x32_bf16 v[22:25], v[176:179], v[208:211], v[22:25]
	v_mfma_f32_16x16x32_bf16 v[18:21], v[184:187], v[208:211], v[18:21]
	v_mfma_f32_16x16x32_bf16 v[6:9], v[176:179], v[216:219], v[6:9]
	v_mfma_f32_16x16x32_bf16 v[2:5], v[184:187], v[216:219], v[2:5]
	s_setprio 0
	s_barrier
	s_add_u32 s63, s63, 0x100
	s_addc_u32 s64, s64, 0
	s_add_u32 s26, s26, 0x100
	s_addc_u32 s27, s27, 0
	s_cmp_ge_i32 s65, s49
	s_mov_b32 s28, s65
	s_cbranch_scc0 .LBB0_418
	s_branch .LBB0_419

; #define PG8_STAGE(bufoff, gbase, voff) do { _Pragma("unroll") for (int _i = 0; _i < 2; ++_i) \
;         __builtin_amdgcn_global_load_lds((const unsigned*)((const char*)(gbase) + (voff)[_i]), (PG8_LAS unsigned*)(lds + (bufoff) + ldsw + _i * 8192), 16, 0, 0); } while (0)
; #define PG8_LDA(dst, b, h) do { if constexpr (DT != 1) { _Pragma("unroll") for (int m = 0; m < 4; ++m) _Pragma("unroll") for (int k = 0; k < 2; ++k) dst[m][k] = *(const PG8_LAS bf16x8*)(lds + PG8_SA(b, h) + aoff + m * 2048 + k * 1024); } \
;         else { _Pragma("unroll") for (int m = 0; m < 4; ++m) dst##8[m] = ld32(lds + PG8_SA(b, h) + aoff + m * 2048); } } while (0)
; #define PG8_LDB(dst, b, h) do { if constexpr (DT != 1) { _Pragma("unroll") for (int n = 0; n < 2; ++n) _Pragma("unroll") for (int k = 0; k < 2; ++k) dst[n][k] = *(const PG8_LAS bf16x8*)(lds + PG8_SB(b, h) + boff + n * 2048 + k * 1024); } \
;         else { _Pragma("unroll") for (int n = 0; n < 2; ++n) dst##8[n] = ld32(lds + PG8_SB(b, h) + boff + n * 2048); } } while (0)
; #define PG8_WAIT_V(n) asm volatile("s_waitcnt vmcnt(" #n ")" ::: "memory")
; #define PG8_WAIT_L(n) asm volatile("s_waitcnt lgkmcnt(" #n ")" ::: "memory")
; #define PG8_BAR __builtin_amdgcn_s_barrier()
;     ...
;         const char* nA = has_next ? (const char*)g.A + (size_t)nxt.pm * tstepA : cA; const char* nB = has_next ? (const char*)g.Bt + (size_t)nxt.pn * tstepB : cB;
;         for (int t = 0; t < nt; t += 2) {
;             const bool last = (t == nt - 2);
;             const char* a1 = cA + (size_t)(t + 1) * kstep;
;             const char* a2 = last ? nA : cA + (size_t)(t + 2) * kstep; const char* b2 = last ? nB : cB + (size_t)(t + 2) * kstep;
;             const char* a3 = a2 + kstep; const char* b3 = b2 + kstep;
;             if (last && has_next) S.a_ready(nxt);
;             if constexpr (SP2) {
;             PG8_LDB(B0, 0, 0); PG8_LDB(B1, 0, 1); PG8_SCHED; PG8_LDA(At, 0, 0); PG8_STAGE(PG8_SA(1, 1), a1 + hstepA, voffA);
;             PG8_WAIT_V(8); PG8_WAIT_L(0); PG8_BAR; PG8_MMA(0, 0, At, B0); PG8_MMA(0, 1, At, B1); PG8_BAR; PG8_SCHED;
;             PG8_LDA(At, 0, 1); PG8_STAGE(PG8_SB(0, 0), b2, voffB); PG8_STAGE(PG8_SB(0, 1), b2 + hstepB, voffB); PG8_STAGE(PG8_SA(0, 0), a2, voffA);
;             PG8_WAIT_V(8); PG8_WAIT_L(0); PG8_BAR; PG8_MMA(1, 0, At, B0); PG8_MMA(1, 1, At, B1); PG8_BAR; PG8_SCHED;
.Lzs_3:
	s_cbranch_vccnz .LBB0_714
	s_and_b64 s[38:39], s[0:1], exec
	s_cselect_b32 s23, s27, s37
	s_cselect_b32 s25, s26, s36
	s_cselect_b32 s65, s29, s35
	s_cselect_b32 s66, s28, s34
	s_add_u32 s67, s34, 0x100
	s_addc_u32 s68, s35, 0
	s_add_u32 s34, s36, 0x80080
	s_addc_u32 s35, s37, 0
	s_mov_b32 s36, 0
	ds_read_b128 v[130:133], v173
	ds_read_b128 v[134:137], v173 offset:1024
	ds_read_b128 v[138:141], v173 offset:2048
	ds_read_b128 v[142:145], v173 offset:3072
	ds_read_b128 v[162:165], v174
	ds_read_b128 v[166:169], v174 offset:1024
	ds_read_b128 v[178:181], v174 offset:2048
	ds_read_b128 v[182:185], v174 offset:3072
	s_add_i32 s69, s36, 2
	s_add_u32 s37, s34, 0xfff80080
	s_addc_u32 s38, s35, -1
	s_cmp_eq_u32 s61, s36
	s_cselect_b32 s36, s66, s67
	s_cselect_b32 s39, s23, s38
	s_cselect_b32 s38, s25, s37
	s_cselect_b32 s37, s65, s68
	s_add_i32 m0, s49, 0xc000
	ds_read_b128 v[186:189], v175
	ds_read_b128 v[190:193], v175 offset:1024
	ds_read_b128 v[194:197], v175 offset:2048
	ds_read_b128 v[198:201], v175 offset:3072
	ds_read_b128 v[202:205], v175 offset:4096
	ds_read_b128 v[206:209], v175 offset:5120
	ds_read_b128 v[210:213], v175 offset:6144
	ds_read_b128 v[214:217], v175 offset:7168
	global_load_lds_dwordx4 v156, s[34:35]
	s_add_i32 m0, s49, 0xe000
	s_nop 0
	global_load_lds_dwordx4 v154, s[34:35]
	s_waitcnt vmcnt(8) lgkmcnt(0)
	s_barrier
	s_setprio 1
	v_mfma_f32_16x16x32_bf16 v[122:125], v[130:133], v[186:189], 0
	v_mfma_f32_16x16x32_bf16 v[126:129], v[138:141], v[186:189], 0
	v_mfma_f32_16x16x32_bf16 v[110:113], v[130:133], v[194:197], 0
	v_mfma_f32_16x16x32_bf16 v[106:109], v[138:141], v[194:197], 0
	v_mfma_f32_16x16x32_bf16 v[94:97], v[130:133], v[202:205], 0
	v_mfma_f32_16x16x32_bf16 v[90:93], v[138:141], v[202:205], 0
	v_mfma_f32_16x16x32_bf16 v[78:81], v[130:133], v[210:213], 0
	v_mfma_f32_16x16x32_bf16 v[74:77], v[138:141], v[210:213], 0
	v_mfma_f32_16x16x32_bf16 v[122:125], v[134:137], v[190:193], v[122:125]
	v_mfma_f32_16x16x32_bf16 v[126:129], v[142:145], v[190:193], v[126:129]
	v_mfma_f32_16x16x32_bf16 v[110:113], v[134:137], v[198:201], v[110:113]
	v_mfma_f32_16x16x32_bf16 v[106:109], v[142:145], v[198:201], v[106:109]
	v_mfma_f32_16x16x32_bf16 v[94:97], v[134:137], v[206:209], v[94:97]
	v_mfma_f32_16x16x32_bf16 v[90:93], v[142:145], v[206:209], v[90:93]
	v_mfma_f32_16x16x32_bf16 v[78:81], v[134:137], v[214:217], v[78:81]
	v_mfma_f32_16x16x32_bf16 v[74:77], v[142:145], v[214:217], v[74:77]
	s_setprio 0
	s_setprio 1
	v_mfma_f32_16x16x32_bf16 v[118:121], v[162:165], v[186:189], 0
	v_mfma_f32_16x16x32_bf16 v[114:117], v[178:181], v[186:189], 0
	v_mfma_f32_16x16x32_bf16 v[102:105], v[162:165], v[194:197], 0
	v_mfma_f32_16x16x32_bf16 v[98:101], v[178:181], v[194:197], 0
	v_mfma_f32_16x16x32_bf16 v[86:89], v[162:165], v[202:205], 0
	v_mfma_f32_16x16x32_bf16 v[82:85], v[178:181], v[202:205], 0
	v_mfma_f32_16x16x32_bf16 v[70:73], v[162:165], v[210:213], 0
	v_mfma_f32_16x16x32_bf16 v[66:69], v[178:181], v[210:213], 0
	v_mfma_f32_16x16x32_bf16 v[118:121], v[166:169], v[190:193], v[118:121]
	v_mfma_f32_16x16x32_bf16 v[114:117], v[182:185], v[190:193], v[114:117]
	v_mfma_f32_16x16x32_bf16 v[102:105], v[166:169], v[198:201], v[102:105]
	v_mfma_f32_16x16x32_bf16 v[98:101], v[182:185], v[198:201], v[98:101]
	v_mfma_f32_16x16x32_bf16 v[86:89], v[166:169], v[206:209], v[86:89]
	v_mfma_f32_16x16x32_bf16 v[82:85], v[182:185], v[206:209], v[82:85]
	v_mfma_f32_16x16x32_bf16 v[70:73], v[166:169], v[214:217], v[70:73]
	v_mfma_f32_16x16x32_bf16 v[66:69], v[182:185], v[214:217], v[66:69]
	s_setprio 0
	s_barrier
	s_mov_b32 m0, s31
	s_add_u32 s98, s36, 0x80
	s_addc_u32 s99, s37, 0
	s_add_u32 s70, s36, 0x80000
	ds_read_b128 v[186:189], v175 offset:16384
	ds_read_b128 v[190:193], v175 offset:17408
	ds_read_b128 v[194:197], v175 offset:18432
	ds_read_b128 v[198:201], v175 offset:19456
	ds_read_b128 v[202:205], v175 offset:20480
	ds_read_b128 v[206:209], v175 offset:21504
	ds_read_b128 v[210:213], v175 offset:22528
	ds_read_b128 v[214:217], v175 offset:23552
	global_load_lds_dwordx4 v148, s[36:37]
	s_mov_b32 m0, s46
	s_addc_u32 s71, s37, 0
	global_load_lds_dwordx4 v152, s[36:37]
	s_mov_b32 m0, s47
	s_nop 0
	global_load_lds_dwordx4 v148, s[70:71]
	s_mov_b32 m0, s48
	s_nop 0
	global_load_lds_dwordx4 v152, s[70:71]
	s_add_u32 s100, s38, 0x80
	s_addc_u32 s101, s39, 0
	s_mov_b32 m0, s49
	s_nop 0
	global_load_lds_dwordx4 v146, s[38:39]
	s_mov_b32 m0, s50
	s_nop 0
	global_load_lds_dwordx4 v150, s[38:39]
	s_waitcnt vmcnt(8) lgkmcnt(0)
	s_barrier
	s_setprio 1
	v_mfma_f32_16x16x32_bf16 v[62:65], v[130:133], v[186:189], 0
	v_mfma_f32_16x16x32_bf16 v[58:61], v[138:141], v[186:189], 0
	v_mfma_f32_16x16x32_bf16 v[46:49], v[130:133], v[194:197], 0
	v_mfma_f32_16x16x32_bf16 v[42:45], v[138:141], v[194:197], 0
	v_mfma_f32_16x16x32_bf16 v[30:33], v[130:133], v[202:205], 0
	v_mfma_f32_16x16x32_bf16 v[26:29], v[138:141], v[202:205], 0
	v_mfma_f32_16x16x32_bf16 v[14:17], v[130:133], v[210:213], 0
	v_mfma_f32_16x16x32_bf16 v[10:13], v[138:141], v[210:213], 0
	v_mfma_f32_16x16x32_bf16 v[62:65], v[134:137], v[190:193], v[62:65]
	v_mfma_f32_16x16x32_bf16 v[58:61], v[142:145], v[190:193], v[58:61]
	v_mfma_f32_16x16x32_bf16 v[46:49], v[134:137], v[198:201], v[46:49]
	v_mfma_f32_16x16x32_bf16 v[42:45], v[142:145], v[198:201], v[42:45]
	v_mfma_f32_16x16x32_bf16 v[30:33], v[134:137], v[206:209], v[30:33]
	v_mfma_f32_16x16x32_bf16 v[26:29], v[142:145], v[206:209], v[26:29]
	v_mfma_f32_16x16x32_bf16 v[14:17], v[134:137], v[214:217], v[14:17]
	v_mfma_f32_16x16x32_bf16 v[10:13], v[142:145], v[214:217], v[10:13]
	s_setprio 0
	s_setprio 1
	v_mfma_f32_16x16x32_bf16 v[54:57], v[162:165], v[186:189], 0
	v_mfma_f32_16x16x32_bf16 v[50:53], v[178:181], v[186:189], 0
	v_mfma_f32_16x16x32_bf16 v[38:41], v[162:165], v[194:197], 0
	v_mfma_f32_16x16x32_bf16 v[34:37], v[178:181], v[194:197], 0
	v_mfma_f32_16x16x32_bf16 v[22:25], v[162:165], v[202:205], 0
	v_mfma_f32_16x16x32_bf16 v[18:21], v[178:181], v[202:205], 0
	v_mfma_f32_16x16x32_bf16 v[6:9], v[162:165], v[210:213], 0
	v_mfma_f32_16x16x32_bf16 v[2:5], v[178:181], v[210:213], 0
	v_mfma_f32_16x16x32_bf16 v[54:57], v[166:169], v[190:193], v[54:57]
	v_mfma_f32_16x16x32_bf16 v[50:53], v[182:185], v[190:193], v[50:53]
	v_mfma_f32_16x16x32_bf16 v[38:41], v[166:169], v[198:201], v[38:41]
	v_mfma_f32_16x16x32_bf16 v[34:37], v[182:185], v[198:201], v[34:37]
	v_mfma_f32_16x16x32_bf16 v[22:25], v[166:169], v[206:209], v[22:25]
	v_mfma_f32_16x16x32_bf16 v[18:21], v[182:185], v[206:209], v[18:21]
	v_mfma_f32_16x16x32_bf16 v[6:9], v[166:169], v[214:217], v[6:9]
	v_mfma_f32_16x16x32_bf16 v[2:5], v[182:185], v[214:217], v[2:5]
	s_setprio 0
	s_barrier
; #define PG8_STAGE(bufoff, gbase, voff) do { _Pragma("unroll") for (int _i = 0; _i < 2; ++_i) \
;         __builtin_amdgcn_global_load_lds((const unsigned*)((const char*)(gbase) + (voff)[_i]), (PG8_LAS unsigned*)(lds + (bufoff) + ldsw + _i * 8192), 16, 0, 0); } while (0)
; #define PG8_LDA(dst, b, h) do { if constexpr (DT != 1) { _Pragma("unroll") for (int m = 0; m < 4; ++m) _Pragma("unroll") for (int k = 0; k < 2; ++k) dst[m][k] = *(const PG8_LAS bf16x8*)(lds + PG8_SA(b, h) + aoff + m * 2048 + k * 1024); } \
;         else { _Pragma("unroll") for (int m = 0; m < 4; ++m) dst##8[m] = ld32(lds + PG8_SA(b, h) + aoff + m * 2048); } } while (0)
; #define PG8_LDB(dst, b, h) do { if constexpr (DT != 1) { _Pragma("unroll") for (int n = 0; n < 2; ++n) _Pragma("unroll") for (int k = 0; k < 2; ++k) dst[n][k] = *(const PG8_LAS bf16x8*)(lds + PG8_SB(b, h) + boff + n * 2048 + k * 1024); } \
;         else { _Pragma("unroll") for (int n = 0; n < 2; ++n) dst##8[n] = ld32(lds + PG8_SB(b, h) + boff + n * 2048); } } while (0)
; #define PG8_WAIT_V(n) asm volatile("s_waitcnt vmcnt(" #n ")" ::: "memory")
; #define PG8_WAIT_L(n) asm volatile("s_waitcnt lgkmcnt(" #n ")" ::: "memory")
; #define PG8_BAR __builtin_amdgcn_s_barrier()
; #define PG8_SCHED __builtin_amdgcn_sched_barrier(0)
;     ...
;         for (int t = 0; t < nt; t += 2) {
;     ...
;             PG8_LDB(B0, 1, 0); PG8_LDB(B1, 1, 1); PG8_SCHED; PG8_LDA(At, 1, 0); PG8_STAGE(PG8_SA(0, 1), a2 + hstepA, voffA);
;             PG8_WAIT_V(8); PG8_WAIT_L(0); PG8_BAR; PG8_MMA(0, 0, At, B0); PG8_MMA(0, 1, At, B1); PG8_BAR; PG8_SCHED;
;             PG8_LDA(At, 1, 1); PG8_STAGE(PG8_SB(1, 0), b3, voffB); PG8_STAGE(PG8_SB(1, 1), b3 + hstepB, voffB); PG8_STAGE(PG8_SA(1, 0), a3, voffA);
;             PG8_WAIT_V(8); PG8_WAIT_L(0); PG8_BAR; PG8_MMA(1, 0, At, B0); PG8_MMA(1, 1, At, B1); PG8_BAR; PG8_SCHED;
	ds_read_b128 v[130:133], v176
	ds_read_b128 v[134:137], v176 offset:1024
	ds_read_b128 v[138:141], v176 offset:2048
	ds_read_b128 v[142:145], v176 offset:3072
	ds_read_b128 v[162:165], v177
	ds_read_b128 v[166:169], v177 offset:1024
	ds_read_b128 v[178:181], v177 offset:2048
	ds_read_b128 v[182:185], v177 offset:3072
	s_add_u32 s38, s38, 0x80000
	s_addc_u32 s39, s39, 0
	s_mov_b32 m0, s51
	ds_read_b128 v[186:189], v175 offset:32768
	ds_read_b128 v[190:193], v175 offset:33792
	ds_read_b128 v[194:197], v175 offset:34816
	ds_read_b128 v[198:201], v175 offset:35840
	ds_read_b128 v[202:205], v175 offset:36864
	ds_read_b128 v[206:209], v175 offset:37888
	ds_read_b128 v[210:213], v175 offset:38912
	ds_read_b128 v[214:217], v175 offset:39936
	global_load_lds_dwordx4 v146, s[38:39]
	s_mov_b32 m0, s52
	s_nop 0
	global_load_lds_dwordx4 v150, s[38:39]
	s_waitcnt vmcnt(8) lgkmcnt(0)
	s_barrier
	s_setprio 1
	v_mfma_f32_16x16x32_bf16 v[122:125], v[130:133], v[186:189], v[122:125]
	v_mfma_f32_16x16x32_bf16 v[126:129], v[138:141], v[186:189], v[126:129]
	v_mfma_f32_16x16x32_bf16 v[110:113], v[130:133], v[194:197], v[110:113]
	v_mfma_f32_16x16x32_bf16 v[106:109], v[138:141], v[194:197], v[106:109]
	v_mfma_f32_16x16x32_bf16 v[94:97], v[130:133], v[202:205], v[94:97]
	v_mfma_f32_16x16x32_bf16 v[90:93], v[138:141], v[202:205], v[90:93]
	v_mfma_f32_16x16x32_bf16 v[78:81], v[130:133], v[210:213], v[78:81]
	v_mfma_f32_16x16x32_bf16 v[74:77], v[138:141], v[210:213], v[74:77]
	v_mfma_f32_16x16x32_bf16 v[122:125], v[134:137], v[190:193], v[122:125]
	v_mfma_f32_16x16x32_bf16 v[126:129], v[142:145], v[190:193], v[126:129]
	v_mfma_f32_16x16x32_bf16 v[110:113], v[134:137], v[198:201], v[110:113]
	v_mfma_f32_16x16x32_bf16 v[106:109], v[142:145], v[198:201], v[106:109]
	v_mfma_f32_16x16x32_bf16 v[94:97], v[134:137], v[206:209], v[94:97]
	v_mfma_f32_16x16x32_bf16 v[90:93], v[142:145], v[206:209], v[90:93]
	v_mfma_f32_16x16x32_bf16 v[78:81], v[134:137], v[214:217], v[78:81]
	v_mfma_f32_16x16x32_bf16 v[74:77], v[142:145], v[214:217], v[74:77]
	s_setprio 0
	s_setprio 1
	v_mfma_f32_16x16x32_bf16 v[118:121], v[162:165], v[186:189], v[118:121]
	v_mfma_f32_16x16x32_bf16 v[114:117], v[178:181], v[186:189], v[114:117]
	v_mfma_f32_16x16x32_bf16 v[102:105], v[162:165], v[194:197], v[102:105]
	v_mfma_f32_16x16x32_bf16 v[98:101], v[178:181], v[194:197], v[98:101]
	v_mfma_f32_16x16x32_bf16 v[86:89], v[162:165], v[202:205], v[86:89]
	v_mfma_f32_16x16x32_bf16 v[82:85], v[178:181], v[202:205], v[82:85]
	v_mfma_f32_16x16x32_bf16 v[70:73], v[162:165], v[210:213], v[70:73]
	v_mfma_f32_16x16x32_bf16 v[66:69], v[178:181], v[210:213], v[66:69]
	v_mfma_f32_16x16x32_bf16 v[118:121], v[166:169], v[190:193], v[118:121]
	v_mfma_f32_16x16x32_bf16 v[114:117], v[182:185], v[190:193], v[114:117]
	v_mfma_f32_16x16x32_bf16 v[102:105], v[166:169], v[198:201], v[102:105]
	v_mfma_f32_16x16x32_bf16 v[98:101], v[182:185], v[198:201], v[98:101]
	v_mfma_f32_16x16x32_bf16 v[86:89], v[166:169], v[206:209], v[86:89]
	v_mfma_f32_16x16x32_bf16 v[82:85], v[182:185], v[206:209], v[82:85]
	v_mfma_f32_16x16x32_bf16 v[70:73], v[166:169], v[214:217], v[70:73]
	v_mfma_f32_16x16x32_bf16 v[66:69], v[182:185], v[214:217], v[66:69]
	s_setprio 0
	s_barrier
	s_mov_b32 m0, s55
	s_add_u32 s36, s36, 0x80080
	ds_read_b128 v[186:189], v175 offset:49152
	ds_read_b128 v[190:193], v175 offset:50176
	ds_read_b128 v[194:197], v175 offset:51200
	ds_read_b128 v[198:201], v175 offset:52224
	ds_read_b128 v[202:205], v175 offset:53248
	ds_read_b128 v[206:209], v175 offset:54272
	ds_read_b128 v[210:213], v175 offset:55296
	ds_read_b128 v[214:217], v175 offset:56320
	global_load_lds_dwordx4 v148, s[98:99]
	s_mov_b32 m0, s56
	s_addc_u32 s37, s37, 0
	global_load_lds_dwordx4 v152, s[98:99]
	s_mov_b32 m0, s59
	s_nop 0
	global_load_lds_dwordx4 v148, s[36:37]
	s_mov_b32 m0, s60
	s_nop 0
	global_load_lds_dwordx4 v152, s[36:37]
	s_mov_b32 m0, s57
	s_nop 0
	global_load_lds_dwordx4 v146, s[100:101]
	s_mov_b32 m0, s58
	s_nop 0
	global_load_lds_dwordx4 v150, s[100:101]
	s_waitcnt vmcnt(8) lgkmcnt(0)
	s_barrier
	s_setprio 1
	v_mfma_f32_16x16x32_bf16 v[62:65], v[130:133], v[186:189], v[62:65]
	v_mfma_f32_16x16x32_bf16 v[58:61], v[138:141], v[186:189], v[58:61]
	v_mfma_f32_16x16x32_bf16 v[46:49], v[130:133], v[194:197], v[46:49]
	v_mfma_f32_16x16x32_bf16 v[42:45], v[138:141], v[194:197], v[42:45]
	v_mfma_f32_16x16x32_bf16 v[30:33], v[130:133], v[202:205], v[30:33]
	v_mfma_f32_16x16x32_bf16 v[26:29], v[138:141], v[202:205], v[26:29]
	v_mfma_f32_16x16x32_bf16 v[14:17], v[130:133], v[210:213], v[14:17]
	v_mfma_f32_16x16x32_bf16 v[10:13], v[138:141], v[210:213], v[10:13]
	v_mfma_f32_16x16x32_bf16 v[62:65], v[134:137], v[190:193], v[62:65]
	v_mfma_f32_16x16x32_bf16 v[58:61], v[142:145], v[190:193], v[58:61]
	v_mfma_f32_16x16x32_bf16 v[46:49], v[134:137], v[198:201], v[46:49]
	v_mfma_f32_16x16x32_bf16 v[42:45], v[142:145], v[198:201], v[42:45]
	v_mfma_f32_16x16x32_bf16 v[30:33], v[134:137], v[206:209], v[30:33]
	v_mfma_f32_16x16x32_bf16 v[26:29], v[142:145], v[206:209], v[26:29]
	v_mfma_f32_16x16x32_bf16 v[14:17], v[134:137], v[214:217], v[14:17]
	v_mfma_f32_16x16x32_bf16 v[10:13], v[142:145], v[214:217], v[10:13]
	s_setprio 0
	s_setprio 1
	v_mfma_f32_16x16x32_bf16 v[54:57], v[162:165], v[186:189], v[54:57]
	v_mfma_f32_16x16x32_bf16 v[50:53], v[178:181], v[186:189], v[50:53]
	v_mfma_f32_16x16x32_bf16 v[38:41], v[162:165], v[194:197], v[38:41]
	v_mfma_f32_16x16x32_bf16 v[34:37], v[178:181], v[194:197], v[34:37]
	v_mfma_f32_16x16x32_bf16 v[22:25], v[162:165], v[202:205], v[22:25]
	v_mfma_f32_16x16x32_bf16 v[18:21], v[178:181], v[202:205], v[18:21]
	v_mfma_f32_16x16x32_bf16 v[6:9], v[162:165], v[210:213], v[6:9]
	v_mfma_f32_16x16x32_bf16 v[2:5], v[178:181], v[210:213], v[2:5]
	v_mfma_f32_16x16x32_bf16 v[54:57], v[166:169], v[190:193], v[54:57]
	v_mfma_f32_16x16x32_bf16 v[50:53], v[182:185], v[190:193], v[50:53]
	v_mfma_f32_16x16x32_bf16 v[38:41], v[166:169], v[198:201], v[38:41]
	v_mfma_f32_16x16x32_bf16 v[34:37], v[182:185], v[198:201], v[34:37]
	v_mfma_f32_16x16x32_bf16 v[22:25], v[166:169], v[206:209], v[22:25]
	v_mfma_f32_16x16x32_bf16 v[18:21], v[182:185], v[206:209], v[18:21]
	v_mfma_f32_16x16x32_bf16 v[6:9], v[166:169], v[214:217], v[6:9]
	v_mfma_f32_16x16x32_bf16 v[2:5], v[182:185], v[214:217], v[2:5]
	s_setprio 0
	s_barrier
	s_add_u32 s67, s67, 0x100
	s_addc_u32 s68, s68, 0
	s_add_u32 s34, s34, 0x100
	s_addc_u32 s35, s35, 0
	s_cmp_ge_i32 s69, s54
	s_mov_b32 s36, s69
	s_cbranch_scc0 .LBB0_713
	s_branch .LBB0_714

; #define PG8_STAGE(bufoff, gbase, voff) do { _Pragma("unroll") for (int _i = 0; _i < 2; ++_i) \
;         __builtin_amdgcn_global_load_lds((const unsigned*)((const char*)(gbase) + (voff)[_i]), (PG8_LAS unsigned*)(lds + (bufoff) + ldsw + _i * 8192), 16, 0, 0); } while (0)
; #define PG8_LDA(dst, b, h) do { if constexpr (DT != 1) { _Pragma("unroll") for (int m = 0; m < 4; ++m) _Pragma("unroll") for (int k = 0; k < 2; ++k) dst[m][k] = *(const PG8_LAS bf16x8*)(lds + PG8_SA(b, h) + aoff + m * 2048 + k * 1024); } \
;         else { _Pragma("unroll") for (int m = 0; m < 4; ++m) dst##8[m] = ld32(lds + PG8_SA(b, h) + aoff + m * 2048); } } while (0)
; #define PG8_LDB(dst, b, h) do { if constexpr (DT != 1) { _Pragma("unroll") for (int n = 0; n < 2; ++n) _Pragma("unroll") for (int k = 0; k < 2; ++k) dst[n][k] = *(const PG8_LAS bf16x8*)(lds + PG8_SB(b, h) + boff + n * 2048 + k * 1024); } \
;         else { _Pragma("unroll") for (int n = 0; n < 2; ++n) dst##8[n] = ld32(lds + PG8_SB(b, h) + boff + n * 2048); } } while (0)
; #define PG8_WAIT_V(n) asm volatile("s_waitcnt vmcnt(" #n ")" ::: "memory")
; #define PG8_WAIT_L(n) asm volatile("s_waitcnt lgkmcnt(" #n ")" ::: "memory")
; #define PG8_BAR __builtin_amdgcn_s_barrier()
;     ...
;         const char* nA = has_next ? (const char*)g.A + (size_t)nxt.pm * tstepA : cA; const char* nB = has_next ? (const char*)g.Bt + (size_t)nxt.pn * tstepB : cB;
;         for (int t = 0; t < nt; t += 2) {
;             const bool last = (t == nt - 2);
;             const char* a1 = cA + (size_t)(t + 1) * kstep;
;             const char* a2 = last ? nA : cA + (size_t)(t + 2) * kstep; const char* b2 = last ? nB : cB + (size_t)(t + 2) * kstep;
;             const char* a3 = a2 + kstep; const char* b3 = b2 + kstep;
;             if (last && has_next) S.a_ready(nxt);
;             if constexpr (SP2) {
;             PG8_LDB(B0, 0, 0); PG8_LDB(B1, 0, 1); PG8_SCHED; PG8_LDA(At, 0, 0); PG8_STAGE(PG8_SA(1, 1), a1 + hstepA, voffA);
;             PG8_WAIT_V(8); PG8_WAIT_L(0); PG8_BAR; PG8_MMA(0, 0, At, B0); PG8_MMA(0, 1, At, B1); PG8_BAR; PG8_SCHED;
;             PG8_LDA(At, 0, 1); PG8_STAGE(PG8_SB(0, 0), b2, voffB); PG8_STAGE(PG8_SB(0, 1), b2 + hstepB, voffB); PG8_STAGE(PG8_SA(0, 0), a2, voffA);
;             PG8_WAIT_V(8); PG8_WAIT_L(0); PG8_BAR; PG8_MMA(1, 0, At, B0); PG8_MMA(1, 1, At, B1); PG8_BAR; PG8_SCHED;
.Lzt_2:
	s_cbranch_vccnz .LBB0_924
	s_add_u32 s65, s28, 0x100
	s_addc_u32 s66, s29, 0
	s_mov_b32 s30, 0
	ds_read_b128 v[146:149], v173
	ds_read_b128 v[150:153], v173 offset:1024
	ds_read_b128 v[154:157], v173 offset:2048
	ds_read_b128 v[158:161], v173 offset:3072
	ds_read_b128 v[162:165], v174
	ds_read_b128 v[166:169], v174 offset:1024
	ds_read_b128 v[178:181], v174 offset:2048
	ds_read_b128 v[182:185], v174 offset:3072
	s_add_i32 s67, s30, 2
	s_add_u32 s28, s26, 0x100
	s_addc_u32 s29, s27, 0
	s_cmp_eq_u32 s58, s30
	s_cselect_b32 s30, s24, s65
	s_cselect_b32 s35, s3, s29
	s_cselect_b32 s34, s2, s28
	s_cselect_b32 s31, s25, s66
	v_lshl_add_u64 v[170:171], s[26:27], 0, v[140:141]
	s_add_i32 m0, s46, 0xc000
	ds_read_b128 v[186:189], v175
	ds_read_b128 v[190:193], v175 offset:1024
	ds_read_b128 v[194:197], v175 offset:2048
	ds_read_b128 v[198:201], v175 offset:3072
	ds_read_b128 v[202:205], v175 offset:4096
	ds_read_b128 v[206:209], v175 offset:5120
	ds_read_b128 v[210:213], v175 offset:6144
	ds_read_b128 v[214:217], v175 offset:7168
	global_load_lds_dwordx4 v[170:171], off
	v_lshl_add_u64 v[170:171], s[26:27], 0, v[138:139]
	s_add_i32 m0, s46, 0xe000
	s_nop 0
	global_load_lds_dwordx4 v[170:171], off
	s_waitcnt vmcnt(8) lgkmcnt(0)
	s_barrier
	s_setprio 1
	v_mfma_f32_16x16x32_bf16 v[126:129], v[146:149], v[186:189], 0
	v_mfma_f32_16x16x32_bf16 v[122:125], v[154:157], v[186:189], 0
	v_mfma_f32_16x16x32_bf16 v[118:121], v[146:149], v[194:197], 0
	v_mfma_f32_16x16x32_bf16 v[114:117], v[154:157], v[194:197], 0
	v_mfma_f32_16x16x32_bf16 v[106:109], v[146:149], v[202:205], 0
	v_mfma_f32_16x16x32_bf16 v[98:101], v[154:157], v[202:205], 0
	v_mfma_f32_16x16x32_bf16 v[90:93], v[146:149], v[210:213], 0
	v_mfma_f32_16x16x32_bf16 v[82:85], v[154:157], v[210:213], 0
	v_mfma_f32_16x16x32_bf16 v[126:129], v[150:153], v[190:193], v[126:129]
	v_mfma_f32_16x16x32_bf16 v[122:125], v[158:161], v[190:193], v[122:125]
	v_mfma_f32_16x16x32_bf16 v[118:121], v[150:153], v[198:201], v[118:121]
	v_mfma_f32_16x16x32_bf16 v[114:117], v[158:161], v[198:201], v[114:117]
	v_mfma_f32_16x16x32_bf16 v[106:109], v[150:153], v[206:209], v[106:109]
	v_mfma_f32_16x16x32_bf16 v[98:101], v[158:161], v[206:209], v[98:101]
	v_mfma_f32_16x16x32_bf16 v[90:93], v[150:153], v[214:217], v[90:93]
	v_mfma_f32_16x16x32_bf16 v[82:85], v[158:161], v[214:217], v[82:85]
	s_setprio 0
	s_setprio 1
	v_mfma_f32_16x16x32_bf16 v[110:113], v[162:165], v[186:189], 0
	v_mfma_f32_16x16x32_bf16 v[102:105], v[178:181], v[186:189], 0
	v_mfma_f32_16x16x32_bf16 v[94:97], v[162:165], v[194:197], 0
	v_mfma_f32_16x16x32_bf16 v[86:89], v[178:181], v[194:197], 0
	v_mfma_f32_16x16x32_bf16 v[78:81], v[162:165], v[202:205], 0
	v_mfma_f32_16x16x32_bf16 v[74:77], v[178:181], v[202:205], 0
	v_mfma_f32_16x16x32_bf16 v[70:73], v[162:165], v[210:213], 0
	v_mfma_f32_16x16x32_bf16 v[66:69], v[178:181], v[210:213], 0
	v_mfma_f32_16x16x32_bf16 v[110:113], v[166:169], v[190:193], v[110:113]
	v_mfma_f32_16x16x32_bf16 v[102:105], v[182:185], v[190:193], v[102:105]
	v_mfma_f32_16x16x32_bf16 v[94:97], v[166:169], v[198:201], v[94:97]
	v_mfma_f32_16x16x32_bf16 v[86:89], v[182:185], v[198:201], v[86:89]
	v_mfma_f32_16x16x32_bf16 v[78:81], v[166:169], v[206:209], v[78:81]
	v_mfma_f32_16x16x32_bf16 v[74:77], v[182:185], v[206:209], v[74:77]
	v_mfma_f32_16x16x32_bf16 v[70:73], v[166:169], v[214:217], v[70:73]
	v_mfma_f32_16x16x32_bf16 v[66:69], v[182:185], v[214:217], v[66:69]
	s_setprio 0
	s_barrier
	s_mov_b32 m0, s42
	s_add_u32 s98, s30, 0x80
	s_addc_u32 s99, s31, 0
	s_add_u32 s26, s30, 0x160000
	ds_read_b128 v[186:189], v175 offset:16384
	ds_read_b128 v[190:193], v175 offset:17408
	ds_read_b128 v[194:197], v175 offset:18432
	ds_read_b128 v[198:201], v175 offset:19456
	ds_read_b128 v[202:205], v175 offset:20480
	ds_read_b128 v[206:209], v175 offset:21504
	ds_read_b128 v[210:213], v175 offset:22528
	ds_read_b128 v[214:217], v175 offset:23552
	global_load_lds_dwordx4 v132, s[30:31]
	s_mov_b32 m0, s43
	s_addc_u32 s27, s31, 0
	global_load_lds_dwordx4 v136, s[30:31]
	s_mov_b32 m0, s44
	s_nop 0
	global_load_lds_dwordx4 v132, s[26:27]
	s_mov_b32 m0, s45
	s_nop 0
	global_load_lds_dwordx4 v136, s[26:27]
	s_add_u32 s100, s34, 0x80
	s_addc_u32 s101, s35, 0
	s_mov_b32 m0, s46
	s_nop 0
	global_load_lds_dwordx4 v130, s[34:35]
	s_mov_b32 m0, s47
	s_nop 0
	global_load_lds_dwordx4 v134, s[34:35]
	s_waitcnt vmcnt(8) lgkmcnt(0)
	s_barrier
	s_setprio 1
	v_mfma_f32_16x16x32_bf16 v[62:65], v[146:149], v[186:189], 0
	v_mfma_f32_16x16x32_bf16 v[58:61], v[154:157], v[186:189], 0
	v_mfma_f32_16x16x32_bf16 v[54:57], v[146:149], v[194:197], 0
	v_mfma_f32_16x16x32_bf16 v[50:53], v[154:157], v[194:197], 0
	v_mfma_f32_16x16x32_bf16 v[42:45], v[146:149], v[202:205], 0
	v_mfma_f32_16x16x32_bf16 v[34:37], v[154:157], v[202:205], 0
	v_mfma_f32_16x16x32_bf16 v[26:29], v[146:149], v[210:213], 0
	v_mfma_f32_16x16x32_bf16 v[18:21], v[154:157], v[210:213], 0
	v_mfma_f32_16x16x32_bf16 v[62:65], v[150:153], v[190:193], v[62:65]
	v_mfma_f32_16x16x32_bf16 v[58:61], v[158:161], v[190:193], v[58:61]
	v_mfma_f32_16x16x32_bf16 v[54:57], v[150:153], v[198:201], v[54:57]
	v_mfma_f32_16x16x32_bf16 v[50:53], v[158:161], v[198:201], v[50:53]
	v_mfma_f32_16x16x32_bf16 v[42:45], v[150:153], v[206:209], v[42:45]
	v_mfma_f32_16x16x32_bf16 v[34:37], v[158:161], v[206:209], v[34:37]
	v_mfma_f32_16x16x32_bf16 v[26:29], v[150:153], v[214:217], v[26:29]
	v_mfma_f32_16x16x32_bf16 v[18:21], v[158:161], v[214:217], v[18:21]
	s_setprio 0
	s_setprio 1
	v_mfma_f32_16x16x32_bf16 v[46:49], v[162:165], v[186:189], 0
	v_mfma_f32_16x16x32_bf16 v[38:41], v[178:181], v[186:189], 0
	v_mfma_f32_16x16x32_bf16 v[30:33], v[162:165], v[194:197], 0
	v_mfma_f32_16x16x32_bf16 v[22:25], v[178:181], v[194:197], 0
	v_mfma_f32_16x16x32_bf16 v[14:17], v[162:165], v[202:205], 0
	v_mfma_f32_16x16x32_bf16 v[10:13], v[178:181], v[202:205], 0
	v_mfma_f32_16x16x32_bf16 v[6:9], v[162:165], v[210:213], 0
	v_mfma_f32_16x16x32_bf16 v[2:5], v[178:181], v[210:213], 0
	v_mfma_f32_16x16x32_bf16 v[46:49], v[166:169], v[190:193], v[46:49]
	v_mfma_f32_16x16x32_bf16 v[38:41], v[182:185], v[190:193], v[38:41]
	v_mfma_f32_16x16x32_bf16 v[30:33], v[166:169], v[198:201], v[30:33]
	v_mfma_f32_16x16x32_bf16 v[22:25], v[182:185], v[198:201], v[22:25]
	v_mfma_f32_16x16x32_bf16 v[14:17], v[166:169], v[206:209], v[14:17]
	v_mfma_f32_16x16x32_bf16 v[10:13], v[182:185], v[206:209], v[10:13]
	v_mfma_f32_16x16x32_bf16 v[6:9], v[166:169], v[214:217], v[6:9]
	v_mfma_f32_16x16x32_bf16 v[2:5], v[182:185], v[214:217], v[2:5]
	s_setprio 0
	s_barrier
; #define PG8_STAGE(bufoff, gbase, voff) do { _Pragma("unroll") for (int _i = 0; _i < 2; ++_i) \
;         __builtin_amdgcn_global_load_lds((const unsigned*)((const char*)(gbase) + (voff)[_i]), (PG8_LAS unsigned*)(lds + (bufoff) + ldsw + _i * 8192), 16, 0, 0); } while (0)
; #define PG8_LDA(dst, b, h) do { if constexpr (DT != 1) { _Pragma("unroll") for (int m = 0; m < 4; ++m) _Pragma("unroll") for (int k = 0; k < 2; ++k) dst[m][k] = *(const PG8_LAS bf16x8*)(lds + PG8_SA(b, h) + aoff + m * 2048 + k * 1024); } \
;         else { _Pragma("unroll") for (int m = 0; m < 4; ++m) dst##8[m] = ld32(lds + PG8_SA(b, h) + aoff + m * 2048); } } while (0)
; #define PG8_LDB(dst, b, h) do { if constexpr (DT != 1) { _Pragma("unroll") for (int n = 0; n < 2; ++n) _Pragma("unroll") for (int k = 0; k < 2; ++k) dst[n][k] = *(const PG8_LAS bf16x8*)(lds + PG8_SB(b, h) + boff + n * 2048 + k * 1024); } \
;         else { _Pragma("unroll") for (int n = 0; n < 2; ++n) dst##8[n] = ld32(lds + PG8_SB(b, h) + boff + n * 2048); } } while (0)
; #define PG8_WAIT_V(n) asm volatile("s_waitcnt vmcnt(" #n ")" ::: "memory")
; #define PG8_WAIT_L(n) asm volatile("s_waitcnt lgkmcnt(" #n ")" ::: "memory")
; #define PG8_BAR __builtin_amdgcn_s_barrier()
; #define PG8_SCHED __builtin_amdgcn_sched_barrier(0)
;     ...
;             PG8_LDB(B0, 1, 0); PG8_LDB(B1, 1, 1); PG8_SCHED; PG8_LDA(At, 1, 0); PG8_STAGE(PG8_SA(0, 1), a2 + hstepA, voffA);
;             PG8_WAIT_V(8); PG8_WAIT_L(0); PG8_BAR; PG8_MMA(0, 0, At, B0); PG8_MMA(0, 1, At, B1); PG8_BAR; PG8_SCHED;
;             PG8_LDA(At, 1, 1); PG8_STAGE(PG8_SB(1, 0), b3, voffB); PG8_STAGE(PG8_SB(1, 1), b3 + hstepB, voffB); PG8_STAGE(PG8_SA(1, 0), a3, voffA);
;             PG8_WAIT_V(8); PG8_WAIT_L(0); PG8_BAR; PG8_MMA(1, 0, At, B0); PG8_MMA(1, 1, At, B1); PG8_BAR; PG8_SCHED;
	ds_read_b128 v[146:149], v176
	ds_read_b128 v[150:153], v176 offset:1024
	ds_read_b128 v[154:157], v176 offset:2048
	ds_read_b128 v[158:161], v176 offset:3072
	ds_read_b128 v[162:165], v177
	ds_read_b128 v[166:169], v177 offset:1024
	ds_read_b128 v[178:181], v177 offset:2048
	ds_read_b128 v[182:185], v177 offset:3072
	s_add_u32 s26, s34, 0x160000
	s_addc_u32 s27, s35, 0
	s_mov_b32 m0, s48
	ds_read_b128 v[186:189], v175 offset:32768
	ds_read_b128 v[190:193], v175 offset:33792
	ds_read_b128 v[194:197], v175 offset:34816
	ds_read_b128 v[198:201], v175 offset:35840
	ds_read_b128 v[202:205], v175 offset:36864
	ds_read_b128 v[206:209], v175 offset:37888
	ds_read_b128 v[210:213], v175 offset:38912
	ds_read_b128 v[214:217], v175 offset:39936
	global_load_lds_dwordx4 v130, s[26:27]
	s_mov_b32 m0, s49
	s_nop 0
	global_load_lds_dwordx4 v134, s[26:27]
	s_waitcnt vmcnt(8) lgkmcnt(0)
	s_barrier
	s_setprio 1
	v_mfma_f32_16x16x32_bf16 v[126:129], v[146:149], v[186:189], v[126:129]
	v_mfma_f32_16x16x32_bf16 v[122:125], v[154:157], v[186:189], v[122:125]
	v_mfma_f32_16x16x32_bf16 v[118:121], v[146:149], v[194:197], v[118:121]
	v_mfma_f32_16x16x32_bf16 v[114:117], v[154:157], v[194:197], v[114:117]
	v_mfma_f32_16x16x32_bf16 v[106:109], v[146:149], v[202:205], v[106:109]
	v_mfma_f32_16x16x32_bf16 v[98:101], v[154:157], v[202:205], v[98:101]
	v_mfma_f32_16x16x32_bf16 v[90:93], v[146:149], v[210:213], v[90:93]
	v_mfma_f32_16x16x32_bf16 v[82:85], v[154:157], v[210:213], v[82:85]
	v_mfma_f32_16x16x32_bf16 v[126:129], v[150:153], v[190:193], v[126:129]
	v_mfma_f32_16x16x32_bf16 v[122:125], v[158:161], v[190:193], v[122:125]
	v_mfma_f32_16x16x32_bf16 v[118:121], v[150:153], v[198:201], v[118:121]
	v_mfma_f32_16x16x32_bf16 v[114:117], v[158:161], v[198:201], v[114:117]
	v_mfma_f32_16x16x32_bf16 v[106:109], v[150:153], v[206:209], v[106:109]
	v_mfma_f32_16x16x32_bf16 v[98:101], v[158:161], v[206:209], v[98:101]
	v_mfma_f32_16x16x32_bf16 v[90:93], v[150:153], v[214:217], v[90:93]
	v_mfma_f32_16x16x32_bf16 v[82:85], v[158:161], v[214:217], v[82:85]
	s_setprio 0
	s_setprio 1
	v_mfma_f32_16x16x32_bf16 v[110:113], v[162:165], v[186:189], v[110:113]
	v_mfma_f32_16x16x32_bf16 v[102:105], v[178:181], v[186:189], v[102:105]
	v_mfma_f32_16x16x32_bf16 v[94:97], v[162:165], v[194:197], v[94:97]
	v_mfma_f32_16x16x32_bf16 v[86:89], v[178:181], v[194:197], v[86:89]
	v_mfma_f32_16x16x32_bf16 v[78:81], v[162:165], v[202:205], v[78:81]
	v_mfma_f32_16x16x32_bf16 v[74:77], v[178:181], v[202:205], v[74:77]
	v_mfma_f32_16x16x32_bf16 v[70:73], v[162:165], v[210:213], v[70:73]
	v_mfma_f32_16x16x32_bf16 v[66:69], v[178:181], v[210:213], v[66:69]
	v_mfma_f32_16x16x32_bf16 v[110:113], v[166:169], v[190:193], v[110:113]
	v_mfma_f32_16x16x32_bf16 v[102:105], v[182:185], v[190:193], v[102:105]
	v_mfma_f32_16x16x32_bf16 v[94:97], v[166:169], v[198:201], v[94:97]
	v_mfma_f32_16x16x32_bf16 v[86:89], v[182:185], v[198:201], v[86:89]
	v_mfma_f32_16x16x32_bf16 v[78:81], v[166:169], v[206:209], v[78:81]
	v_mfma_f32_16x16x32_bf16 v[74:77], v[182:185], v[206:209], v[74:77]
	v_mfma_f32_16x16x32_bf16 v[70:73], v[166:169], v[214:217], v[70:73]
	v_mfma_f32_16x16x32_bf16 v[66:69], v[182:185], v[214:217], v[66:69]
	s_setprio 0
	s_barrier
	s_mov_b32 m0, s52
	s_add_u32 s26, s30, 0x160080
	ds_read_b128 v[186:189], v175 offset:49152
	ds_read_b128 v[190:193], v175 offset:50176
	ds_read_b128 v[194:197], v175 offset:51200
	ds_read_b128 v[198:201], v175 offset:52224
	ds_read_b128 v[202:205], v175 offset:53248
	ds_read_b128 v[206:209], v175 offset:54272
	ds_read_b128 v[210:213], v175 offset:55296
	ds_read_b128 v[214:217], v175 offset:56320
	global_load_lds_dwordx4 v132, s[98:99]
	s_mov_b32 m0, s53
	s_addc_u32 s27, s31, 0
	global_load_lds_dwordx4 v136, s[98:99]
	s_mov_b32 m0, s56
	s_nop 0
	global_load_lds_dwordx4 v132, s[26:27]
	s_mov_b32 m0, s57
	s_nop 0
	global_load_lds_dwordx4 v136, s[26:27]
	s_mov_b32 m0, s54
	s_nop 0
	global_load_lds_dwordx4 v130, s[100:101]
	s_mov_b32 m0, s55
	s_nop 0
	global_load_lds_dwordx4 v134, s[100:101]
	s_waitcnt vmcnt(8) lgkmcnt(0)
	s_barrier
	s_setprio 1
	v_mfma_f32_16x16x32_bf16 v[62:65], v[146:149], v[186:189], v[62:65]
	v_mfma_f32_16x16x32_bf16 v[58:61], v[154:157], v[186:189], v[58:61]
	v_mfma_f32_16x16x32_bf16 v[54:57], v[146:149], v[194:197], v[54:57]
	v_mfma_f32_16x16x32_bf16 v[50:53], v[154:157], v[194:197], v[50:53]
	v_mfma_f32_16x16x32_bf16 v[42:45], v[146:149], v[202:205], v[42:45]
	v_mfma_f32_16x16x32_bf16 v[34:37], v[154:157], v[202:205], v[34:37]
	v_mfma_f32_16x16x32_bf16 v[26:29], v[146:149], v[210:213], v[26:29]
	v_mfma_f32_16x16x32_bf16 v[18:21], v[154:157], v[210:213], v[18:21]
	v_mfma_f32_16x16x32_bf16 v[62:65], v[150:153], v[190:193], v[62:65]
	v_mfma_f32_16x16x32_bf16 v[58:61], v[158:161], v[190:193], v[58:61]
	v_mfma_f32_16x16x32_bf16 v[54:57], v[150:153], v[198:201], v[54:57]
	v_mfma_f32_16x16x32_bf16 v[50:53], v[158:161], v[198:201], v[50:53]
	v_mfma_f32_16x16x32_bf16 v[42:45], v[150:153], v[206:209], v[42:45]
	v_mfma_f32_16x16x32_bf16 v[34:37], v[158:161], v[206:209], v[34:37]
	v_mfma_f32_16x16x32_bf16 v[26:29], v[150:153], v[214:217], v[26:29]
	v_mfma_f32_16x16x32_bf16 v[18:21], v[158:161], v[214:217], v[18:21]
	s_setprio 0
	s_setprio 1
	v_mfma_f32_16x16x32_bf16 v[46:49], v[162:165], v[186:189], v[46:49]
	v_mfma_f32_16x16x32_bf16 v[38:41], v[178:181], v[186:189], v[38:41]
	v_mfma_f32_16x16x32_bf16 v[30:33], v[162:165], v[194:197], v[30:33]
	v_mfma_f32_16x16x32_bf16 v[22:25], v[178:181], v[194:197], v[22:25]
	v_mfma_f32_16x16x32_bf16 v[14:17], v[162:165], v[202:205], v[14:17]
	v_mfma_f32_16x16x32_bf16 v[10:13], v[178:181], v[202:205], v[10:13]
	v_mfma_f32_16x16x32_bf16 v[6:9], v[162:165], v[210:213], v[6:9]
	v_mfma_f32_16x16x32_bf16 v[2:5], v[178:181], v[210:213], v[2:5]
	v_mfma_f32_16x16x32_bf16 v[46:49], v[166:169], v[190:193], v[46:49]
	v_mfma_f32_16x16x32_bf16 v[38:41], v[182:185], v[190:193], v[38:41]
	v_mfma_f32_16x16x32_bf16 v[30:33], v[166:169], v[198:201], v[30:33]
	v_mfma_f32_16x16x32_bf16 v[22:25], v[182:185], v[198:201], v[22:25]
	v_mfma_f32_16x16x32_bf16 v[14:17], v[166:169], v[206:209], v[14:17]
	v_mfma_f32_16x16x32_bf16 v[10:13], v[182:185], v[206:209], v[10:13]
	v_mfma_f32_16x16x32_bf16 v[6:9], v[166:169], v[214:217], v[6:9]
	v_mfma_f32_16x16x32_bf16 v[2:5], v[182:185], v[214:217], v[2:5]
	s_setprio 0
	s_barrier
	s_add_u32 s65, s65, 0x100
	s_addc_u32 s66, s66, 0
	s_cmp_ge_i32 s67, s51
	s_mov_b64 s[26:27], s[28:29]
	s_mov_b32 s30, s67
	s_cbranch_scc0 .LBB0_922
	s_branch .Lpx_5

;     __device__ __forceinline__ void operator()(const f32x4 (&acc)[2][2][4][2], const Unit& u, int wr, int wc, int fr, int fq) const {
;     ...
;                 for (int m = 0; m < 4; ++m) { const size_t off = (size_t)(row0 + ai * HALF + m * 16) * ldc + col0;
; #pragma unroll
;                     for (int bj = 0; bj < 2; ++bj) { const h16x8_t w = wv[m][bj];
;                         const f32x4 b0 = (f32x4){(float)w[0], (float)w[1], (float)w[2], (float)w[3]}, b1 = (f32x4){(float)w[4], (float)w[5], (float)w[6], (float)w[7]};
;                         const f32x4 o0 = b0 + acc[ai][bj][m][0] * s, o1 = b1 + acc[ai][bj][m][1] * s;
;                         if (OB) { h16x8_t wo; wo[0] = (_Float16)o0[0]; wo[1] = (_Float16)o0[1]; wo[2] = (_Float16)o0[2]; wo[3] = (_Float16)o0[3]; wo[4] = (_Float16)o1[0]; wo[5] = (_Float16)o1[1]; wo[6] = (_Float16)o1[2]; wo[7] = (_Float16)o1[3];
;                             *(h16x8_t*)((bf16_t*)out + off + bj * HALF) = wo; }
;                         else { *(f32x4*)((float*)out + off + bj * HALF) = o0; *(f32x4*)((float*)out + off + bj * HALF + 4) = o1; } } }
.Lpx_5:
	v_pk_mul_f32 v[128:129], v[128:129], 0.5 op_sel_hi:[1,0]
	v_pk_mul_f32 v[126:127], v[126:127], 0.5 op_sel_hi:[1,0]
	v_pk_mul_f32 v[124:125], v[124:125], 0.5 op_sel_hi:[1,0]
	v_pk_mul_f32 v[122:123], v[122:123], 0.5 op_sel_hi:[1,0]
	v_pk_mul_f32 v[152:153], v[112:113], 0.5 op_sel_hi:[1,0]
	v_pk_mul_f32 v[154:155], v[110:111], 0.5 op_sel_hi:[1,0]
	v_pk_mul_f32 v[156:157], v[104:105], 0.5 op_sel_hi:[1,0]
	v_pk_mul_f32 v[158:159], v[102:103], 0.5 op_sel_hi:[1,0]
	v_pk_mul_f32 v[120:121], v[120:121], 0.5 op_sel_hi:[1,0]
	v_pk_mul_f32 v[118:119], v[118:119], 0.5 op_sel_hi:[1,0]
	v_pk_mul_f32 v[116:117], v[116:117], 0.5 op_sel_hi:[1,0]
	v_pk_mul_f32 v[114:115], v[114:115], 0.5 op_sel_hi:[1,0]
	v_pk_mul_f32 v[160:161], v[96:97], 0.5 op_sel_hi:[1,0]
	v_pk_mul_f32 v[146:147], v[94:95], 0.5 op_sel_hi:[1,0]
	v_pk_mul_f32 v[150:151], v[88:89], 0.5 op_sel_hi:[1,0]
	v_pk_mul_f32 v[148:149], v[86:87], 0.5 op_sel_hi:[1,0]
	v_pk_mul_f32 v[94:95], v[108:109], 0.5 op_sel_hi:[1,0]
	v_pk_mul_f32 v[96:97], v[106:107], 0.5 op_sel_hi:[1,0]
	v_pk_mul_f32 v[100:101], v[100:101], 0.5 op_sel_hi:[1,0]
	v_pk_mul_f32 v[98:99], v[98:99], 0.5 op_sel_hi:[1,0]
	v_pk_mul_f32 v[106:107], v[80:81], 0.5 op_sel_hi:[1,0]
	v_pk_mul_f32 v[108:109], v[78:79], 0.5 op_sel_hi:[1,0]
	v_pk_mul_f32 v[110:111], v[76:77], 0.5 op_sel_hi:[1,0]
	v_pk_mul_f32 v[112:113], v[74:75], 0.5 op_sel_hi:[1,0]
	v_pk_mul_f32 v[74:75], v[92:93], 0.5 op_sel_hi:[1,0]
	v_pk_mul_f32 v[86:87], v[90:91], 0.5 op_sel_hi:[1,0]
	v_pk_mul_f32 v[84:85], v[84:85], 0.5 op_sel_hi:[1,0]
	v_pk_mul_f32 v[88:89], v[82:83], 0.5 op_sel_hi:[1,0]
	v_pk_mul_f32 v[90:91], v[72:73], 0.5 op_sel_hi:[1,0]
	v_pk_mul_f32 v[92:93], v[70:71], 0.5 op_sel_hi:[1,0]
	v_pk_mul_f32 v[102:103], v[68:69], 0.5 op_sel_hi:[1,0]
	v_pk_mul_f32 v[104:105], v[66:67], 0.5 op_sel_hi:[1,0]
	v_pk_mul_f32 v[72:73], v[64:65], 0.5 op_sel_hi:[1,0]
	v_pk_mul_f32 v[70:71], v[62:63], 0.5 op_sel_hi:[1,0]
	v_pk_mul_f32 v[82:83], v[60:61], 0.5 op_sel_hi:[1,0]
	v_pk_mul_f32 v[80:81], v[58:59], 0.5 op_sel_hi:[1,0]
	v_pk_mul_f32 v[68:69], v[48:49], 0.5 op_sel_hi:[1,0]
	v_pk_mul_f32 v[66:67], v[46:47], 0.5 op_sel_hi:[1,0]
	v_pk_mul_f32 v[78:79], v[40:41], 0.5 op_sel_hi:[1,0]
	v_pk_mul_f32 v[76:77], v[38:39], 0.5 op_sel_hi:[1,0]
	v_pk_mul_f32 v[56:57], v[56:57], 0.5 op_sel_hi:[1,0]
	v_pk_mul_f32 v[54:55], v[54:55], 0.5 op_sel_hi:[1,0]
	v_pk_mul_f32 v[64:65], v[52:53], 0.5 op_sel_hi:[1,0]
	v_pk_mul_f32 v[62:63], v[50:51], 0.5 op_sel_hi:[1,0]
	v_pk_mul_f32 v[52:53], v[32:33], 0.5 op_sel_hi:[1,0]
	v_pk_mul_f32 v[50:51], v[30:31], 0.5 op_sel_hi:[1,0]
	v_pk_mul_f32 v[60:61], v[24:25], 0.5 op_sel_hi:[1,0]
	v_pk_mul_f32 v[58:59], v[22:23], 0.5 op_sel_hi:[1,0]
	v_pk_mul_f32 v[40:41], v[44:45], 0.5 op_sel_hi:[1,0]
	v_pk_mul_f32 v[38:39], v[42:43], 0.5 op_sel_hi:[1,0]
	v_pk_mul_f32 v[48:49], v[36:37], 0.5 op_sel_hi:[1,0]
	v_pk_mul_f32 v[46:47], v[34:35], 0.5 op_sel_hi:[1,0]
	v_pk_mul_f32 v[36:37], v[16:17], 0.5 op_sel_hi:[1,0]
	v_pk_mul_f32 v[34:35], v[14:15], 0.5 op_sel_hi:[1,0]
	v_pk_mul_f32 v[44:45], v[12:13], 0.5 op_sel_hi:[1,0]
	v_pk_mul_f32 v[42:43], v[10:11], 0.5 op_sel_hi:[1,0]
	v_pk_mul_f32 v[24:25], v[28:29], 0.5 op_sel_hi:[1,0]
	v_pk_mul_f32 v[22:23], v[26:27], 0.5 op_sel_hi:[1,0]
	v_pk_mul_f32 v[32:33], v[20:21], 0.5 op_sel_hi:[1,0]
	v_pk_mul_f32 v[30:31], v[18:19], 0.5 op_sel_hi:[1,0]
	v_pk_mul_f32 v[20:21], v[8:9], 0.5 op_sel_hi:[1,0]
	v_pk_mul_f32 v[18:19], v[6:7], 0.5 op_sel_hi:[1,0]
	v_pk_mul_f32 v[28:29], v[4:5], 0.5 op_sel_hi:[1,0]
	v_pk_mul_f32 v[26:27], v[2:3], 0.5 op_sel_hi:[1,0]

; #define PG8_STAGE(bufoff, gbase, voff) do { _Pragma("unroll") for (int _i = 0; _i < 2; ++_i) \
;         __builtin_amdgcn_global_load_lds((const unsigned*)((const char*)(gbase) + (voff)[_i]), (PG8_LAS unsigned*)(lds + (bufoff) + ldsw + _i * 8192), 16, 0, 0); } while (0)
; #define PG8_LDA(dst, b, h) do { if constexpr (DT != 1) { _Pragma("unroll") for (int m = 0; m < 4; ++m) _Pragma("unroll") for (int k = 0; k < 2; ++k) dst[m][k] = *(const PG8_LAS bf16x8*)(lds + PG8_SA(b, h) + aoff + m * 2048 + k * 1024); } \
;         else { _Pragma("unroll") for (int m = 0; m < 4; ++m) dst##8[m] = ld32(lds + PG8_SA(b, h) + aoff + m * 2048); } } while (0)
; #define PG8_LDB(dst, b, h) do { if constexpr (DT != 1) { _Pragma("unroll") for (int n = 0; n < 2; ++n) _Pragma("unroll") for (int k = 0; k < 2; ++k) dst[n][k] = *(const PG8_LAS bf16x8*)(lds + PG8_SB(b, h) + boff + n * 2048 + k * 1024); } \
;         else { _Pragma("unroll") for (int n = 0; n < 2; ++n) dst##8[n] = ld32(lds + PG8_SB(b, h) + boff + n * 2048); } } while (0)
; #define PG8_WAIT_V(n) asm volatile("s_waitcnt vmcnt(" #n ")" ::: "memory")
; #define PG8_WAIT_L(n) asm volatile("s_waitcnt lgkmcnt(" #n ")" ::: "memory")
; #define PG8_BAR __builtin_amdgcn_s_barrier()
; #define PG8_SCHED __builtin_amdgcn_sched_barrier(0)
;     ...
;         for (int t = 0; t < nt; t += 2) {
;             const bool last = (t == nt - 2);
;             const char* a1 = cA + (size_t)(t + 1) * kstep;
;             const char* a2 = last ? nA : cA + (size_t)(t + 2) * kstep; const char* b2 = last ? nB : cB + (size_t)(t + 2) * kstep;
;             const char* a3 = a2 + kstep; const char* b3 = b2 + kstep;
;             if (last && has_next) S.a_ready(nxt);
;             if constexpr (SP2) {
;             PG8_LDB(B0, 0, 0); PG8_LDB(B1, 0, 1); PG8_SCHED; PG8_LDA(At, 0, 0); PG8_STAGE(PG8_SA(1, 1), a1 + hstepA, voffA);
;             PG8_WAIT_V(8); PG8_WAIT_L(0); PG8_BAR; PG8_MMA(0, 0, At, B0); PG8_MMA(0, 1, At, B1); PG8_BAR; PG8_SCHED;
;             PG8_LDA(At, 0, 1); PG8_STAGE(PG8_SB(0, 0), b2, voffB); PG8_STAGE(PG8_SB(0, 1), b2 + hstepB, voffB); PG8_STAGE(PG8_SA(0, 0), a2, voffA);
;             PG8_WAIT_V(8); PG8_WAIT_L(0); PG8_BAR; PG8_MMA(1, 0, At, B0); PG8_MMA(1, 1, At, B1); PG8_BAR; PG8_SCHED;
.Lzt_4:
	s_cbranch_vccnz .LBB0_1414
	s_and_b64 s[28:29], s[0:1], exec
	s_cselect_b32 s15, s19, s27
	s_cselect_b32 s17, s18, s26
	s_cselect_b32 s64, s21, s25
	s_cselect_b32 s65, s20, s24
	s_add_u32 s66, s24, 0x100
	s_addc_u32 s67, s25, 0
	s_add_u32 s24, s26, 0x40080
	s_addc_u32 s25, s27, 0
	s_mov_b32 s26, 0
	v_add_u32_e32 v162, s35, v168
	v_add_u32_e32 v166, s36, v168
	ds_read_b128 v[150:153], v162
	ds_read_b128 v[154:157], v162 offset:1024
	ds_read_b128 v[158:161], v162 offset:2048
	ds_read_b128 v[162:165], v162 offset:3072
	ds_read_b128 v[178:181], v166
	ds_read_b128 v[182:185], v166 offset:1024
	ds_read_b128 v[186:189], v166 offset:2048
	ds_read_b128 v[190:193], v166 offset:3072
	s_add_i32 s68, s26, 2
	s_add_u32 s27, s24, 0xfffc0080
	s_addc_u32 s28, s25, -1
	s_cmp_eq_u32 s61, s26
	s_cselect_b32 s26, s65, s66
	s_cselect_b32 s29, s15, s28
	s_cselect_b32 s28, s17, s27
	s_cselect_b32 s27, s64, s67
	s_add_i32 m0, s46, 0xc000
	ds_read_b128 v[194:197], v177
	ds_read_b128 v[198:201], v177 offset:1024
	ds_read_b128 v[202:205], v177 offset:2048
	ds_read_b128 v[206:209], v177 offset:3072
	ds_read_b128 v[210:213], v177 offset:4096
	ds_read_b128 v[214:217], v177 offset:5120
	ds_read_b128 v[218:221], v177 offset:6144
	ds_read_b128 v[222:225], v177 offset:7168
	global_load_lds_dwordx4 v144, s[24:25]
	s_add_i32 m0, s46, 0xe000
	s_nop 0
	global_load_lds_dwordx4 v142, s[24:25]
	s_waitcnt vmcnt(8) lgkmcnt(0)
	s_barrier
	s_setprio 1
	v_mfma_i32_16x16x64_i8 v[126:129], v[150:153], v[194:197], 0
	v_mfma_i32_16x16x64_i8 v[122:125], v[158:161], v[194:197], 0
	v_mfma_i32_16x16x64_i8 v[118:121], v[150:153], v[202:205], 0
	v_mfma_i32_16x16x64_i8 v[114:117], v[158:161], v[202:205], 0
	v_mfma_i32_16x16x64_i8 v[106:109], v[150:153], v[210:213], 0
	v_mfma_i32_16x16x64_i8 v[98:101], v[158:161], v[210:213], 0
	v_mfma_i32_16x16x64_i8 v[90:93], v[150:153], v[218:221], 0
	v_mfma_i32_16x16x64_i8 v[82:85], v[158:161], v[218:221], 0
	v_mfma_i32_16x16x64_i8 v[126:129], v[154:157], v[198:201], v[126:129]
	v_mfma_i32_16x16x64_i8 v[122:125], v[162:165], v[198:201], v[122:125]
	v_mfma_i32_16x16x64_i8 v[118:121], v[154:157], v[206:209], v[118:121]
	v_mfma_i32_16x16x64_i8 v[114:117], v[162:165], v[206:209], v[114:117]
	v_mfma_i32_16x16x64_i8 v[106:109], v[154:157], v[214:217], v[106:109]
	v_mfma_i32_16x16x64_i8 v[98:101], v[162:165], v[214:217], v[98:101]
	v_mfma_i32_16x16x64_i8 v[90:93], v[154:157], v[222:225], v[90:93]
	v_mfma_i32_16x16x64_i8 v[82:85], v[162:165], v[222:225], v[82:85]
	s_setprio 0
	s_setprio 1
	v_mfma_i32_16x16x64_i8 v[110:113], v[178:181], v[194:197], 0
	v_mfma_i32_16x16x64_i8 v[102:105], v[186:189], v[194:197], 0
	v_mfma_i32_16x16x64_i8 v[94:97], v[178:181], v[202:205], 0
	v_mfma_i32_16x16x64_i8 v[86:89], v[186:189], v[202:205], 0
	v_mfma_i32_16x16x64_i8 v[78:81], v[178:181], v[210:213], 0
	v_mfma_i32_16x16x64_i8 v[74:77], v[186:189], v[210:213], 0
	v_mfma_i32_16x16x64_i8 v[70:73], v[178:181], v[218:221], 0
	v_mfma_i32_16x16x64_i8 v[66:69], v[186:189], v[218:221], 0
	v_mfma_i32_16x16x64_i8 v[110:113], v[182:185], v[198:201], v[110:113]
	v_mfma_i32_16x16x64_i8 v[102:105], v[190:193], v[198:201], v[102:105]
	v_mfma_i32_16x16x64_i8 v[94:97], v[182:185], v[206:209], v[94:97]
	v_mfma_i32_16x16x64_i8 v[86:89], v[190:193], v[206:209], v[86:89]
	v_mfma_i32_16x16x64_i8 v[78:81], v[182:185], v[214:217], v[78:81]
	v_mfma_i32_16x16x64_i8 v[74:77], v[190:193], v[214:217], v[74:77]
	v_mfma_i32_16x16x64_i8 v[70:73], v[182:185], v[222:225], v[70:73]
	v_mfma_i32_16x16x64_i8 v[66:69], v[190:193], v[222:225], v[66:69]
	s_setprio 0
	s_barrier
	s_mov_b32 m0, s23
	s_add_u32 s98, s26, 0x80
	s_addc_u32 s99, s27, 0
	s_add_u32 s70, s26, 0x40000
	ds_read_b128 v[194:197], v177 offset:16384
	ds_read_b128 v[198:201], v177 offset:17408
	ds_read_b128 v[202:205], v177 offset:18432
	ds_read_b128 v[206:209], v177 offset:19456
	ds_read_b128 v[210:213], v177 offset:20480
	ds_read_b128 v[214:217], v177 offset:21504
	ds_read_b128 v[218:221], v177 offset:22528
	ds_read_b128 v[222:225], v177 offset:23552
	global_load_lds_dwordx4 v132, s[26:27]
	s_mov_b32 m0, s43
	s_addc_u32 s71, s27, 0
	global_load_lds_dwordx4 v136, s[26:27]
	s_mov_b32 m0, s44
	s_nop 0
	global_load_lds_dwordx4 v132, s[70:71]
	s_mov_b32 m0, s45
	s_nop 0
	global_load_lds_dwordx4 v136, s[70:71]
	s_add_u32 s100, s28, 0x80
	s_addc_u32 s101, s29, 0
	s_mov_b32 m0, s46
	s_nop 0
	global_load_lds_dwordx4 v130, s[28:29]
	s_mov_b32 m0, s47
	s_nop 0
	global_load_lds_dwordx4 v134, s[28:29]
	s_waitcnt vmcnt(8) lgkmcnt(0)
	s_barrier
	s_setprio 1
	v_mfma_i32_16x16x64_i8 v[62:65], v[150:153], v[194:197], 0
	v_mfma_i32_16x16x64_i8 v[58:61], v[158:161], v[194:197], 0
	v_mfma_i32_16x16x64_i8 v[54:57], v[150:153], v[202:205], 0
	v_mfma_i32_16x16x64_i8 v[50:53], v[158:161], v[202:205], 0
	v_mfma_i32_16x16x64_i8 v[42:45], v[150:153], v[210:213], 0
	v_mfma_i32_16x16x64_i8 v[34:37], v[158:161], v[210:213], 0
	v_mfma_i32_16x16x64_i8 v[26:29], v[150:153], v[218:221], 0
	v_mfma_i32_16x16x64_i8 v[18:21], v[158:161], v[218:221], 0
	v_mfma_i32_16x16x64_i8 v[62:65], v[154:157], v[198:201], v[62:65]
	v_mfma_i32_16x16x64_i8 v[58:61], v[162:165], v[198:201], v[58:61]
	v_mfma_i32_16x16x64_i8 v[54:57], v[154:157], v[206:209], v[54:57]
	v_mfma_i32_16x16x64_i8 v[50:53], v[162:165], v[206:209], v[50:53]
	v_mfma_i32_16x16x64_i8 v[42:45], v[154:157], v[214:217], v[42:45]
	v_mfma_i32_16x16x64_i8 v[34:37], v[162:165], v[214:217], v[34:37]
	v_mfma_i32_16x16x64_i8 v[26:29], v[154:157], v[222:225], v[26:29]
	v_mfma_i32_16x16x64_i8 v[18:21], v[162:165], v[222:225], v[18:21]
	s_setprio 0
	s_setprio 1
	v_mfma_i32_16x16x64_i8 v[46:49], v[178:181], v[194:197], 0
	v_mfma_i32_16x16x64_i8 v[38:41], v[186:189], v[194:197], 0
	v_mfma_i32_16x16x64_i8 v[30:33], v[178:181], v[202:205], 0
	v_mfma_i32_16x16x64_i8 v[22:25], v[186:189], v[202:205], 0
	v_mfma_i32_16x16x64_i8 v[14:17], v[178:181], v[210:213], 0
	v_mfma_i32_16x16x64_i8 v[10:13], v[186:189], v[210:213], 0
	v_mfma_i32_16x16x64_i8 v[6:9], v[178:181], v[218:221], 0
	v_mfma_i32_16x16x64_i8 v[2:5], v[186:189], v[218:221], 0
	v_mfma_i32_16x16x64_i8 v[46:49], v[182:185], v[198:201], v[46:49]
	v_mfma_i32_16x16x64_i8 v[38:41], v[190:193], v[198:201], v[38:41]
	v_mfma_i32_16x16x64_i8 v[30:33], v[182:185], v[206:209], v[30:33]
	v_mfma_i32_16x16x64_i8 v[22:25], v[190:193], v[206:209], v[22:25]
	v_mfma_i32_16x16x64_i8 v[14:17], v[182:185], v[214:217], v[14:17]
	v_mfma_i32_16x16x64_i8 v[10:13], v[190:193], v[214:217], v[10:13]
	v_mfma_i32_16x16x64_i8 v[6:9], v[182:185], v[222:225], v[6:9]
	v_mfma_i32_16x16x64_i8 v[2:5], v[190:193], v[222:225], v[2:5]
	s_setprio 0
	s_barrier
; #define PG8_STAGE(bufoff, gbase, voff) do { _Pragma("unroll") for (int _i = 0; _i < 2; ++_i) \
;         __builtin_amdgcn_global_load_lds((const unsigned*)((const char*)(gbase) + (voff)[_i]), (PG8_LAS unsigned*)(lds + (bufoff) + ldsw + _i * 8192), 16, 0, 0); } while (0)
; #define PG8_LDA(dst, b, h) do { if constexpr (DT != 1) { _Pragma("unroll") for (int m = 0; m < 4; ++m) _Pragma("unroll") for (int k = 0; k < 2; ++k) dst[m][k] = *(const PG8_LAS bf16x8*)(lds + PG8_SA(b, h) + aoff + m * 2048 + k * 1024); } \
;         else { _Pragma("unroll") for (int m = 0; m < 4; ++m) dst##8[m] = ld32(lds + PG8_SA(b, h) + aoff + m * 2048); } } while (0)
; #define PG8_LDB(dst, b, h) do { if constexpr (DT != 1) { _Pragma("unroll") for (int n = 0; n < 2; ++n) _Pragma("unroll") for (int k = 0; k < 2; ++k) dst[n][k] = *(const PG8_LAS bf16x8*)(lds + PG8_SB(b, h) + boff + n * 2048 + k * 1024); } \
;         else { _Pragma("unroll") for (int n = 0; n < 2; ++n) dst##8[n] = ld32(lds + PG8_SB(b, h) + boff + n * 2048); } } while (0)
; #define PG8_WAIT_V(n) asm volatile("s_waitcnt vmcnt(" #n ")" ::: "memory")
; #define PG8_WAIT_L(n) asm volatile("s_waitcnt lgkmcnt(" #n ")" ::: "memory")
; #define PG8_BAR __builtin_amdgcn_s_barrier()
; #define PG8_SCHED __builtin_amdgcn_sched_barrier(0)
;     ...
;             PG8_LDB(B0, 1, 0); PG8_LDB(B1, 1, 1); PG8_SCHED; PG8_LDA(At, 1, 0); PG8_STAGE(PG8_SA(0, 1), a2 + hstepA, voffA);
;             PG8_WAIT_V(8); PG8_WAIT_L(0); PG8_BAR; PG8_MMA(0, 0, At, B0); PG8_MMA(0, 1, At, B1); PG8_BAR; PG8_SCHED;
;             PG8_LDA(At, 1, 1); PG8_STAGE(PG8_SB(1, 0), b3, voffB); PG8_STAGE(PG8_SB(1, 1), b3 + hstepB, voffB); PG8_STAGE(PG8_SA(1, 0), a3, voffA);
;             PG8_WAIT_V(8); PG8_WAIT_L(0); PG8_BAR; PG8_MMA(1, 0, At, B0); PG8_MMA(1, 1, At, B1); PG8_BAR; PG8_SCHED;
	v_add_u32_e32 v162, s51, v168
	v_add_u32_e32 v190, s52, v168
	ds_read_b128 v[150:153], v162
	ds_read_b128 v[154:157], v162 offset:1024
	ds_read_b128 v[158:161], v162 offset:2048
	ds_read_b128 v[162:165], v162 offset:3072
	ds_read_b128 v[178:181], v190
	ds_read_b128 v[182:185], v190 offset:1024
	ds_read_b128 v[186:189], v190 offset:2048
	ds_read_b128 v[190:193], v190 offset:3072
	s_add_u32 s28, s28, 0x40000
	s_addc_u32 s29, s29, 0
	s_mov_b32 m0, s48
	ds_read_b128 v[194:197], v177 offset:32768
	ds_read_b128 v[198:201], v177 offset:33792
	ds_read_b128 v[202:205], v177 offset:34816
	ds_read_b128 v[206:209], v177 offset:35840
	ds_read_b128 v[210:213], v177 offset:36864
	ds_read_b128 v[214:217], v177 offset:37888
	ds_read_b128 v[218:221], v177 offset:38912
	ds_read_b128 v[222:225], v177 offset:39936
	global_load_lds_dwordx4 v130, s[28:29]
	s_mov_b32 m0, s49
	s_nop 0
	global_load_lds_dwordx4 v134, s[28:29]
	s_waitcnt vmcnt(8) lgkmcnt(0)
	s_barrier
	s_setprio 1
	v_mfma_i32_16x16x64_i8 v[126:129], v[150:153], v[194:197], v[126:129]
	v_mfma_i32_16x16x64_i8 v[122:125], v[158:161], v[194:197], v[122:125]
	v_mfma_i32_16x16x64_i8 v[118:121], v[150:153], v[202:205], v[118:121]
	v_mfma_i32_16x16x64_i8 v[114:117], v[158:161], v[202:205], v[114:117]
	v_mfma_i32_16x16x64_i8 v[106:109], v[150:153], v[210:213], v[106:109]
	v_mfma_i32_16x16x64_i8 v[98:101], v[158:161], v[210:213], v[98:101]
	v_mfma_i32_16x16x64_i8 v[90:93], v[150:153], v[218:221], v[90:93]
	v_mfma_i32_16x16x64_i8 v[82:85], v[158:161], v[218:221], v[82:85]
	v_mfma_i32_16x16x64_i8 v[126:129], v[154:157], v[198:201], v[126:129]
	v_mfma_i32_16x16x64_i8 v[122:125], v[162:165], v[198:201], v[122:125]
	v_mfma_i32_16x16x64_i8 v[118:121], v[154:157], v[206:209], v[118:121]
	v_mfma_i32_16x16x64_i8 v[114:117], v[162:165], v[206:209], v[114:117]
	v_mfma_i32_16x16x64_i8 v[106:109], v[154:157], v[214:217], v[106:109]
	v_mfma_i32_16x16x64_i8 v[98:101], v[162:165], v[214:217], v[98:101]
	v_mfma_i32_16x16x64_i8 v[90:93], v[154:157], v[222:225], v[90:93]
	v_mfma_i32_16x16x64_i8 v[82:85], v[162:165], v[222:225], v[82:85]
	s_setprio 0
	s_setprio 1
	v_mfma_i32_16x16x64_i8 v[110:113], v[178:181], v[194:197], v[110:113]
	v_mfma_i32_16x16x64_i8 v[102:105], v[186:189], v[194:197], v[102:105]
	v_mfma_i32_16x16x64_i8 v[94:97], v[178:181], v[202:205], v[94:97]
	v_mfma_i32_16x16x64_i8 v[86:89], v[186:189], v[202:205], v[86:89]
	v_mfma_i32_16x16x64_i8 v[78:81], v[178:181], v[210:213], v[78:81]
	v_mfma_i32_16x16x64_i8 v[74:77], v[186:189], v[210:213], v[74:77]
	v_mfma_i32_16x16x64_i8 v[70:73], v[178:181], v[218:221], v[70:73]
	v_mfma_i32_16x16x64_i8 v[66:69], v[186:189], v[218:221], v[66:69]
	v_mfma_i32_16x16x64_i8 v[110:113], v[182:185], v[198:201], v[110:113]
	v_mfma_i32_16x16x64_i8 v[102:105], v[190:193], v[198:201], v[102:105]
	v_mfma_i32_16x16x64_i8 v[94:97], v[182:185], v[206:209], v[94:97]
	v_mfma_i32_16x16x64_i8 v[86:89], v[190:193], v[206:209], v[86:89]
	v_mfma_i32_16x16x64_i8 v[78:81], v[182:185], v[214:217], v[78:81]
	v_mfma_i32_16x16x64_i8 v[74:77], v[190:193], v[214:217], v[74:77]
	v_mfma_i32_16x16x64_i8 v[70:73], v[182:185], v[222:225], v[70:73]
	v_mfma_i32_16x16x64_i8 v[66:69], v[190:193], v[222:225], v[66:69]
	s_setprio 0
	s_barrier
	s_mov_b32 m0, s55
	s_add_u32 s26, s26, 0x40080
	ds_read_b128 v[194:197], v177 offset:49152
	ds_read_b128 v[198:201], v177 offset:50176
	ds_read_b128 v[202:205], v177 offset:51200
	ds_read_b128 v[206:209], v177 offset:52224
	ds_read_b128 v[210:213], v177 offset:53248
	ds_read_b128 v[214:217], v177 offset:54272
	ds_read_b128 v[218:221], v177 offset:55296
	ds_read_b128 v[222:225], v177 offset:56320
	global_load_lds_dwordx4 v132, s[98:99]
	s_mov_b32 m0, s56
	s_addc_u32 s27, s27, 0
	global_load_lds_dwordx4 v136, s[98:99]
	s_mov_b32 m0, s59
	s_nop 0
	global_load_lds_dwordx4 v132, s[26:27]
	s_mov_b32 m0, s60
	s_nop 0
	global_load_lds_dwordx4 v136, s[26:27]
	s_mov_b32 m0, s57
	s_nop 0
	global_load_lds_dwordx4 v130, s[100:101]
	s_mov_b32 m0, s58
	s_nop 0
	global_load_lds_dwordx4 v134, s[100:101]
	s_waitcnt vmcnt(8) lgkmcnt(0)
	s_barrier
	s_setprio 1
	v_mfma_i32_16x16x64_i8 v[62:65], v[150:153], v[194:197], v[62:65]
	v_mfma_i32_16x16x64_i8 v[58:61], v[158:161], v[194:197], v[58:61]
	v_mfma_i32_16x16x64_i8 v[54:57], v[150:153], v[202:205], v[54:57]
	v_mfma_i32_16x16x64_i8 v[50:53], v[158:161], v[202:205], v[50:53]
	v_mfma_i32_16x16x64_i8 v[42:45], v[150:153], v[210:213], v[42:45]
	v_mfma_i32_16x16x64_i8 v[34:37], v[158:161], v[210:213], v[34:37]
	v_mfma_i32_16x16x64_i8 v[26:29], v[150:153], v[218:221], v[26:29]
	v_mfma_i32_16x16x64_i8 v[18:21], v[158:161], v[218:221], v[18:21]
	v_mfma_i32_16x16x64_i8 v[62:65], v[154:157], v[198:201], v[62:65]
	v_mfma_i32_16x16x64_i8 v[58:61], v[162:165], v[198:201], v[58:61]
	v_mfma_i32_16x16x64_i8 v[54:57], v[154:157], v[206:209], v[54:57]
	v_mfma_i32_16x16x64_i8 v[50:53], v[162:165], v[206:209], v[50:53]
	v_mfma_i32_16x16x64_i8 v[42:45], v[154:157], v[214:217], v[42:45]
	v_mfma_i32_16x16x64_i8 v[34:37], v[162:165], v[214:217], v[34:37]
	v_mfma_i32_16x16x64_i8 v[26:29], v[154:157], v[222:225], v[26:29]
	v_mfma_i32_16x16x64_i8 v[18:21], v[162:165], v[222:225], v[18:21]
	s_setprio 0
	s_setprio 1
	v_mfma_i32_16x16x64_i8 v[46:49], v[178:181], v[194:197], v[46:49]
	v_mfma_i32_16x16x64_i8 v[38:41], v[186:189], v[194:197], v[38:41]
	v_mfma_i32_16x16x64_i8 v[30:33], v[178:181], v[202:205], v[30:33]
	v_mfma_i32_16x16x64_i8 v[22:25], v[186:189], v[202:205], v[22:25]
	v_mfma_i32_16x16x64_i8 v[14:17], v[178:181], v[210:213], v[14:17]
	v_mfma_i32_16x16x64_i8 v[10:13], v[186:189], v[210:213], v[10:13]
	v_mfma_i32_16x16x64_i8 v[6:9], v[178:181], v[218:221], v[6:9]
	v_mfma_i32_16x16x64_i8 v[2:5], v[186:189], v[218:221], v[2:5]
	v_mfma_i32_16x16x64_i8 v[46:49], v[182:185], v[198:201], v[46:49]
	v_mfma_i32_16x16x64_i8 v[38:41], v[190:193], v[198:201], v[38:41]
	v_mfma_i32_16x16x64_i8 v[30:33], v[182:185], v[206:209], v[30:33]
	v_mfma_i32_16x16x64_i8 v[22:25], v[190:193], v[206:209], v[22:25]
	v_mfma_i32_16x16x64_i8 v[14:17], v[182:185], v[214:217], v[14:17]
	v_mfma_i32_16x16x64_i8 v[10:13], v[190:193], v[214:217], v[10:13]
	v_mfma_i32_16x16x64_i8 v[6:9], v[182:185], v[222:225], v[6:9]
	v_mfma_i32_16x16x64_i8 v[2:5], v[190:193], v[222:225], v[2:5]
	s_setprio 0
	s_barrier
	s_add_u32 s66, s66, 0x100
	s_addc_u32 s67, s67, 0
	s_add_u32 s24, s24, 0x100
	s_addc_u32 s25, s25, 0
	s_cmp_ge_i32 s68, s54
	s_mov_b32 s26, s68
	s_cbranch_scc0 .LBB0_1412
	s_branch .Lpx_8

; __device__ __forceinline__ f32x4 i32bits_to_f32(f32x4 v) { return (f32x4){(float)__float_as_int(v.x), (float)__float_as_int(v.y), (float)__float_as_int(v.z), (float)__float_as_int(v.w)}; }
;     __device__ __forceinline__ void operator()(const f32x4 (&acc)[2][2][4][2], const Unit& u, int wr, int wc, int fr, int fq) const {
;     ...
;                 for (int bj = 0; bj < 2; ++bj) { f32x4 v0 = acc[ai][bj][m][0], v1 = acc[ai][bj][m][1];
;                     if (IN8) { v0 = i32bits_to_f32(v0) * cs[bj][0] * rs; v1 = i32bits_to_f32(v1) * cs[bj][1] * rs; }
.Lpx_8:
	v_cvt_f32_i32_e32 v150, v126
	v_cvt_f32_i32_e32 v151, v127
	v_cvt_f32_i32_e32 v126, v128
	v_cvt_f32_i32_e32 v127, v129
	v_cvt_f32_i32_e32 v122, v122
	v_cvt_f32_i32_e32 v123, v123
	v_cvt_f32_i32_e32 v124, v124
	v_cvt_f32_i32_e32 v125, v125
	v_cvt_f32_i32_e32 v158, v110
	v_cvt_f32_i32_e32 v159, v111
	v_cvt_f32_i32_e32 v160, v112
	v_cvt_f32_i32_e32 v161, v113
	v_cvt_f32_i32_e32 v162, v102
	v_cvt_f32_i32_e32 v163, v103
	v_cvt_f32_i32_e32 v164, v104
	v_cvt_f32_i32_e32 v165, v105
	v_cvt_f32_i32_e32 v152, v118
	v_cvt_f32_i32_e32 v153, v119
	v_cvt_f32_i32_e32 v154, v120
	v_cvt_f32_i32_e32 v155, v121
	v_cvt_f32_i32_e32 v128, v114
	v_cvt_f32_i32_e32 v129, v115
	v_cvt_f32_i32_e32 v156, v116
	v_cvt_f32_i32_e32 v157, v117
	v_cvt_f32_i32_e32 v116, v94
	v_cvt_f32_i32_e32 v117, v95
	v_cvt_f32_i32_e32 v120, v96
	v_cvt_f32_i32_e32 v121, v97
	v_cvt_f32_i32_e32 v114, v86
	v_cvt_f32_i32_e32 v115, v87
	v_cvt_f32_i32_e32 v118, v88
	v_cvt_f32_i32_e32 v119, v89
	v_cvt_f32_i32_e32 v102, v106
	v_cvt_f32_i32_e32 v103, v107
	v_cvt_f32_i32_e32 v104, v108
	v_cvt_f32_i32_e32 v105, v109
	v_cvt_f32_i32_e32 v98, v98
	v_cvt_f32_i32_e32 v99, v99
	v_cvt_f32_i32_e32 v100, v100
	v_cvt_f32_i32_e32 v101, v101
	v_cvt_f32_i32_e32 v108, v78
	v_cvt_f32_i32_e32 v109, v79
	v_cvt_f32_i32_e32 v112, v80
	v_cvt_f32_i32_e32 v113, v81
	v_cvt_f32_i32_e32 v106, v74
	v_cvt_f32_i32_e32 v107, v75
	v_cvt_f32_i32_e32 v110, v76
	v_cvt_f32_i32_e32 v111, v77
	v_cvt_f32_i32_e32 v76, v90
	v_cvt_f32_i32_e32 v77, v91
	v_cvt_f32_i32_e32 v80, v92
	v_cvt_f32_i32_e32 v81, v93
	v_cvt_f32_i32_e32 v74, v82
	v_cvt_f32_i32_e32 v75, v83
	v_cvt_f32_i32_e32 v78, v84
	v_cvt_f32_i32_e32 v79, v85
	v_cvt_f32_i32_e32 v92, v70
	v_cvt_f32_i32_e32 v93, v71
	v_cvt_f32_i32_e32 v96, v72
	v_cvt_f32_i32_e32 v97, v73
	v_cvt_f32_i32_e32 v90, v66
	v_cvt_f32_i32_e32 v91, v67
	v_cvt_f32_i32_e32 v94, v68
	v_cvt_f32_i32_e32 v95, v69
	v_cvt_f32_i32_e32 v68, v62
	v_cvt_f32_i32_e32 v69, v63
	v_cvt_f32_i32_e32 v72, v64
	v_cvt_f32_i32_e32 v73, v65
	v_cvt_f32_i32_e32 v66, v58
	v_cvt_f32_i32_e32 v67, v59
	v_cvt_f32_i32_e32 v70, v60
	v_cvt_f32_i32_e32 v71, v61
	v_cvt_f32_i32_e32 v84, v46
	v_cvt_f32_i32_e32 v85, v47
	v_cvt_f32_i32_e32 v88, v48
	v_cvt_f32_i32_e32 v89, v49
	v_cvt_f32_i32_e32 v82, v38
	v_cvt_f32_i32_e32 v83, v39
	v_cvt_f32_i32_e32 v86, v40
	v_cvt_f32_i32_e32 v87, v41
	v_cvt_f32_i32_e32 v54, v54
	v_cvt_f32_i32_e32 v55, v55
	v_cvt_f32_i32_e32 v56, v56
	v_cvt_f32_i32_e32 v57, v57
	v_cvt_f32_i32_e32 v50, v50
	v_cvt_f32_i32_e32 v51, v51
	v_cvt_f32_i32_e32 v52, v52
	v_cvt_f32_i32_e32 v53, v53
	v_cvt_f32_i32_e32 v60, v30
	v_cvt_f32_i32_e32 v61, v31
	v_cvt_f32_i32_e32 v64, v32
	v_cvt_f32_i32_e32 v65, v33
	v_cvt_f32_i32_e32 v58, v22
	v_cvt_f32_i32_e32 v59, v23
	v_cvt_f32_i32_e32 v62, v24
	v_cvt_f32_i32_e32 v63, v25
	v_cvt_f32_i32_e32 v38, v42
	v_cvt_f32_i32_e32 v39, v43
	v_cvt_f32_i32_e32 v40, v44
	v_cvt_f32_i32_e32 v41, v45
	v_cvt_f32_i32_e32 v34, v34
	v_cvt_f32_i32_e32 v35, v35
	v_cvt_f32_i32_e32 v36, v36
	v_cvt_f32_i32_e32 v37, v37
	v_cvt_f32_i32_e32 v44, v14
	v_cvt_f32_i32_e32 v45, v15
	v_cvt_f32_i32_e32 v48, v16
	v_cvt_f32_i32_e32 v49, v17
	v_cvt_f32_i32_e32 v42, v10
	v_cvt_f32_i32_e32 v43, v11
	v_cvt_f32_i32_e32 v46, v12
	v_cvt_f32_i32_e32 v47, v13
	v_cvt_f32_i32_e32 v22, v26
	v_cvt_f32_i32_e32 v23, v27
	v_cvt_f32_i32_e32 v24, v28
	v_cvt_f32_i32_e32 v25, v29
	v_cvt_f32_i32_e32 v18, v18
	v_cvt_f32_i32_e32 v19, v19
	v_cvt_f32_i32_e32 v20, v20
	v_cvt_f32_i32_e32 v21, v21
	v_cvt_f32_i32_e32 v28, v6
	v_cvt_f32_i32_e32 v29, v7
	v_cvt_f32_i32_e32 v32, v8
	v_cvt_f32_i32_e32 v33, v9
	v_cvt_f32_i32_e32 v26, v2
	v_cvt_f32_i32_e32 v27, v3
	v_cvt_f32_i32_e32 v30, v4
	v_cvt_f32_i32_e32 v31, v5

; #define PG8_STAGE(bufoff, gbase, voff) do { _Pragma("unroll") for (int _i = 0; _i < 2; ++_i) \
;         __builtin_amdgcn_global_load_lds((const unsigned*)((const char*)(gbase) + (voff)[_i]), (PG8_LAS unsigned*)(lds + (bufoff) + ldsw + _i * 8192), 16, 0, 0); } while (0)
; #define PG8_LDA(dst, b, h) do { if constexpr (DT != 1) { _Pragma("unroll") for (int m = 0; m < 4; ++m) _Pragma("unroll") for (int k = 0; k < 2; ++k) dst[m][k] = *(const PG8_LAS bf16x8*)(lds + PG8_SA(b, h) + aoff + m * 2048 + k * 1024); } \
;         else { _Pragma("unroll") for (int m = 0; m < 4; ++m) dst##8[m] = ld32(lds + PG8_SA(b, h) + aoff + m * 2048); } } while (0)
; #define PG8_LDB(dst, b, h) do { if constexpr (DT != 1) { _Pragma("unroll") for (int n = 0; n < 2; ++n) _Pragma("unroll") for (int k = 0; k < 2; ++k) dst[n][k] = *(const PG8_LAS bf16x8*)(lds + PG8_SB(b, h) + boff + n * 2048 + k * 1024); } \
;         else { _Pragma("unroll") for (int n = 0; n < 2; ++n) dst##8[n] = ld32(lds + PG8_SB(b, h) + boff + n * 2048); } } while (0)
; #define PG8_WAIT_V(n) asm volatile("s_waitcnt vmcnt(" #n ")" ::: "memory")
; #define PG8_WAIT_L(n) asm volatile("s_waitcnt lgkmcnt(" #n ")" ::: "memory")
; #define PG8_BAR __builtin_amdgcn_s_barrier()
; #define PG8_SCHED __builtin_amdgcn_sched_barrier(0)
;     ...
;         for (int t = 0; t < nt; t += 2) {
;             const bool last = (t == nt - 2);
;             const char* a1 = cA + (size_t)(t + 1) * kstep;
;             const char* a2 = last ? nA : cA + (size_t)(t + 2) * kstep; const char* b2 = last ? nB : cB + (size_t)(t + 2) * kstep;
;             const char* a3 = a2 + kstep; const char* b3 = b2 + kstep;
;             if (last && has_next) S.a_ready(nxt);
;             if constexpr (SP2) {
;             PG8_LDB(B0, 0, 0); PG8_LDB(B1, 0, 1); PG8_SCHED; PG8_LDA(At, 0, 0); PG8_STAGE(PG8_SA(1, 1), a1 + hstepA, voffA);
;             PG8_WAIT_V(8); PG8_WAIT_L(0); PG8_BAR; PG8_MMA(0, 0, At, B0); PG8_MMA(0, 1, At, B1); PG8_BAR; PG8_SCHED;
;             PG8_LDA(At, 0, 1); PG8_STAGE(PG8_SB(0, 0), b2, voffB); PG8_STAGE(PG8_SB(0, 1), b2 + hstepB, voffB); PG8_STAGE(PG8_SA(0, 0), a2, voffA);
;             PG8_WAIT_V(8); PG8_WAIT_L(0); PG8_BAR; PG8_MMA(1, 0, At, B0); PG8_MMA(1, 1, At, B1); PG8_BAR; PG8_SCHED;
.Lzs_9:
	s_cbranch_vccnz .LBB0_2263
	s_and_b64 s[30:31], s[4:5], exec
	s_cselect_b32 s2, s19, s29
	s_cselect_b32 s15, s18, s28
	s_cselect_b32 s17, s21, s27
	s_cselect_b32 s23, s20, s26
	s_add_u32 s25, s26, 0x100
	s_addc_u32 s64, s27, 0
	s_add_u32 s26, s28, 0x80080
	s_addc_u32 s27, s29, 0
	s_mov_b32 s28, 0
	ds_read_b128 v[154:157], v148
	ds_read_b128 v[158:161], v148 offset:1024
	ds_read_b128 v[162:165], v148 offset:2048
	ds_read_b128 v[166:169], v148 offset:3072
	ds_read_b128 v[170:173], v149
	ds_read_b128 v[174:177], v149 offset:1024
	ds_read_b128 v[178:181], v149 offset:2048
	ds_read_b128 v[182:185], v149 offset:3072
	s_add_i32 s65, s28, 2
	s_add_u32 s29, s26, 0xfff80080
	s_addc_u32 s30, s27, -1
	s_cmp_eq_u32 s61, s28
	s_cselect_b32 s28, s23, s25
	s_cselect_b32 s31, s2, s30
	s_cselect_b32 s30, s15, s29
	s_cselect_b32 s29, s17, s64
	s_add_i32 m0, s44, 0xc000
	ds_read_b128 v[186:189], v150
	ds_read_b128 v[190:193], v150 offset:1024
	ds_read_b128 v[194:197], v150 offset:2048
	ds_read_b128 v[198:201], v150 offset:3072
	ds_read_b128 v[202:205], v150 offset:4096
	ds_read_b128 v[206:209], v150 offset:5120
	ds_read_b128 v[210:213], v150 offset:6144
	ds_read_b128 v[214:217], v150 offset:7168
	global_load_lds_dwordx4 v142, s[26:27]
	s_add_i32 m0, s44, 0xe000
	s_nop 0
	global_load_lds_dwordx4 v140, s[26:27]
	s_waitcnt vmcnt(8) lgkmcnt(0)
	s_barrier
	s_setprio 1
	v_mfma_f32_16x16x32_bf16 v[126:129], v[154:157], v[186:189], 0
	v_mfma_f32_16x16x32_bf16 v[122:125], v[162:165], v[186:189], 0
	v_mfma_f32_16x16x32_bf16 v[110:113], v[154:157], v[194:197], 0
	v_mfma_f32_16x16x32_bf16 v[106:109], v[162:165], v[194:197], 0
	v_mfma_f32_16x16x32_bf16 v[94:97], v[154:157], v[202:205], 0
	v_mfma_f32_16x16x32_bf16 v[90:93], v[162:165], v[202:205], 0
	v_mfma_f32_16x16x32_bf16 v[78:81], v[154:157], v[210:213], 0
	v_mfma_f32_16x16x32_bf16 v[74:77], v[162:165], v[210:213], 0
	v_mfma_f32_16x16x32_bf16 v[126:129], v[158:161], v[190:193], v[126:129]
	v_mfma_f32_16x16x32_bf16 v[122:125], v[166:169], v[190:193], v[122:125]
	v_mfma_f32_16x16x32_bf16 v[110:113], v[158:161], v[198:201], v[110:113]
	v_mfma_f32_16x16x32_bf16 v[106:109], v[166:169], v[198:201], v[106:109]
	v_mfma_f32_16x16x32_bf16 v[94:97], v[158:161], v[206:209], v[94:97]
	v_mfma_f32_16x16x32_bf16 v[90:93], v[166:169], v[206:209], v[90:93]
	v_mfma_f32_16x16x32_bf16 v[78:81], v[158:161], v[214:217], v[78:81]
	v_mfma_f32_16x16x32_bf16 v[74:77], v[166:169], v[214:217], v[74:77]
	s_setprio 0
	s_setprio 1
	v_mfma_f32_16x16x32_bf16 v[118:121], v[170:173], v[186:189], 0
	v_mfma_f32_16x16x32_bf16 v[114:117], v[178:181], v[186:189], 0
	v_mfma_f32_16x16x32_bf16 v[102:105], v[170:173], v[194:197], 0
	v_mfma_f32_16x16x32_bf16 v[98:101], v[178:181], v[194:197], 0
	v_mfma_f32_16x16x32_bf16 v[86:89], v[170:173], v[202:205], 0
	v_mfma_f32_16x16x32_bf16 v[82:85], v[178:181], v[202:205], 0
	v_mfma_f32_16x16x32_bf16 v[70:73], v[170:173], v[210:213], 0
	v_mfma_f32_16x16x32_bf16 v[66:69], v[178:181], v[210:213], 0
	v_mfma_f32_16x16x32_bf16 v[118:121], v[174:177], v[190:193], v[118:121]
	v_mfma_f32_16x16x32_bf16 v[114:117], v[182:185], v[190:193], v[114:117]
	v_mfma_f32_16x16x32_bf16 v[102:105], v[174:177], v[198:201], v[102:105]
	v_mfma_f32_16x16x32_bf16 v[98:101], v[182:185], v[198:201], v[98:101]
	v_mfma_f32_16x16x32_bf16 v[86:89], v[174:177], v[206:209], v[86:89]
	v_mfma_f32_16x16x32_bf16 v[82:85], v[182:185], v[206:209], v[82:85]
	v_mfma_f32_16x16x32_bf16 v[70:73], v[174:177], v[214:217], v[70:73]
	v_mfma_f32_16x16x32_bf16 v[66:69], v[182:185], v[214:217], v[66:69]
	s_setprio 0
	s_barrier
	s_mov_b32 m0, s40
	s_add_u32 s98, s28, 0x80
	s_addc_u32 s99, s29, 0
	s_add_u32 s66, s28, 0x80000
	ds_read_b128 v[186:189], v150 offset:16384
	ds_read_b128 v[190:193], v150 offset:17408
	ds_read_b128 v[194:197], v150 offset:18432
	ds_read_b128 v[198:201], v150 offset:19456
	ds_read_b128 v[202:205], v150 offset:20480
	ds_read_b128 v[206:209], v150 offset:21504
	ds_read_b128 v[210:213], v150 offset:22528
	ds_read_b128 v[214:217], v150 offset:23552
	global_load_lds_dwordx4 v132, s[28:29]
	s_mov_b32 m0, s41
	s_addc_u32 s67, s29, 0
	global_load_lds_dwordx4 v136, s[28:29]
	s_mov_b32 m0, s42
	s_nop 0
	global_load_lds_dwordx4 v132, s[66:67]
	s_mov_b32 m0, s43
	s_nop 0
	global_load_lds_dwordx4 v136, s[66:67]
	s_add_u32 s100, s30, 0x80
	s_addc_u32 s101, s31, 0
	s_mov_b32 m0, s44
	s_nop 0
	global_load_lds_dwordx4 v130, s[30:31]
	s_mov_b32 m0, s45
	s_nop 0
	global_load_lds_dwordx4 v134, s[30:31]
	s_waitcnt vmcnt(8) lgkmcnt(0)
	s_barrier
	s_setprio 1
	v_mfma_f32_16x16x32_bf16 v[62:65], v[154:157], v[186:189], 0
	v_mfma_f32_16x16x32_bf16 v[58:61], v[162:165], v[186:189], 0
	v_mfma_f32_16x16x32_bf16 v[46:49], v[154:157], v[194:197], 0
	v_mfma_f32_16x16x32_bf16 v[42:45], v[162:165], v[194:197], 0
	v_mfma_f32_16x16x32_bf16 v[30:33], v[154:157], v[202:205], 0
	v_mfma_f32_16x16x32_bf16 v[26:29], v[162:165], v[202:205], 0
	v_mfma_f32_16x16x32_bf16 v[14:17], v[154:157], v[210:213], 0
	v_mfma_f32_16x16x32_bf16 v[10:13], v[162:165], v[210:213], 0
	v_mfma_f32_16x16x32_bf16 v[62:65], v[158:161], v[190:193], v[62:65]
	v_mfma_f32_16x16x32_bf16 v[58:61], v[166:169], v[190:193], v[58:61]
	v_mfma_f32_16x16x32_bf16 v[46:49], v[158:161], v[198:201], v[46:49]
	v_mfma_f32_16x16x32_bf16 v[42:45], v[166:169], v[198:201], v[42:45]
	v_mfma_f32_16x16x32_bf16 v[30:33], v[158:161], v[206:209], v[30:33]
	v_mfma_f32_16x16x32_bf16 v[26:29], v[166:169], v[206:209], v[26:29]
	v_mfma_f32_16x16x32_bf16 v[14:17], v[158:161], v[214:217], v[14:17]
	v_mfma_f32_16x16x32_bf16 v[10:13], v[166:169], v[214:217], v[10:13]
	s_setprio 0
	s_setprio 1
	v_mfma_f32_16x16x32_bf16 v[54:57], v[170:173], v[186:189], 0
	v_mfma_f32_16x16x32_bf16 v[50:53], v[178:181], v[186:189], 0
	v_mfma_f32_16x16x32_bf16 v[38:41], v[170:173], v[194:197], 0
	v_mfma_f32_16x16x32_bf16 v[34:37], v[178:181], v[194:197], 0
	v_mfma_f32_16x16x32_bf16 v[22:25], v[170:173], v[202:205], 0
	v_mfma_f32_16x16x32_bf16 v[18:21], v[178:181], v[202:205], 0
	v_mfma_f32_16x16x32_bf16 v[6:9], v[170:173], v[210:213], 0
	v_mfma_f32_16x16x32_bf16 v[2:5], v[178:181], v[210:213], 0
	v_mfma_f32_16x16x32_bf16 v[54:57], v[174:177], v[190:193], v[54:57]
	v_mfma_f32_16x16x32_bf16 v[50:53], v[182:185], v[190:193], v[50:53]
	v_mfma_f32_16x16x32_bf16 v[38:41], v[174:177], v[198:201], v[38:41]
	v_mfma_f32_16x16x32_bf16 v[34:37], v[182:185], v[198:201], v[34:37]
	v_mfma_f32_16x16x32_bf16 v[22:25], v[174:177], v[206:209], v[22:25]
	v_mfma_f32_16x16x32_bf16 v[18:21], v[182:185], v[206:209], v[18:21]
	v_mfma_f32_16x16x32_bf16 v[6:9], v[174:177], v[214:217], v[6:9]
	v_mfma_f32_16x16x32_bf16 v[2:5], v[182:185], v[214:217], v[2:5]
	s_setprio 0
	s_barrier
; #define PG8_STAGE(bufoff, gbase, voff) do { _Pragma("unroll") for (int _i = 0; _i < 2; ++_i) \
;         __builtin_amdgcn_global_load_lds((const unsigned*)((const char*)(gbase) + (voff)[_i]), (PG8_LAS unsigned*)(lds + (bufoff) + ldsw + _i * 8192), 16, 0, 0); } while (0)
; #define PG8_LDA(dst, b, h) do { if constexpr (DT != 1) { _Pragma("unroll") for (int m = 0; m < 4; ++m) _Pragma("unroll") for (int k = 0; k < 2; ++k) dst[m][k] = *(const PG8_LAS bf16x8*)(lds + PG8_SA(b, h) + aoff + m * 2048 + k * 1024); } \
;         else { _Pragma("unroll") for (int m = 0; m < 4; ++m) dst##8[m] = ld32(lds + PG8_SA(b, h) + aoff + m * 2048); } } while (0)
; #define PG8_LDB(dst, b, h) do { if constexpr (DT != 1) { _Pragma("unroll") for (int n = 0; n < 2; ++n) _Pragma("unroll") for (int k = 0; k < 2; ++k) dst[n][k] = *(const PG8_LAS bf16x8*)(lds + PG8_SB(b, h) + boff + n * 2048 + k * 1024); } \
;         else { _Pragma("unroll") for (int n = 0; n < 2; ++n) dst##8[n] = ld32(lds + PG8_SB(b, h) + boff + n * 2048); } } while (0)
; #define PG8_WAIT_V(n) asm volatile("s_waitcnt vmcnt(" #n ")" ::: "memory")
; #define PG8_WAIT_L(n) asm volatile("s_waitcnt lgkmcnt(" #n ")" ::: "memory")
; #define PG8_BAR __builtin_amdgcn_s_barrier()
; #define PG8_SCHED __builtin_amdgcn_sched_barrier(0)
;     ...
;             PG8_LDB(B0, 1, 0); PG8_LDB(B1, 1, 1); PG8_SCHED; PG8_LDA(At, 1, 0); PG8_STAGE(PG8_SA(0, 1), a2 + hstepA, voffA);
;             PG8_WAIT_V(8); PG8_WAIT_L(0); PG8_BAR; PG8_MMA(0, 0, At, B0); PG8_MMA(0, 1, At, B1); PG8_BAR; PG8_SCHED;
;             PG8_LDA(At, 1, 1); PG8_STAGE(PG8_SB(1, 0), b3, voffB); PG8_STAGE(PG8_SB(1, 1), b3 + hstepB, voffB); PG8_STAGE(PG8_SA(1, 0), a3, voffA);
;             PG8_WAIT_V(8); PG8_WAIT_L(0); PG8_BAR; PG8_MMA(1, 0, At, B0); PG8_MMA(1, 1, At, B1); PG8_BAR; PG8_SCHED;
	ds_read_b128 v[154:157], v151
	ds_read_b128 v[158:161], v151 offset:1024
	ds_read_b128 v[162:165], v151 offset:2048
	ds_read_b128 v[166:169], v151 offset:3072
	ds_read_b128 v[170:173], v152
	ds_read_b128 v[174:177], v152 offset:1024
	ds_read_b128 v[178:181], v152 offset:2048
	ds_read_b128 v[182:185], v152 offset:3072
	s_add_u32 s30, s30, 0x80000
	s_addc_u32 s31, s31, 0
	s_mov_b32 m0, s46
	ds_read_b128 v[186:189], v150 offset:32768
	ds_read_b128 v[190:193], v150 offset:33792
	ds_read_b128 v[194:197], v150 offset:34816
	ds_read_b128 v[198:201], v150 offset:35840
	ds_read_b128 v[202:205], v150 offset:36864
	ds_read_b128 v[206:209], v150 offset:37888
	ds_read_b128 v[210:213], v150 offset:38912
	ds_read_b128 v[214:217], v150 offset:39936
	global_load_lds_dwordx4 v130, s[30:31]
	s_mov_b32 m0, s47
	s_nop 0
	global_load_lds_dwordx4 v134, s[30:31]
	s_waitcnt vmcnt(8) lgkmcnt(0)
	s_barrier
	s_setprio 1
	v_mfma_f32_16x16x32_bf16 v[126:129], v[154:157], v[186:189], v[126:129]
	v_mfma_f32_16x16x32_bf16 v[122:125], v[162:165], v[186:189], v[122:125]
	v_mfma_f32_16x16x32_bf16 v[110:113], v[154:157], v[194:197], v[110:113]
	v_mfma_f32_16x16x32_bf16 v[106:109], v[162:165], v[194:197], v[106:109]
	v_mfma_f32_16x16x32_bf16 v[94:97], v[154:157], v[202:205], v[94:97]
	v_mfma_f32_16x16x32_bf16 v[90:93], v[162:165], v[202:205], v[90:93]
	v_mfma_f32_16x16x32_bf16 v[78:81], v[154:157], v[210:213], v[78:81]
	v_mfma_f32_16x16x32_bf16 v[74:77], v[162:165], v[210:213], v[74:77]
	v_mfma_f32_16x16x32_bf16 v[126:129], v[158:161], v[190:193], v[126:129]
	v_mfma_f32_16x16x32_bf16 v[122:125], v[166:169], v[190:193], v[122:125]
	v_mfma_f32_16x16x32_bf16 v[110:113], v[158:161], v[198:201], v[110:113]
	v_mfma_f32_16x16x32_bf16 v[106:109], v[166:169], v[198:201], v[106:109]
	v_mfma_f32_16x16x32_bf16 v[94:97], v[158:161], v[206:209], v[94:97]
	v_mfma_f32_16x16x32_bf16 v[90:93], v[166:169], v[206:209], v[90:93]
	v_mfma_f32_16x16x32_bf16 v[78:81], v[158:161], v[214:217], v[78:81]
	v_mfma_f32_16x16x32_bf16 v[74:77], v[166:169], v[214:217], v[74:77]
	s_setprio 0
	s_setprio 1
	v_mfma_f32_16x16x32_bf16 v[118:121], v[170:173], v[186:189], v[118:121]
	v_mfma_f32_16x16x32_bf16 v[114:117], v[178:181], v[186:189], v[114:117]
	v_mfma_f32_16x16x32_bf16 v[102:105], v[170:173], v[194:197], v[102:105]
	v_mfma_f32_16x16x32_bf16 v[98:101], v[178:181], v[194:197], v[98:101]
	v_mfma_f32_16x16x32_bf16 v[86:89], v[170:173], v[202:205], v[86:89]
	v_mfma_f32_16x16x32_bf16 v[82:85], v[178:181], v[202:205], v[82:85]
	v_mfma_f32_16x16x32_bf16 v[70:73], v[170:173], v[210:213], v[70:73]
	v_mfma_f32_16x16x32_bf16 v[66:69], v[178:181], v[210:213], v[66:69]
	v_mfma_f32_16x16x32_bf16 v[118:121], v[174:177], v[190:193], v[118:121]
	v_mfma_f32_16x16x32_bf16 v[114:117], v[182:185], v[190:193], v[114:117]
	v_mfma_f32_16x16x32_bf16 v[102:105], v[174:177], v[198:201], v[102:105]
	v_mfma_f32_16x16x32_bf16 v[98:101], v[182:185], v[198:201], v[98:101]
	v_mfma_f32_16x16x32_bf16 v[86:89], v[174:177], v[206:209], v[86:89]
	v_mfma_f32_16x16x32_bf16 v[82:85], v[182:185], v[206:209], v[82:85]
	v_mfma_f32_16x16x32_bf16 v[70:73], v[174:177], v[214:217], v[70:73]
	v_mfma_f32_16x16x32_bf16 v[66:69], v[182:185], v[214:217], v[66:69]
	s_setprio 0
	s_barrier
	s_mov_b32 m0, s53
	s_add_u32 s28, s28, 0x80080
	ds_read_b128 v[186:189], v150 offset:49152
	ds_read_b128 v[190:193], v150 offset:50176
	ds_read_b128 v[194:197], v150 offset:51200
	ds_read_b128 v[198:201], v150 offset:52224
	ds_read_b128 v[202:205], v150 offset:53248
	ds_read_b128 v[206:209], v150 offset:54272
	ds_read_b128 v[210:213], v150 offset:55296
	ds_read_b128 v[214:217], v150 offset:56320
	global_load_lds_dwordx4 v132, s[98:99]
	s_mov_b32 m0, s54
	s_addc_u32 s29, s29, 0
	global_load_lds_dwordx4 v136, s[98:99]
	s_mov_b32 m0, s57
	s_nop 0
	global_load_lds_dwordx4 v132, s[28:29]
	s_mov_b32 m0, s58
	s_nop 0
	global_load_lds_dwordx4 v136, s[28:29]
	s_mov_b32 m0, s55
	s_nop 0
	global_load_lds_dwordx4 v130, s[100:101]
	s_mov_b32 m0, s56
	s_nop 0
	global_load_lds_dwordx4 v134, s[100:101]
	s_waitcnt vmcnt(8) lgkmcnt(0)
	s_barrier
	s_setprio 1
	v_mfma_f32_16x16x32_bf16 v[62:65], v[154:157], v[186:189], v[62:65]
	v_mfma_f32_16x16x32_bf16 v[58:61], v[162:165], v[186:189], v[58:61]
	v_mfma_f32_16x16x32_bf16 v[46:49], v[154:157], v[194:197], v[46:49]
	v_mfma_f32_16x16x32_bf16 v[42:45], v[162:165], v[194:197], v[42:45]
	v_mfma_f32_16x16x32_bf16 v[30:33], v[154:157], v[202:205], v[30:33]
	v_mfma_f32_16x16x32_bf16 v[26:29], v[162:165], v[202:205], v[26:29]
	v_mfma_f32_16x16x32_bf16 v[14:17], v[154:157], v[210:213], v[14:17]
	v_mfma_f32_16x16x32_bf16 v[10:13], v[162:165], v[210:213], v[10:13]
	v_mfma_f32_16x16x32_bf16 v[62:65], v[158:161], v[190:193], v[62:65]
	v_mfma_f32_16x16x32_bf16 v[58:61], v[166:169], v[190:193], v[58:61]
	v_mfma_f32_16x16x32_bf16 v[46:49], v[158:161], v[198:201], v[46:49]
	v_mfma_f32_16x16x32_bf16 v[42:45], v[166:169], v[198:201], v[42:45]
	v_mfma_f32_16x16x32_bf16 v[30:33], v[158:161], v[206:209], v[30:33]
	v_mfma_f32_16x16x32_bf16 v[26:29], v[166:169], v[206:209], v[26:29]
	v_mfma_f32_16x16x32_bf16 v[14:17], v[158:161], v[214:217], v[14:17]
	v_mfma_f32_16x16x32_bf16 v[10:13], v[166:169], v[214:217], v[10:13]
	s_setprio 0
	s_setprio 1
	v_mfma_f32_16x16x32_bf16 v[54:57], v[170:173], v[186:189], v[54:57]
	v_mfma_f32_16x16x32_bf16 v[50:53], v[178:181], v[186:189], v[50:53]
	v_mfma_f32_16x16x32_bf16 v[38:41], v[170:173], v[194:197], v[38:41]
	v_mfma_f32_16x16x32_bf16 v[34:37], v[178:181], v[194:197], v[34:37]
	v_mfma_f32_16x16x32_bf16 v[22:25], v[170:173], v[202:205], v[22:25]
	v_mfma_f32_16x16x32_bf16 v[18:21], v[178:181], v[202:205], v[18:21]
	v_mfma_f32_16x16x32_bf16 v[6:9], v[170:173], v[210:213], v[6:9]
	v_mfma_f32_16x16x32_bf16 v[2:5], v[178:181], v[210:213], v[2:5]
	v_mfma_f32_16x16x32_bf16 v[54:57], v[174:177], v[190:193], v[54:57]
	v_mfma_f32_16x16x32_bf16 v[50:53], v[182:185], v[190:193], v[50:53]
	v_mfma_f32_16x16x32_bf16 v[38:41], v[174:177], v[198:201], v[38:41]
	v_mfma_f32_16x16x32_bf16 v[34:37], v[182:185], v[198:201], v[34:37]
	v_mfma_f32_16x16x32_bf16 v[22:25], v[174:177], v[206:209], v[22:25]
	v_mfma_f32_16x16x32_bf16 v[18:21], v[182:185], v[206:209], v[18:21]
	v_mfma_f32_16x16x32_bf16 v[6:9], v[174:177], v[214:217], v[6:9]
	v_mfma_f32_16x16x32_bf16 v[2:5], v[182:185], v[214:217], v[2:5]
	s_setprio 0
	s_barrier
	s_add_u32 s25, s25, 0x100
	s_addc_u32 s64, s64, 0
	s_add_u32 s26, s26, 0x100
	s_addc_u32 s27, s27, 0
	s_cmp_ge_i32 s65, s52
	s_mov_b32 s28, s65
	s_cbranch_scc0 .LBB0_2262
	s_branch .LBB0_2263

; #define PG8_STAGE(bufoff, gbase, voff) do { _Pragma("unroll") for (int _i = 0; _i < 2; ++_i) \
;         __builtin_amdgcn_global_load_lds((const unsigned*)((const char*)(gbase) + (voff)[_i]), (PG8_LAS unsigned*)(lds + (bufoff) + ldsw + _i * 8192), 16, 0, 0); } while (0)
; #define PG8_LDA(dst, b, h) do { if constexpr (DT != 1) { _Pragma("unroll") for (int m = 0; m < 4; ++m) _Pragma("unroll") for (int k = 0; k < 2; ++k) dst[m][k] = *(const PG8_LAS bf16x8*)(lds + PG8_SA(b, h) + aoff + m * 2048 + k * 1024); } \
;         else { _Pragma("unroll") for (int m = 0; m < 4; ++m) dst##8[m] = ld32(lds + PG8_SA(b, h) + aoff + m * 2048); } } while (0)
; #define PG8_LDB(dst, b, h) do { if constexpr (DT != 1) { _Pragma("unroll") for (int n = 0; n < 2; ++n) _Pragma("unroll") for (int k = 0; k < 2; ++k) dst[n][k] = *(const PG8_LAS bf16x8*)(lds + PG8_SB(b, h) + boff + n * 2048 + k * 1024); } \
;         else { _Pragma("unroll") for (int n = 0; n < 2; ++n) dst##8[n] = ld32(lds + PG8_SB(b, h) + boff + n * 2048); } } while (0)
; #define PG8_WAIT_V(n) asm volatile("s_waitcnt vmcnt(" #n ")" ::: "memory")
; #define PG8_WAIT_L(n) asm volatile("s_waitcnt lgkmcnt(" #n ")" ::: "memory")
; #define PG8_BAR __builtin_amdgcn_s_barrier()
; #define PG8_SCHED __builtin_amdgcn_sched_barrier(0)
;     ...
;         for (int t = 0; t < nt; t += 2) {
;             const bool last = (t == nt - 2);
;             const char* a1 = cA + (size_t)(t + 1) * kstep;
;             const char* a2 = last ? nA : cA + (size_t)(t + 2) * kstep; const char* b2 = last ? nB : cB + (size_t)(t + 2) * kstep;
;             const char* a3 = a2 + kstep; const char* b3 = b2 + kstep;
;             if (last && has_next) S.a_ready(nxt);
;             if constexpr (SP2) {
;             PG8_LDB(B0, 0, 0); PG8_LDB(B1, 0, 1); PG8_SCHED; PG8_LDA(At, 0, 0); PG8_STAGE(PG8_SA(1, 1), a1 + hstepA, voffA);
;             PG8_WAIT_V(8); PG8_WAIT_L(0); PG8_BAR; PG8_MMA(0, 0, At, B0); PG8_MMA(0, 1, At, B1); PG8_BAR; PG8_SCHED;
;             PG8_LDA(At, 0, 1); PG8_STAGE(PG8_SB(0, 0), b2, voffB); PG8_STAGE(PG8_SB(0, 1), b2 + hstepB, voffB); PG8_STAGE(PG8_SA(0, 0), a2, voffA);
;             PG8_WAIT_V(8); PG8_WAIT_L(0); PG8_BAR; PG8_MMA(1, 0, At, B0); PG8_MMA(1, 1, At, B1); PG8_BAR; PG8_SCHED;
.Lzs_10:
	s_cbranch_vccnz .LBB0_3358
	s_and_b64 s[44:45], s[0:1], exec
	s_cselect_b32 s3, s35, s43
	s_cselect_b32 s29, s34, s42
	s_cselect_b32 s31, s37, s41
	s_cselect_b32 s39, s36, s40
	s_add_u32 s76, s40, 0x100
	s_addc_u32 s77, s41, 0
	s_add_u32 s40, s42, 0x10080
	s_addc_u32 s41, s43, 0
	s_mov_b32 s42, 0
	ds_read_b128 v[130:133], v173
	ds_read_b128 v[134:137], v173 offset:1024
	ds_read_b128 v[138:141], v173 offset:2048
	ds_read_b128 v[142:145], v173 offset:3072
	ds_read_b128 v[164:167], v174
	ds_read_b128 v[168:171], v174 offset:1024
	ds_read_b128 v[178:181], v174 offset:2048
	ds_read_b128 v[182:185], v174 offset:3072
	s_add_i32 s78, s42, 2
	s_add_u32 s43, s40, 0xffff0080
	s_addc_u32 s44, s41, -1
	s_cmp_eq_u32 s74, s42
	s_cselect_b32 s42, s39, s76
	s_cselect_b32 s45, s3, s44
	s_cselect_b32 s44, s29, s43
	s_cselect_b32 s43, s31, s77
	s_add_i32 m0, s56, 0xc000
	ds_read_b128 v[186:189], v175
	ds_read_b128 v[190:193], v175 offset:1024
	ds_read_b128 v[194:197], v175 offset:2048
	ds_read_b128 v[198:201], v175 offset:3072
	ds_read_b128 v[202:205], v175 offset:4096
	ds_read_b128 v[206:209], v175 offset:5120
	ds_read_b128 v[210:213], v175 offset:6144
	ds_read_b128 v[214:217], v175 offset:7168
	global_load_lds_dwordx4 v158, s[40:41]
	s_add_i32 m0, s56, 0xe000
	s_nop 0
	global_load_lds_dwordx4 v156, s[40:41]
	s_waitcnt vmcnt(8) lgkmcnt(0)
	s_barrier
	s_setprio 1
	v_mfma_f32_16x16x32_bf16 v[126:129], v[130:133], v[186:189], 0
	v_mfma_f32_16x16x32_bf16 v[122:125], v[138:141], v[186:189], 0
	v_mfma_f32_16x16x32_bf16 v[110:113], v[130:133], v[194:197], 0
	v_mfma_f32_16x16x32_bf16 v[106:109], v[138:141], v[194:197], 0
	v_mfma_f32_16x16x32_bf16 v[94:97], v[130:133], v[202:205], 0
	v_mfma_f32_16x16x32_bf16 v[90:93], v[138:141], v[202:205], 0
	v_mfma_f32_16x16x32_bf16 v[78:81], v[130:133], v[210:213], 0
	v_mfma_f32_16x16x32_bf16 v[74:77], v[138:141], v[210:213], 0
	v_mfma_f32_16x16x32_bf16 v[126:129], v[134:137], v[190:193], v[126:129]
	v_mfma_f32_16x16x32_bf16 v[122:125], v[142:145], v[190:193], v[122:125]
	v_mfma_f32_16x16x32_bf16 v[110:113], v[134:137], v[198:201], v[110:113]
	v_mfma_f32_16x16x32_bf16 v[106:109], v[142:145], v[198:201], v[106:109]
	v_mfma_f32_16x16x32_bf16 v[94:97], v[134:137], v[206:209], v[94:97]
	v_mfma_f32_16x16x32_bf16 v[90:93], v[142:145], v[206:209], v[90:93]
	v_mfma_f32_16x16x32_bf16 v[78:81], v[134:137], v[214:217], v[78:81]
	v_mfma_f32_16x16x32_bf16 v[74:77], v[142:145], v[214:217], v[74:77]
	s_setprio 0
	s_setprio 1
	v_mfma_f32_16x16x32_bf16 v[118:121], v[164:167], v[186:189], 0
	v_mfma_f32_16x16x32_bf16 v[114:117], v[178:181], v[186:189], 0
	v_mfma_f32_16x16x32_bf16 v[102:105], v[164:167], v[194:197], 0
	v_mfma_f32_16x16x32_bf16 v[98:101], v[178:181], v[194:197], 0
	v_mfma_f32_16x16x32_bf16 v[86:89], v[164:167], v[202:205], 0
	v_mfma_f32_16x16x32_bf16 v[82:85], v[178:181], v[202:205], 0
	v_mfma_f32_16x16x32_bf16 v[70:73], v[164:167], v[210:213], 0
	v_mfma_f32_16x16x32_bf16 v[66:69], v[178:181], v[210:213], 0
	v_mfma_f32_16x16x32_bf16 v[118:121], v[168:171], v[190:193], v[118:121]
	v_mfma_f32_16x16x32_bf16 v[114:117], v[182:185], v[190:193], v[114:117]
	v_mfma_f32_16x16x32_bf16 v[102:105], v[168:171], v[198:201], v[102:105]
	v_mfma_f32_16x16x32_bf16 v[98:101], v[182:185], v[198:201], v[98:101]
	v_mfma_f32_16x16x32_bf16 v[86:89], v[168:171], v[206:209], v[86:89]
	v_mfma_f32_16x16x32_bf16 v[82:85], v[182:185], v[206:209], v[82:85]
	v_mfma_f32_16x16x32_bf16 v[70:73], v[168:171], v[214:217], v[70:73]
	v_mfma_f32_16x16x32_bf16 v[66:69], v[182:185], v[214:217], v[66:69]
	s_setprio 0
	s_barrier
	s_mov_b32 m0, s52
	s_add_u32 s98, s42, 0x80
	s_addc_u32 s99, s43, 0
	s_add_u32 s80, s42, 0x10000
	ds_read_b128 v[186:189], v175 offset:16384
	ds_read_b128 v[190:193], v175 offset:17408
	ds_read_b128 v[194:197], v175 offset:18432
	ds_read_b128 v[198:201], v175 offset:19456
	ds_read_b128 v[202:205], v175 offset:20480
	ds_read_b128 v[206:209], v175 offset:21504
	ds_read_b128 v[210:213], v175 offset:22528
	ds_read_b128 v[214:217], v175 offset:23552
	global_load_lds_dwordx4 v148, s[42:43]
	s_mov_b32 m0, s53
	s_addc_u32 s81, s43, 0
	global_load_lds_dwordx4 v152, s[42:43]
	s_mov_b32 m0, s54
	s_nop 0
	global_load_lds_dwordx4 v148, s[80:81]
	s_mov_b32 m0, s55
	s_nop 0
	global_load_lds_dwordx4 v152, s[80:81]
	s_add_u32 s100, s44, 0x80
	s_addc_u32 s101, s45, 0
	s_mov_b32 m0, s56
	s_nop 0
	global_load_lds_dwordx4 v146, s[44:45]
	s_mov_b32 m0, s57
	s_nop 0
	global_load_lds_dwordx4 v150, s[44:45]
	s_waitcnt vmcnt(8) lgkmcnt(0)
	s_barrier
	s_setprio 1
	v_mfma_f32_16x16x32_bf16 v[62:65], v[130:133], v[186:189], 0
	v_mfma_f32_16x16x32_bf16 v[58:61], v[138:141], v[186:189], 0
	v_mfma_f32_16x16x32_bf16 v[46:49], v[130:133], v[194:197], 0
	v_mfma_f32_16x16x32_bf16 v[42:45], v[138:141], v[194:197], 0
	v_mfma_f32_16x16x32_bf16 v[30:33], v[130:133], v[202:205], 0
	v_mfma_f32_16x16x32_bf16 v[26:29], v[138:141], v[202:205], 0
	v_mfma_f32_16x16x32_bf16 v[14:17], v[130:133], v[210:213], 0
	v_mfma_f32_16x16x32_bf16 v[10:13], v[138:141], v[210:213], 0
	v_mfma_f32_16x16x32_bf16 v[62:65], v[134:137], v[190:193], v[62:65]
	v_mfma_f32_16x16x32_bf16 v[58:61], v[142:145], v[190:193], v[58:61]
	v_mfma_f32_16x16x32_bf16 v[46:49], v[134:137], v[198:201], v[46:49]
	v_mfma_f32_16x16x32_bf16 v[42:45], v[142:145], v[198:201], v[42:45]
	v_mfma_f32_16x16x32_bf16 v[30:33], v[134:137], v[206:209], v[30:33]
	v_mfma_f32_16x16x32_bf16 v[26:29], v[142:145], v[206:209], v[26:29]
	v_mfma_f32_16x16x32_bf16 v[14:17], v[134:137], v[214:217], v[14:17]
	v_mfma_f32_16x16x32_bf16 v[10:13], v[142:145], v[214:217], v[10:13]
	s_setprio 0
	s_setprio 1
	v_mfma_f32_16x16x32_bf16 v[54:57], v[164:167], v[186:189], 0
	v_mfma_f32_16x16x32_bf16 v[50:53], v[178:181], v[186:189], 0
	v_mfma_f32_16x16x32_bf16 v[38:41], v[164:167], v[194:197], 0
	v_mfma_f32_16x16x32_bf16 v[34:37], v[178:181], v[194:197], 0
	v_mfma_f32_16x16x32_bf16 v[22:25], v[164:167], v[202:205], 0
	v_mfma_f32_16x16x32_bf16 v[18:21], v[178:181], v[202:205], 0
	v_mfma_f32_16x16x32_bf16 v[6:9], v[164:167], v[210:213], 0
	v_mfma_f32_16x16x32_bf16 v[2:5], v[178:181], v[210:213], 0
	v_mfma_f32_16x16x32_bf16 v[54:57], v[168:171], v[190:193], v[54:57]
	v_mfma_f32_16x16x32_bf16 v[50:53], v[182:185], v[190:193], v[50:53]
	v_mfma_f32_16x16x32_bf16 v[38:41], v[168:171], v[198:201], v[38:41]
	v_mfma_f32_16x16x32_bf16 v[34:37], v[182:185], v[198:201], v[34:37]
	v_mfma_f32_16x16x32_bf16 v[22:25], v[168:171], v[206:209], v[22:25]
	v_mfma_f32_16x16x32_bf16 v[18:21], v[182:185], v[206:209], v[18:21]
	v_mfma_f32_16x16x32_bf16 v[6:9], v[168:171], v[214:217], v[6:9]
	v_mfma_f32_16x16x32_bf16 v[2:5], v[182:185], v[214:217], v[2:5]
	s_setprio 0
	s_barrier
; #define PG8_STAGE(bufoff, gbase, voff) do { _Pragma("unroll") for (int _i = 0; _i < 2; ++_i) \
;         __builtin_amdgcn_global_load_lds((const unsigned*)((const char*)(gbase) + (voff)[_i]), (PG8_LAS unsigned*)(lds + (bufoff) + ldsw + _i * 8192), 16, 0, 0); } while (0)
; #define PG8_LDA(dst, b, h) do { if constexpr (DT != 1) { _Pragma("unroll") for (int m = 0; m < 4; ++m) _Pragma("unroll") for (int k = 0; k < 2; ++k) dst[m][k] = *(const PG8_LAS bf16x8*)(lds + PG8_SA(b, h) + aoff + m * 2048 + k * 1024); } \
;         else { _Pragma("unroll") for (int m = 0; m < 4; ++m) dst##8[m] = ld32(lds + PG8_SA(b, h) + aoff + m * 2048); } } while (0)
; #define PG8_LDB(dst, b, h) do { if constexpr (DT != 1) { _Pragma("unroll") for (int n = 0; n < 2; ++n) _Pragma("unroll") for (int k = 0; k < 2; ++k) dst[n][k] = *(const PG8_LAS bf16x8*)(lds + PG8_SB(b, h) + boff + n * 2048 + k * 1024); } \
;         else { _Pragma("unroll") for (int n = 0; n < 2; ++n) dst##8[n] = ld32(lds + PG8_SB(b, h) + boff + n * 2048); } } while (0)
; #define PG8_WAIT_V(n) asm volatile("s_waitcnt vmcnt(" #n ")" ::: "memory")
; #define PG8_WAIT_L(n) asm volatile("s_waitcnt lgkmcnt(" #n ")" ::: "memory")
; #define PG8_BAR __builtin_amdgcn_s_barrier()
; #define PG8_SCHED __builtin_amdgcn_sched_barrier(0)
;     ...
;             PG8_LDB(B0, 1, 0); PG8_LDB(B1, 1, 1); PG8_SCHED; PG8_LDA(At, 1, 0); PG8_STAGE(PG8_SA(0, 1), a2 + hstepA, voffA);
;             PG8_WAIT_V(8); PG8_WAIT_L(0); PG8_BAR; PG8_MMA(0, 0, At, B0); PG8_MMA(0, 1, At, B1); PG8_BAR; PG8_SCHED;
;             PG8_LDA(At, 1, 1); PG8_STAGE(PG8_SB(1, 0), b3, voffB); PG8_STAGE(PG8_SB(1, 1), b3 + hstepB, voffB); PG8_STAGE(PG8_SA(1, 0), a3, voffA);
;             PG8_WAIT_V(8); PG8_WAIT_L(0); PG8_BAR; PG8_MMA(1, 0, At, B0); PG8_MMA(1, 1, At, B1); PG8_BAR; PG8_SCHED;
	ds_read_b128 v[130:133], v176
	ds_read_b128 v[134:137], v176 offset:1024
	ds_read_b128 v[138:141], v176 offset:2048
	ds_read_b128 v[142:145], v176 offset:3072
	ds_read_b128 v[164:167], v177
	ds_read_b128 v[168:171], v177 offset:1024
	ds_read_b128 v[178:181], v177 offset:2048
	ds_read_b128 v[182:185], v177 offset:3072
	s_add_u32 s44, s44, 0x10000
	s_addc_u32 s45, s45, 0
	s_mov_b32 m0, s58
	ds_read_b128 v[186:189], v175 offset:32768
	ds_read_b128 v[190:193], v175 offset:33792
	ds_read_b128 v[194:197], v175 offset:34816
	ds_read_b128 v[198:201], v175 offset:35840
	ds_read_b128 v[202:205], v175 offset:36864
	ds_read_b128 v[206:209], v175 offset:37888
	ds_read_b128 v[210:213], v175 offset:38912
	ds_read_b128 v[214:217], v175 offset:39936
	global_load_lds_dwordx4 v146, s[44:45]
	s_mov_b32 m0, s59
	s_nop 0
	global_load_lds_dwordx4 v150, s[44:45]
	s_waitcnt vmcnt(8) lgkmcnt(0)
	s_barrier
	s_setprio 1
	v_mfma_f32_16x16x32_bf16 v[126:129], v[130:133], v[186:189], v[126:129]
	v_mfma_f32_16x16x32_bf16 v[122:125], v[138:141], v[186:189], v[122:125]
	v_mfma_f32_16x16x32_bf16 v[110:113], v[130:133], v[194:197], v[110:113]
	v_mfma_f32_16x16x32_bf16 v[106:109], v[138:141], v[194:197], v[106:109]
	v_mfma_f32_16x16x32_bf16 v[94:97], v[130:133], v[202:205], v[94:97]
	v_mfma_f32_16x16x32_bf16 v[90:93], v[138:141], v[202:205], v[90:93]
	v_mfma_f32_16x16x32_bf16 v[78:81], v[130:133], v[210:213], v[78:81]
	v_mfma_f32_16x16x32_bf16 v[74:77], v[138:141], v[210:213], v[74:77]
	v_mfma_f32_16x16x32_bf16 v[126:129], v[134:137], v[190:193], v[126:129]
	v_mfma_f32_16x16x32_bf16 v[122:125], v[142:145], v[190:193], v[122:125]
	v_mfma_f32_16x16x32_bf16 v[110:113], v[134:137], v[198:201], v[110:113]
	v_mfma_f32_16x16x32_bf16 v[106:109], v[142:145], v[198:201], v[106:109]
	v_mfma_f32_16x16x32_bf16 v[94:97], v[134:137], v[206:209], v[94:97]
	v_mfma_f32_16x16x32_bf16 v[90:93], v[142:145], v[206:209], v[90:93]
	v_mfma_f32_16x16x32_bf16 v[78:81], v[134:137], v[214:217], v[78:81]
	v_mfma_f32_16x16x32_bf16 v[74:77], v[142:145], v[214:217], v[74:77]
	s_setprio 0
	s_setprio 1
	v_mfma_f32_16x16x32_bf16 v[118:121], v[164:167], v[186:189], v[118:121]
	v_mfma_f32_16x16x32_bf16 v[114:117], v[178:181], v[186:189], v[114:117]
	v_mfma_f32_16x16x32_bf16 v[102:105], v[164:167], v[194:197], v[102:105]
	v_mfma_f32_16x16x32_bf16 v[98:101], v[178:181], v[194:197], v[98:101]
	v_mfma_f32_16x16x32_bf16 v[86:89], v[164:167], v[202:205], v[86:89]
	v_mfma_f32_16x16x32_bf16 v[82:85], v[178:181], v[202:205], v[82:85]
	v_mfma_f32_16x16x32_bf16 v[70:73], v[164:167], v[210:213], v[70:73]
	v_mfma_f32_16x16x32_bf16 v[66:69], v[178:181], v[210:213], v[66:69]
	v_mfma_f32_16x16x32_bf16 v[118:121], v[168:171], v[190:193], v[118:121]
	v_mfma_f32_16x16x32_bf16 v[114:117], v[182:185], v[190:193], v[114:117]
	v_mfma_f32_16x16x32_bf16 v[102:105], v[168:171], v[198:201], v[102:105]
	v_mfma_f32_16x16x32_bf16 v[98:101], v[182:185], v[198:201], v[98:101]
	v_mfma_f32_16x16x32_bf16 v[86:89], v[168:171], v[206:209], v[86:89]
	v_mfma_f32_16x16x32_bf16 v[82:85], v[182:185], v[206:209], v[82:85]
	v_mfma_f32_16x16x32_bf16 v[70:73], v[168:171], v[214:217], v[70:73]
	v_mfma_f32_16x16x32_bf16 v[66:69], v[182:185], v[214:217], v[66:69]
	s_setprio 0
	s_barrier
	s_mov_b32 m0, s66
	s_add_u32 s42, s42, 0x10080
	ds_read_b128 v[186:189], v175 offset:49152
	ds_read_b128 v[190:193], v175 offset:50176
	ds_read_b128 v[194:197], v175 offset:51200
	ds_read_b128 v[198:201], v175 offset:52224
	ds_read_b128 v[202:205], v175 offset:53248
	ds_read_b128 v[206:209], v175 offset:54272
	ds_read_b128 v[210:213], v175 offset:55296
	ds_read_b128 v[214:217], v175 offset:56320
	global_load_lds_dwordx4 v148, s[98:99]
	s_mov_b32 m0, s67
	s_addc_u32 s43, s43, 0
	global_load_lds_dwordx4 v152, s[98:99]
	s_mov_b32 m0, s70
	s_nop 0
	global_load_lds_dwordx4 v148, s[42:43]
	s_mov_b32 m0, s71
	s_nop 0
	global_load_lds_dwordx4 v152, s[42:43]
	s_mov_b32 m0, s68
	s_nop 0
	global_load_lds_dwordx4 v146, s[100:101]
	s_mov_b32 m0, s69
	s_nop 0
	global_load_lds_dwordx4 v150, s[100:101]
	s_waitcnt vmcnt(8) lgkmcnt(0)
	s_barrier
	s_setprio 1
	v_mfma_f32_16x16x32_bf16 v[62:65], v[130:133], v[186:189], v[62:65]
	v_mfma_f32_16x16x32_bf16 v[58:61], v[138:141], v[186:189], v[58:61]
	v_mfma_f32_16x16x32_bf16 v[46:49], v[130:133], v[194:197], v[46:49]
	v_mfma_f32_16x16x32_bf16 v[42:45], v[138:141], v[194:197], v[42:45]
	v_mfma_f32_16x16x32_bf16 v[30:33], v[130:133], v[202:205], v[30:33]
	v_mfma_f32_16x16x32_bf16 v[26:29], v[138:141], v[202:205], v[26:29]
	v_mfma_f32_16x16x32_bf16 v[14:17], v[130:133], v[210:213], v[14:17]
	v_mfma_f32_16x16x32_bf16 v[10:13], v[138:141], v[210:213], v[10:13]
	v_mfma_f32_16x16x32_bf16 v[62:65], v[134:137], v[190:193], v[62:65]
	v_mfma_f32_16x16x32_bf16 v[58:61], v[142:145], v[190:193], v[58:61]
	v_mfma_f32_16x16x32_bf16 v[46:49], v[134:137], v[198:201], v[46:49]
	v_mfma_f32_16x16x32_bf16 v[42:45], v[142:145], v[198:201], v[42:45]
	v_mfma_f32_16x16x32_bf16 v[30:33], v[134:137], v[206:209], v[30:33]
	v_mfma_f32_16x16x32_bf16 v[26:29], v[142:145], v[206:209], v[26:29]
	v_mfma_f32_16x16x32_bf16 v[14:17], v[134:137], v[214:217], v[14:17]
	v_mfma_f32_16x16x32_bf16 v[10:13], v[142:145], v[214:217], v[10:13]
	s_setprio 0
	s_setprio 1
	v_mfma_f32_16x16x32_bf16 v[54:57], v[164:167], v[186:189], v[54:57]
	v_mfma_f32_16x16x32_bf16 v[50:53], v[178:181], v[186:189], v[50:53]
	v_mfma_f32_16x16x32_bf16 v[38:41], v[164:167], v[194:197], v[38:41]
	v_mfma_f32_16x16x32_bf16 v[34:37], v[178:181], v[194:197], v[34:37]
	v_mfma_f32_16x16x32_bf16 v[22:25], v[164:167], v[202:205], v[22:25]
	v_mfma_f32_16x16x32_bf16 v[18:21], v[178:181], v[202:205], v[18:21]
	v_mfma_f32_16x16x32_bf16 v[6:9], v[164:167], v[210:213], v[6:9]
	v_mfma_f32_16x16x32_bf16 v[2:5], v[178:181], v[210:213], v[2:5]
	v_mfma_f32_16x16x32_bf16 v[54:57], v[168:171], v[190:193], v[54:57]
	v_mfma_f32_16x16x32_bf16 v[50:53], v[182:185], v[190:193], v[50:53]
	v_mfma_f32_16x16x32_bf16 v[38:41], v[168:171], v[198:201], v[38:41]
	v_mfma_f32_16x16x32_bf16 v[34:37], v[182:185], v[198:201], v[34:37]
	v_mfma_f32_16x16x32_bf16 v[22:25], v[168:171], v[206:209], v[22:25]
	v_mfma_f32_16x16x32_bf16 v[18:21], v[182:185], v[206:209], v[18:21]
	v_mfma_f32_16x16x32_bf16 v[6:9], v[168:171], v[214:217], v[6:9]
	v_mfma_f32_16x16x32_bf16 v[2:5], v[182:185], v[214:217], v[2:5]
	s_setprio 0
	s_barrier
	s_add_u32 s76, s76, 0x100
	s_addc_u32 s77, s77, 0
	s_add_u32 s40, s40, 0x100
	s_addc_u32 s41, s41, 0
	s_cmp_ge_i32 s78, s65
	s_mov_b32 s42, s78
	s_cbranch_scc0 .LBB0_3356
	s_branch .Lpx_15

;     __device__ __forceinline__ void operator()(const f32x4 (&acc)[2][2][4][2], const Unit& u, int wr, int wc, int fr, int fq) const {
;         const int pml = u.pm & (MROWS_TILES - 1), row0 = pml * BM + wr * 64 + fr, seg = u.pn >> 3, col0 = (u.pn & 7) * BM + wc * 32 + 8 * fq;
;         const float* bias = seg == 0 ? w0 : a0;
.Lpx_15:
	v_readlane_b32 s76, v247, 9

; #define PG8_STAGE(bufoff, gbase, voff) do { _Pragma("unroll") for (int _i = 0; _i < 2; ++_i) \
;         __builtin_amdgcn_global_load_lds((const unsigned*)((const char*)(gbase) + (voff)[_i]), (PG8_LAS unsigned*)(lds + (bufoff) + ldsw + _i * 8192), 16, 0, 0); } while (0)
; #define PG8_LDA(dst, b, h) do { if constexpr (DT != 1) { _Pragma("unroll") for (int m = 0; m < 4; ++m) _Pragma("unroll") for (int k = 0; k < 2; ++k) dst[m][k] = *(const PG8_LAS bf16x8*)(lds + PG8_SA(b, h) + aoff + m * 2048 + k * 1024); } \
;         else { _Pragma("unroll") for (int m = 0; m < 4; ++m) dst##8[m] = ld32(lds + PG8_SA(b, h) + aoff + m * 2048); } } while (0)
; #define PG8_LDB(dst, b, h) do { if constexpr (DT != 1) { _Pragma("unroll") for (int n = 0; n < 2; ++n) _Pragma("unroll") for (int k = 0; k < 2; ++k) dst[n][k] = *(const PG8_LAS bf16x8*)(lds + PG8_SB(b, h) + boff + n * 2048 + k * 1024); } \
;         else { _Pragma("unroll") for (int n = 0; n < 2; ++n) dst##8[n] = ld32(lds + PG8_SB(b, h) + boff + n * 2048); } } while (0)
; #define PG8_WAIT_V(n) asm volatile("s_waitcnt vmcnt(" #n ")" ::: "memory")
; #define PG8_WAIT_L(n) asm volatile("s_waitcnt lgkmcnt(" #n ")" ::: "memory")
; #define PG8_BAR __builtin_amdgcn_s_barrier()
; #define PG8_SCHED __builtin_amdgcn_sched_barrier(0)
;     ...
;         for (int t = 0; t < nt; t += 2) {
;             const bool last = (t == nt - 2);
;             const char* a1 = cA + (size_t)(t + 1) * kstep;
;             const char* a2 = last ? nA : cA + (size_t)(t + 2) * kstep; const char* b2 = last ? nB : cB + (size_t)(t + 2) * kstep;
;             const char* a3 = a2 + kstep; const char* b3 = b2 + kstep;
;             if (last && has_next) S.a_ready(nxt);
;             if constexpr (SP2) {
;             PG8_LDB(B0, 0, 0); PG8_LDB(B1, 0, 1); PG8_SCHED; PG8_LDA(At, 0, 0); PG8_STAGE(PG8_SA(1, 1), a1 + hstepA, voffA);
;             PG8_WAIT_V(8); PG8_WAIT_L(0); PG8_BAR; PG8_MMA(0, 0, At, B0); PG8_MMA(0, 1, At, B1); PG8_BAR; PG8_SCHED;
;             PG8_LDA(At, 0, 1); PG8_STAGE(PG8_SB(0, 0), b2, voffB); PG8_STAGE(PG8_SB(0, 1), b2 + hstepB, voffB); PG8_STAGE(PG8_SA(0, 0), a2, voffA);
;             PG8_WAIT_V(8); PG8_WAIT_L(0); PG8_BAR; PG8_MMA(1, 0, At, B0); PG8_MMA(1, 1, At, B1); PG8_BAR; PG8_SCHED;
.Lzs_13:
	s_cbranch_vccnz .LBB0_4142
	s_and_b64 s[28:29], s[0:1], exec
	s_cselect_b32 s15, s19, s27
	s_cselect_b32 s17, s18, s26
	s_cselect_b32 s65, s21, s25
	s_cselect_b32 s66, s20, s24
	s_add_u32 s67, s24, 0x100
	s_addc_u32 s68, s25, 0
	s_add_u32 s24, s26, 0x40080
	s_addc_u32 s25, s27, 0
	s_mov_b32 s26, 0
	v_add_u32_e32 v160, s35, v164
	ds_read_b128 v[122:125], v160
	ds_read_b128 v[126:129], v160 offset:1024
	ds_read_b128 v[130:133], v160 offset:2048
	ds_read_b128 v[170:173], v160 offset:3072
	v_add_u32_e32 v160, s36, v164
	ds_read_b128 v[174:177], v160
	ds_read_b128 v[178:181], v160 offset:1024
	ds_read_b128 v[182:185], v160 offset:2048
	ds_read_b128 v[186:189], v160 offset:3072
	s_add_i32 s69, s26, 2
	s_add_u32 s27, s24, 0xfffc0080
	s_addc_u32 s28, s25, -1
	s_cmp_eq_u32 s61, s26
	s_cselect_b32 s26, s66, s67
	s_cselect_b32 s29, s15, s28
	s_cselect_b32 s28, s17, s27
	s_cselect_b32 s27, s65, s68
	s_add_i32 m0, s46, 0xc000
	ds_read_b128 v[190:193], v167
	ds_read_b128 v[194:197], v167 offset:1024
	ds_read_b128 v[198:201], v167 offset:2048
	ds_read_b128 v[202:205], v167 offset:3072
	ds_read_b128 v[206:209], v167 offset:4096
	ds_read_b128 v[210:213], v167 offset:5120
	ds_read_b128 v[214:217], v167 offset:6144
	ds_read_b128 v[218:221], v167 offset:7168
	global_load_lds_dwordx4 v154, s[24:25]
	s_add_i32 m0, s46, 0xe000
	s_nop 0
	global_load_lds_dwordx4 v152, s[24:25]
	s_waitcnt vmcnt(8) lgkmcnt(0)
	s_barrier
	s_setprio 1
	v_mfma_i32_16x16x64_i8 v[134:137], v[122:125], v[190:193], 0
	v_mfma_i32_16x16x64_i8 v[114:117], v[130:133], v[190:193], 0
	v_mfma_i32_16x16x64_i8 v[106:109], v[122:125], v[198:201], 0
	v_mfma_i32_16x16x64_i8 v[98:101], v[130:133], v[198:201], 0
	v_mfma_i32_16x16x64_i8 v[90:93], v[122:125], v[206:209], 0
	v_mfma_i32_16x16x64_i8 v[82:85], v[130:133], v[206:209], 0
	v_mfma_i32_16x16x64_i8 v[74:77], v[122:125], v[214:217], 0
	v_mfma_i32_16x16x64_i8 v[66:69], v[130:133], v[214:217], 0
	v_mfma_i32_16x16x64_i8 v[134:137], v[126:129], v[194:197], v[134:137]
	v_mfma_i32_16x16x64_i8 v[114:117], v[170:173], v[194:197], v[114:117]
	v_mfma_i32_16x16x64_i8 v[106:109], v[126:129], v[202:205], v[106:109]
	v_mfma_i32_16x16x64_i8 v[98:101], v[170:173], v[202:205], v[98:101]
	v_mfma_i32_16x16x64_i8 v[90:93], v[126:129], v[210:213], v[90:93]
	v_mfma_i32_16x16x64_i8 v[82:85], v[170:173], v[210:213], v[82:85]
	v_mfma_i32_16x16x64_i8 v[74:77], v[126:129], v[218:221], v[74:77]
	v_mfma_i32_16x16x64_i8 v[66:69], v[170:173], v[218:221], v[66:69]
	s_setprio 0
	s_setprio 1
	v_mfma_i32_16x16x64_i8 v[138:141], v[174:177], v[190:193], 0
	v_mfma_i32_16x16x64_i8 v[118:121], v[182:185], v[190:193], 0
	v_mfma_i32_16x16x64_i8 v[110:113], v[174:177], v[198:201], 0
	v_mfma_i32_16x16x64_i8 v[102:105], v[182:185], v[198:201], 0
	v_mfma_i32_16x16x64_i8 v[94:97], v[174:177], v[206:209], 0
	v_mfma_i32_16x16x64_i8 v[86:89], v[182:185], v[206:209], 0
	v_mfma_i32_16x16x64_i8 v[78:81], v[174:177], v[214:217], 0
	v_mfma_i32_16x16x64_i8 v[70:73], v[182:185], v[214:217], 0
	v_mfma_i32_16x16x64_i8 v[138:141], v[178:181], v[194:197], v[138:141]
	v_mfma_i32_16x16x64_i8 v[118:121], v[186:189], v[194:197], v[118:121]
	v_mfma_i32_16x16x64_i8 v[110:113], v[178:181], v[202:205], v[110:113]
	v_mfma_i32_16x16x64_i8 v[102:105], v[186:189], v[202:205], v[102:105]
	v_mfma_i32_16x16x64_i8 v[94:97], v[178:181], v[210:213], v[94:97]
	v_mfma_i32_16x16x64_i8 v[86:89], v[186:189], v[210:213], v[86:89]
	v_mfma_i32_16x16x64_i8 v[78:81], v[178:181], v[218:221], v[78:81]
	v_mfma_i32_16x16x64_i8 v[70:73], v[186:189], v[218:221], v[70:73]
	s_setprio 0
	s_barrier
	s_mov_b32 m0, s23
	s_add_u32 s98, s26, 0x80
	s_addc_u32 s99, s27, 0
	s_add_u32 s70, s26, 0x40000
	ds_read_b128 v[190:193], v167 offset:16384
	ds_read_b128 v[194:197], v167 offset:17408
	ds_read_b128 v[198:201], v167 offset:18432
	ds_read_b128 v[202:205], v167 offset:19456
	ds_read_b128 v[206:209], v167 offset:20480
	ds_read_b128 v[210:213], v167 offset:21504
	ds_read_b128 v[214:217], v167 offset:22528
	ds_read_b128 v[218:221], v167 offset:23552
	global_load_lds_dwordx4 v144, s[26:27]
	s_mov_b32 m0, s43
	s_addc_u32 s71, s27, 0
	global_load_lds_dwordx4 v148, s[26:27]
	s_mov_b32 m0, s44
	s_nop 0
	global_load_lds_dwordx4 v144, s[70:71]
	s_mov_b32 m0, s45
	s_nop 0
	global_load_lds_dwordx4 v148, s[70:71]
	s_add_u32 s100, s28, 0x80
	s_addc_u32 s101, s29, 0
	s_mov_b32 m0, s46
	s_nop 0
	global_load_lds_dwordx4 v142, s[28:29]
	s_mov_b32 m0, s47
	s_nop 0
	global_load_lds_dwordx4 v146, s[28:29]
	s_waitcnt vmcnt(8) lgkmcnt(0)
	s_barrier
	s_setprio 1
	v_mfma_i32_16x16x64_i8 v[58:61], v[122:125], v[190:193], 0
	v_mfma_i32_16x16x64_i8 v[50:53], v[130:133], v[190:193], 0
	v_mfma_i32_16x16x64_i8 v[42:45], v[122:125], v[198:201], 0
	v_mfma_i32_16x16x64_i8 v[34:37], v[130:133], v[198:201], 0
	v_mfma_i32_16x16x64_i8 v[26:29], v[122:125], v[206:209], 0
	v_mfma_i32_16x16x64_i8 v[18:21], v[130:133], v[206:209], 0
	v_mfma_i32_16x16x64_i8 v[10:13], v[122:125], v[214:217], 0
	v_mfma_i32_16x16x64_i8 v[2:5], v[130:133], v[214:217], 0
	v_mfma_i32_16x16x64_i8 v[58:61], v[126:129], v[194:197], v[58:61]
	v_mfma_i32_16x16x64_i8 v[50:53], v[170:173], v[194:197], v[50:53]
	v_mfma_i32_16x16x64_i8 v[42:45], v[126:129], v[202:205], v[42:45]
	v_mfma_i32_16x16x64_i8 v[34:37], v[170:173], v[202:205], v[34:37]
	v_mfma_i32_16x16x64_i8 v[26:29], v[126:129], v[210:213], v[26:29]
	v_mfma_i32_16x16x64_i8 v[18:21], v[170:173], v[210:213], v[18:21]
	v_mfma_i32_16x16x64_i8 v[10:13], v[126:129], v[218:221], v[10:13]
	v_mfma_i32_16x16x64_i8 v[2:5], v[170:173], v[218:221], v[2:5]
	s_setprio 0
	s_setprio 1
	v_mfma_i32_16x16x64_i8 v[62:65], v[174:177], v[190:193], 0
	v_mfma_i32_16x16x64_i8 v[54:57], v[182:185], v[190:193], 0
	v_mfma_i32_16x16x64_i8 v[46:49], v[174:177], v[198:201], 0
	v_mfma_i32_16x16x64_i8 v[38:41], v[182:185], v[198:201], 0
	v_mfma_i32_16x16x64_i8 v[30:33], v[174:177], v[206:209], 0
	v_mfma_i32_16x16x64_i8 v[22:25], v[182:185], v[206:209], 0
	v_mfma_i32_16x16x64_i8 v[14:17], v[174:177], v[214:217], 0
	v_mfma_i32_16x16x64_i8 v[6:9], v[182:185], v[214:217], 0
	v_mfma_i32_16x16x64_i8 v[62:65], v[178:181], v[194:197], v[62:65]
	v_mfma_i32_16x16x64_i8 v[54:57], v[186:189], v[194:197], v[54:57]
	v_mfma_i32_16x16x64_i8 v[46:49], v[178:181], v[202:205], v[46:49]
	v_mfma_i32_16x16x64_i8 v[38:41], v[186:189], v[202:205], v[38:41]
	v_mfma_i32_16x16x64_i8 v[30:33], v[178:181], v[210:213], v[30:33]
	v_mfma_i32_16x16x64_i8 v[22:25], v[186:189], v[210:213], v[22:25]
	v_mfma_i32_16x16x64_i8 v[14:17], v[178:181], v[218:221], v[14:17]
	v_mfma_i32_16x16x64_i8 v[6:9], v[186:189], v[218:221], v[6:9]
	s_setprio 0
	s_barrier
; #define PG8_STAGE(bufoff, gbase, voff) do { _Pragma("unroll") for (int _i = 0; _i < 2; ++_i) \
;         __builtin_amdgcn_global_load_lds((const unsigned*)((const char*)(gbase) + (voff)[_i]), (PG8_LAS unsigned*)(lds + (bufoff) + ldsw + _i * 8192), 16, 0, 0); } while (0)
; #define PG8_LDA(dst, b, h) do { if constexpr (DT != 1) { _Pragma("unroll") for (int m = 0; m < 4; ++m) _Pragma("unroll") for (int k = 0; k < 2; ++k) dst[m][k] = *(const PG8_LAS bf16x8*)(lds + PG8_SA(b, h) + aoff + m * 2048 + k * 1024); } \
;         else { _Pragma("unroll") for (int m = 0; m < 4; ++m) dst##8[m] = ld32(lds + PG8_SA(b, h) + aoff + m * 2048); } } while (0)
; #define PG8_LDB(dst, b, h) do { if constexpr (DT != 1) { _Pragma("unroll") for (int n = 0; n < 2; ++n) _Pragma("unroll") for (int k = 0; k < 2; ++k) dst[n][k] = *(const PG8_LAS bf16x8*)(lds + PG8_SB(b, h) + boff + n * 2048 + k * 1024); } \
;         else { _Pragma("unroll") for (int n = 0; n < 2; ++n) dst##8[n] = ld32(lds + PG8_SB(b, h) + boff + n * 2048); } } while (0)
; #define PG8_WAIT_V(n) asm volatile("s_waitcnt vmcnt(" #n ")" ::: "memory")
; #define PG8_WAIT_L(n) asm volatile("s_waitcnt lgkmcnt(" #n ")" ::: "memory")
; #define PG8_BAR __builtin_amdgcn_s_barrier()
; #define PG8_SCHED __builtin_amdgcn_sched_barrier(0)
;     ...
;             PG8_LDB(B0, 1, 0); PG8_LDB(B1, 1, 1); PG8_SCHED; PG8_LDA(At, 1, 0); PG8_STAGE(PG8_SA(0, 1), a2 + hstepA, voffA);
;             PG8_WAIT_V(8); PG8_WAIT_L(0); PG8_BAR; PG8_MMA(0, 0, At, B0); PG8_MMA(0, 1, At, B1); PG8_BAR; PG8_SCHED;
;             PG8_LDA(At, 1, 1); PG8_STAGE(PG8_SB(1, 0), b3, voffB); PG8_STAGE(PG8_SB(1, 1), b3 + hstepB, voffB); PG8_STAGE(PG8_SA(1, 0), a3, voffA);
;             PG8_WAIT_V(8); PG8_WAIT_L(0); PG8_BAR; PG8_MMA(1, 0, At, B0); PG8_MMA(1, 1, At, B1); PG8_BAR; PG8_SCHED;
	v_add_u32_e32 v160, s51, v164
	ds_read_b128 v[122:125], v160
	ds_read_b128 v[126:129], v160 offset:1024
	ds_read_b128 v[130:133], v160 offset:2048
	ds_read_b128 v[170:173], v160 offset:3072
	v_add_u32_e32 v160, s52, v164
	ds_read_b128 v[174:177], v160
	ds_read_b128 v[178:181], v160 offset:1024
	ds_read_b128 v[182:185], v160 offset:2048
	ds_read_b128 v[186:189], v160 offset:3072
	s_add_u32 s28, s28, 0x40000
	s_addc_u32 s29, s29, 0
	s_mov_b32 m0, s48
	ds_read_b128 v[190:193], v167 offset:32768
	ds_read_b128 v[194:197], v167 offset:33792
	ds_read_b128 v[198:201], v167 offset:34816
	ds_read_b128 v[202:205], v167 offset:35840
	ds_read_b128 v[206:209], v167 offset:36864
	ds_read_b128 v[210:213], v167 offset:37888
	ds_read_b128 v[214:217], v167 offset:38912
	ds_read_b128 v[218:221], v167 offset:39936
	global_load_lds_dwordx4 v142, s[28:29]
	s_mov_b32 m0, s49
	s_nop 0
	global_load_lds_dwordx4 v146, s[28:29]
	s_waitcnt vmcnt(8) lgkmcnt(0)
	s_barrier
	s_setprio 1
	v_mfma_i32_16x16x64_i8 v[134:137], v[122:125], v[190:193], v[134:137]
	v_mfma_i32_16x16x64_i8 v[114:117], v[130:133], v[190:193], v[114:117]
	v_mfma_i32_16x16x64_i8 v[106:109], v[122:125], v[198:201], v[106:109]
	v_mfma_i32_16x16x64_i8 v[98:101], v[130:133], v[198:201], v[98:101]
	v_mfma_i32_16x16x64_i8 v[90:93], v[122:125], v[206:209], v[90:93]
	v_mfma_i32_16x16x64_i8 v[82:85], v[130:133], v[206:209], v[82:85]
	v_mfma_i32_16x16x64_i8 v[74:77], v[122:125], v[214:217], v[74:77]
	v_mfma_i32_16x16x64_i8 v[66:69], v[130:133], v[214:217], v[66:69]
	v_mfma_i32_16x16x64_i8 v[134:137], v[126:129], v[194:197], v[134:137]
	v_mfma_i32_16x16x64_i8 v[114:117], v[170:173], v[194:197], v[114:117]
	v_mfma_i32_16x16x64_i8 v[106:109], v[126:129], v[202:205], v[106:109]
	v_mfma_i32_16x16x64_i8 v[98:101], v[170:173], v[202:205], v[98:101]
	v_mfma_i32_16x16x64_i8 v[90:93], v[126:129], v[210:213], v[90:93]
	v_mfma_i32_16x16x64_i8 v[82:85], v[170:173], v[210:213], v[82:85]
	v_mfma_i32_16x16x64_i8 v[74:77], v[126:129], v[218:221], v[74:77]
	v_mfma_i32_16x16x64_i8 v[66:69], v[170:173], v[218:221], v[66:69]
	s_setprio 0
	s_setprio 1
	v_mfma_i32_16x16x64_i8 v[138:141], v[174:177], v[190:193], v[138:141]
	v_mfma_i32_16x16x64_i8 v[118:121], v[182:185], v[190:193], v[118:121]
	v_mfma_i32_16x16x64_i8 v[110:113], v[174:177], v[198:201], v[110:113]
	v_mfma_i32_16x16x64_i8 v[102:105], v[182:185], v[198:201], v[102:105]
	v_mfma_i32_16x16x64_i8 v[94:97], v[174:177], v[206:209], v[94:97]
	v_mfma_i32_16x16x64_i8 v[86:89], v[182:185], v[206:209], v[86:89]
	v_mfma_i32_16x16x64_i8 v[78:81], v[174:177], v[214:217], v[78:81]
	v_mfma_i32_16x16x64_i8 v[70:73], v[182:185], v[214:217], v[70:73]
	v_mfma_i32_16x16x64_i8 v[138:141], v[178:181], v[194:197], v[138:141]
	v_mfma_i32_16x16x64_i8 v[118:121], v[186:189], v[194:197], v[118:121]
	v_mfma_i32_16x16x64_i8 v[110:113], v[178:181], v[202:205], v[110:113]
	v_mfma_i32_16x16x64_i8 v[102:105], v[186:189], v[202:205], v[102:105]
	v_mfma_i32_16x16x64_i8 v[94:97], v[178:181], v[210:213], v[94:97]
	v_mfma_i32_16x16x64_i8 v[86:89], v[186:189], v[210:213], v[86:89]
	v_mfma_i32_16x16x64_i8 v[78:81], v[178:181], v[218:221], v[78:81]
	v_mfma_i32_16x16x64_i8 v[70:73], v[186:189], v[218:221], v[70:73]
	s_setprio 0
	s_barrier
	s_mov_b32 m0, s55
	s_add_u32 s26, s26, 0x40080
	ds_read_b128 v[190:193], v167 offset:49152
	ds_read_b128 v[194:197], v167 offset:50176
	ds_read_b128 v[198:201], v167 offset:51200
	ds_read_b128 v[202:205], v167 offset:52224
	ds_read_b128 v[206:209], v167 offset:53248
	ds_read_b128 v[210:213], v167 offset:54272
	ds_read_b128 v[214:217], v167 offset:55296
	ds_read_b128 v[218:221], v167 offset:56320
	global_load_lds_dwordx4 v144, s[98:99]
	s_mov_b32 m0, s56
	s_addc_u32 s27, s27, 0
	global_load_lds_dwordx4 v148, s[98:99]
	s_mov_b32 m0, s59
	s_nop 0
	global_load_lds_dwordx4 v144, s[26:27]
	s_mov_b32 m0, s60
	s_nop 0
	global_load_lds_dwordx4 v148, s[26:27]
	s_mov_b32 m0, s57
	s_nop 0
	global_load_lds_dwordx4 v142, s[100:101]
	s_mov_b32 m0, s58
	s_nop 0
	global_load_lds_dwordx4 v146, s[100:101]
	s_waitcnt vmcnt(8) lgkmcnt(0)
	s_barrier
	s_setprio 1
	v_mfma_i32_16x16x64_i8 v[58:61], v[122:125], v[190:193], v[58:61]
	v_mfma_i32_16x16x64_i8 v[50:53], v[130:133], v[190:193], v[50:53]
	v_mfma_i32_16x16x64_i8 v[42:45], v[122:125], v[198:201], v[42:45]
	v_mfma_i32_16x16x64_i8 v[34:37], v[130:133], v[198:201], v[34:37]
	v_mfma_i32_16x16x64_i8 v[26:29], v[122:125], v[206:209], v[26:29]
	v_mfma_i32_16x16x64_i8 v[18:21], v[130:133], v[206:209], v[18:21]
	v_mfma_i32_16x16x64_i8 v[10:13], v[122:125], v[214:217], v[10:13]
	v_mfma_i32_16x16x64_i8 v[2:5], v[130:133], v[214:217], v[2:5]
	v_mfma_i32_16x16x64_i8 v[58:61], v[126:129], v[194:197], v[58:61]
	v_mfma_i32_16x16x64_i8 v[50:53], v[170:173], v[194:197], v[50:53]
	v_mfma_i32_16x16x64_i8 v[42:45], v[126:129], v[202:205], v[42:45]
	v_mfma_i32_16x16x64_i8 v[34:37], v[170:173], v[202:205], v[34:37]
	v_mfma_i32_16x16x64_i8 v[26:29], v[126:129], v[210:213], v[26:29]
	v_mfma_i32_16x16x64_i8 v[18:21], v[170:173], v[210:213], v[18:21]
	v_mfma_i32_16x16x64_i8 v[10:13], v[126:129], v[218:221], v[10:13]
	v_mfma_i32_16x16x64_i8 v[2:5], v[170:173], v[218:221], v[2:5]
	s_setprio 0
	s_setprio 1
	v_mfma_i32_16x16x64_i8 v[62:65], v[174:177], v[190:193], v[62:65]
	v_mfma_i32_16x16x64_i8 v[54:57], v[182:185], v[190:193], v[54:57]
	v_mfma_i32_16x16x64_i8 v[46:49], v[174:177], v[198:201], v[46:49]
	v_mfma_i32_16x16x64_i8 v[38:41], v[182:185], v[198:201], v[38:41]
	v_mfma_i32_16x16x64_i8 v[30:33], v[174:177], v[206:209], v[30:33]
	v_mfma_i32_16x16x64_i8 v[22:25], v[182:185], v[206:209], v[22:25]
	v_mfma_i32_16x16x64_i8 v[14:17], v[174:177], v[214:217], v[14:17]
	v_mfma_i32_16x16x64_i8 v[6:9], v[182:185], v[214:217], v[6:9]
	v_mfma_i32_16x16x64_i8 v[62:65], v[178:181], v[194:197], v[62:65]
	v_mfma_i32_16x16x64_i8 v[54:57], v[186:189], v[194:197], v[54:57]
	v_mfma_i32_16x16x64_i8 v[46:49], v[178:181], v[202:205], v[46:49]
	v_mfma_i32_16x16x64_i8 v[38:41], v[186:189], v[202:205], v[38:41]
	v_mfma_i32_16x16x64_i8 v[30:33], v[178:181], v[210:213], v[30:33]
	v_mfma_i32_16x16x64_i8 v[22:25], v[186:189], v[210:213], v[22:25]
	v_mfma_i32_16x16x64_i8 v[14:17], v[178:181], v[218:221], v[14:17]
	v_mfma_i32_16x16x64_i8 v[6:9], v[186:189], v[218:221], v[6:9]
	s_setprio 0
	s_barrier
	s_add_u32 s67, s67, 0x100
	s_addc_u32 s68, s68, 0
	s_add_u32 s24, s24, 0x100
	s_addc_u32 s25, s25, 0
	s_cmp_ge_i32 s69, s54
	s_mov_b32 s26, s69
	s_cbranch_scc0 .LBB0_4141
	s_branch .LBB0_4142

; #define PG8_STAGE(bufoff, gbase, voff) do { _Pragma("unroll") for (int _i = 0; _i < 2; ++_i) \
;         __builtin_amdgcn_global_load_lds((const unsigned*)((const char*)(gbase) + (voff)[_i]), (PG8_LAS unsigned*)(lds + (bufoff) + ldsw + _i * 8192), 16, 0, 0); } while (0)
; #define PG8_LDA(dst, b, h) do { if constexpr (DT != 1) { _Pragma("unroll") for (int m = 0; m < 4; ++m) _Pragma("unroll") for (int k = 0; k < 2; ++k) dst[m][k] = *(const PG8_LAS bf16x8*)(lds + PG8_SA(b, h) + aoff + m * 2048 + k * 1024); } \
;         else { _Pragma("unroll") for (int m = 0; m < 4; ++m) dst##8[m] = ld32(lds + PG8_SA(b, h) + aoff + m * 2048); } } while (0)
; #define PG8_LDB(dst, b, h) do { if constexpr (DT != 1) { _Pragma("unroll") for (int n = 0; n < 2; ++n) _Pragma("unroll") for (int k = 0; k < 2; ++k) dst[n][k] = *(const PG8_LAS bf16x8*)(lds + PG8_SB(b, h) + boff + n * 2048 + k * 1024); } \
;         else { _Pragma("unroll") for (int n = 0; n < 2; ++n) dst##8[n] = ld32(lds + PG8_SB(b, h) + boff + n * 2048); } } while (0)
; #define PG8_WAIT_V(n) asm volatile("s_waitcnt vmcnt(" #n ")" ::: "memory")
; #define PG8_WAIT_L(n) asm volatile("s_waitcnt lgkmcnt(" #n ")" ::: "memory")
; #define PG8_BAR __builtin_amdgcn_s_barrier()
; #define PG8_SCHED __builtin_amdgcn_sched_barrier(0)
;     ...
;         for (int t = 0; t < nt; t += 2) {
;             const bool last = (t == nt - 2);
;             const char* a1 = cA + (size_t)(t + 1) * kstep;
;             const char* a2 = last ? nA : cA + (size_t)(t + 2) * kstep; const char* b2 = last ? nB : cB + (size_t)(t + 2) * kstep;
;             const char* a3 = a2 + kstep; const char* b3 = b2 + kstep;
;             if (last && has_next) S.a_ready(nxt);
;             if constexpr (SP2) {
;             PG8_LDB(B0, 0, 0); PG8_LDB(B1, 0, 1); PG8_SCHED; PG8_LDA(At, 0, 0); PG8_STAGE(PG8_SA(1, 1), a1 + hstepA, voffA);
;             PG8_WAIT_V(8); PG8_WAIT_L(0); PG8_BAR; PG8_MMA(0, 0, At, B0); PG8_MMA(0, 1, At, B1); PG8_BAR; PG8_SCHED;
;             PG8_LDA(At, 0, 1); PG8_STAGE(PG8_SB(0, 0), b2, voffB); PG8_STAGE(PG8_SB(0, 1), b2 + hstepB, voffB); PG8_STAGE(PG8_SA(0, 0), a2, voffA);
;             PG8_WAIT_V(8); PG8_WAIT_L(0); PG8_BAR; PG8_MMA(1, 0, At, B0); PG8_MMA(1, 1, At, B1); PG8_BAR; PG8_SCHED;
.Lzs_14:
	s_cbranch_vccnz .LBB0_4218
	s_add_u32 s66, s30, 0x100
	s_addc_u32 s67, s31, 0
	s_mov_b32 s34, 0
	ds_read_b128 v[18:21], v187
	ds_read_b128 v[22:25], v187 offset:16
	ds_read_b128 v[26:29], v187 offset:2048
	ds_read_b128 v[30:33], v187 offset:2064
	ds_read_b128 v[2:5], v188
	ds_read_b128 v[6:9], v188 offset:16
	ds_read_b128 v[10:13], v188 offset:2048
	ds_read_b128 v[14:17], v188 offset:2064
	s_add_i32 s68, s34, 2
	s_add_u32 s30, s28, 0x100
	s_addc_u32 s31, s29, 0
	s_cmp_eq_u32 s59, s34
	s_cselect_b32 s34, s26, s66
	s_cselect_b32 s37, s3, s31
	s_cselect_b32 s36, s2, s30
	s_cselect_b32 s35, s27, s67
	v_lshl_add_u64 v[218:219], s[28:29], 0, v[172:173]
	s_add_i32 m0, s47, 0xc000
	ds_read_b128 v[178:181], v189
	ds_read_b128 v[182:185], v189 offset:16
	ds_read_b128 v[194:197], v189 offset:2048
	ds_read_b128 v[198:201], v189 offset:2064
	ds_read_b128 v[202:205], v189 offset:4096
	ds_read_b128 v[206:209], v189 offset:4112
	ds_read_b128 v[210:213], v189 offset:6144
	ds_read_b128 v[214:217], v189 offset:6160
	global_load_lds_dwordx4 v[218:219], off
	v_lshl_add_u64 v[218:219], s[28:29], 0, v[170:171]
	s_add_i32 m0, s47, 0xe000
	s_nop 0
	global_load_lds_dwordx4 v[218:219], off
	s_waitcnt vmcnt(8) lgkmcnt(0)
	s_barrier
	s_setprio 1
	v_mfma_scale_f32_16x16x128_f8f6f4 v[158:161], v[18:25], v[178:185], 0, v190, v190 op_sel_hi:[0,0,0]
	v_mfma_scale_f32_16x16x128_f8f6f4 v[154:157], v[26:33], v[178:185], 0, v190, v190 op_sel_hi:[0,0,0]
	v_mfma_scale_f32_16x16x128_f8f6f4 v[150:153], v[18:25], v[194:201], 0, v190, v190 op_sel_hi:[0,0,0]
	v_mfma_scale_f32_16x16x128_f8f6f4 v[146:149], v[26:33], v[194:201], 0, v190, v190 op_sel_hi:[0,0,0]
	v_mfma_scale_f32_16x16x128_f8f6f4 v[126:129], v[18:25], v[202:209], 0, v190, v190 op_sel_hi:[0,0,0]
	v_mfma_scale_f32_16x16x128_f8f6f4 v[122:125], v[26:33], v[202:209], 0, v190, v190 op_sel_hi:[0,0,0]
	v_mfma_scale_f32_16x16x128_f8f6f4 v[118:121], v[18:25], v[210:217], 0, v190, v190 op_sel_hi:[0,0,0]
	v_mfma_scale_f32_16x16x128_f8f6f4 v[110:113], v[26:33], v[210:217], 0, v190, v190 op_sel_hi:[0,0,0]
	s_setprio 0
	s_setprio 1
	v_mfma_scale_f32_16x16x128_f8f6f4 v[142:145], v[2:9], v[178:185], 0, v190, v190 op_sel_hi:[0,0,0]
	v_mfma_scale_f32_16x16x128_f8f6f4 v[138:141], v[10:17], v[178:185], 0, v190, v190 op_sel_hi:[0,0,0]
	v_mfma_scale_f32_16x16x128_f8f6f4 v[134:137], v[2:9], v[194:201], 0, v190, v190 op_sel_hi:[0,0,0]
	v_mfma_scale_f32_16x16x128_f8f6f4 v[130:133], v[10:17], v[194:201], 0, v190, v190 op_sel_hi:[0,0,0]
	v_mfma_scale_f32_16x16x128_f8f6f4 v[114:117], v[2:9], v[202:209], 0, v190, v190 op_sel_hi:[0,0,0]
	v_mfma_scale_f32_16x16x128_f8f6f4 v[106:109], v[10:17], v[202:209], 0, v190, v190 op_sel_hi:[0,0,0]
	v_mfma_scale_f32_16x16x128_f8f6f4 v[102:105], v[2:9], v[210:217], 0, v190, v190 op_sel_hi:[0,0,0]
	v_mfma_scale_f32_16x16x128_f8f6f4 v[98:101], v[10:17], v[210:217], 0, v190, v190 op_sel_hi:[0,0,0]
	s_setprio 0
	s_barrier
	s_mov_b32 m0, s43
	s_add_u32 s98, s34, 0x80
	s_addc_u32 s99, s35, 0
	s_add_u32 s28, s34, 0xb0000
	ds_read_b128 v[194:197], v189 offset:16384
	ds_read_b128 v[198:201], v189 offset:16400
	ds_read_b128 v[202:205], v189 offset:18432
	ds_read_b128 v[206:209], v189 offset:18448
	ds_read_b128 v[210:213], v189 offset:20480
	ds_read_b128 v[214:217], v189 offset:20496
	ds_read_b128 v[218:221], v189 offset:22528
	ds_read_b128 v[222:225], v189 offset:22544
	global_load_lds_dwordx4 v164, s[34:35]
	s_mov_b32 m0, s44
	s_addc_u32 s29, s35, 0
	global_load_lds_dwordx4 v168, s[34:35]
	s_mov_b32 m0, s45
	s_nop 0
	global_load_lds_dwordx4 v164, s[28:29]
	s_mov_b32 m0, s46
	s_nop 0
	global_load_lds_dwordx4 v168, s[28:29]
	s_add_u32 s100, s36, 0x80
	s_addc_u32 s101, s37, 0
	s_mov_b32 m0, s47
	s_nop 0
	global_load_lds_dwordx4 v162, s[36:37]
	s_mov_b32 m0, s48
	s_nop 0
	global_load_lds_dwordx4 v166, s[36:37]
	s_waitcnt vmcnt(8) lgkmcnt(0)
	s_barrier
	s_setprio 1
	v_mfma_scale_f32_16x16x128_f8f6f4 v[94:97], v[18:25], v[194:201], 0, v190, v190 op_sel_hi:[0,0,0]
	v_mfma_scale_f32_16x16x128_f8f6f4 v[90:93], v[26:33], v[194:201], 0, v190, v190 op_sel_hi:[0,0,0]
	v_mfma_scale_f32_16x16x128_f8f6f4 v[78:81], v[18:25], v[202:209], 0, v190, v190 op_sel_hi:[0,0,0]
	v_mfma_scale_f32_16x16x128_f8f6f4 v[74:77], v[26:33], v[202:209], 0, v190, v190 op_sel_hi:[0,0,0]
	v_mfma_scale_f32_16x16x128_f8f6f4 v[226:229], v[18:25], v[210:217], 0, v190, v190 op_sel_hi:[0,0,0]
	v_mfma_scale_f32_16x16x128_f8f6f4 v[230:233], v[26:33], v[210:217], 0, v190, v190 op_sel_hi:[0,0,0]
	v_mfma_scale_f32_16x16x128_f8f6f4 v[234:237], v[18:25], v[218:225], 0, v190, v190 op_sel_hi:[0,0,0]
	v_mfma_scale_f32_16x16x128_f8f6f4 v[238:241], v[26:33], v[218:225], 0, v190, v190 op_sel_hi:[0,0,0]
	s_setprio 0
	s_setprio 1
	v_mfma_scale_f32_16x16x128_f8f6f4 v[86:89], v[2:9], v[194:201], 0, v190, v190 op_sel_hi:[0,0,0]
	v_mfma_scale_f32_16x16x128_f8f6f4 v[82:85], v[10:17], v[194:201], 0, v190, v190 op_sel_hi:[0,0,0]
	v_mfma_scale_f32_16x16x128_f8f6f4 v[70:73], v[2:9], v[202:209], 0, v190, v190 op_sel_hi:[0,0,0]
	v_mfma_scale_f32_16x16x128_f8f6f4 v[66:69], v[10:17], v[202:209], 0, v190, v190 op_sel_hi:[0,0,0]
	v_mfma_scale_f32_16x16x128_f8f6f4 v[242:245], v[2:9], v[210:217], 0, v190, v190 op_sel_hi:[0,0,0]
	v_mfma_scale_f32_16x16x128_f8f6f4 v[210:213], v[10:17], v[210:217], 0, v190, v190 op_sel_hi:[0,0,0]
	v_mfma_scale_f32_16x16x128_f8f6f4 v[214:217], v[2:9], v[218:225], 0, v190, v190 op_sel_hi:[0,0,0]
	v_mfma_scale_f32_16x16x128_f8f6f4 v[218:221], v[10:17], v[218:225], 0, v190, v190 op_sel_hi:[0,0,0]
	s_setprio 0
	s_barrier
; #define PG8_STAGE(bufoff, gbase, voff) do { _Pragma("unroll") for (int _i = 0; _i < 2; ++_i) \
;         __builtin_amdgcn_global_load_lds((const unsigned*)((const char*)(gbase) + (voff)[_i]), (PG8_LAS unsigned*)(lds + (bufoff) + ldsw + _i * 8192), 16, 0, 0); } while (0)
; #define PG8_LDA(dst, b, h) do { if constexpr (DT != 1) { _Pragma("unroll") for (int m = 0; m < 4; ++m) _Pragma("unroll") for (int k = 0; k < 2; ++k) dst[m][k] = *(const PG8_LAS bf16x8*)(lds + PG8_SA(b, h) + aoff + m * 2048 + k * 1024); } \
;         else { _Pragma("unroll") for (int m = 0; m < 4; ++m) dst##8[m] = ld32(lds + PG8_SA(b, h) + aoff + m * 2048); } } while (0)
; #define PG8_LDB(dst, b, h) do { if constexpr (DT != 1) { _Pragma("unroll") for (int n = 0; n < 2; ++n) _Pragma("unroll") for (int k = 0; k < 2; ++k) dst[n][k] = *(const PG8_LAS bf16x8*)(lds + PG8_SB(b, h) + boff + n * 2048 + k * 1024); } \
;         else { _Pragma("unroll") for (int n = 0; n < 2; ++n) dst##8[n] = ld32(lds + PG8_SB(b, h) + boff + n * 2048); } } while (0)
; #define PG8_WAIT_V(n) asm volatile("s_waitcnt vmcnt(" #n ")" ::: "memory")
; #define PG8_WAIT_L(n) asm volatile("s_waitcnt lgkmcnt(" #n ")" ::: "memory")
; #define PG8_BAR __builtin_amdgcn_s_barrier()
; #define PG8_SCHED __builtin_amdgcn_sched_barrier(0)
;     ...
;             PG8_LDB(B0, 1, 0); PG8_LDB(B1, 1, 1); PG8_SCHED; PG8_LDA(At, 1, 0); PG8_STAGE(PG8_SA(0, 1), a2 + hstepA, voffA);
;             PG8_WAIT_V(8); PG8_WAIT_L(0); PG8_BAR; PG8_MMA(0, 0, At, B0); PG8_MMA(0, 1, At, B1); PG8_BAR; PG8_SCHED;
;             PG8_LDA(At, 1, 1); PG8_STAGE(PG8_SB(1, 0), b3, voffB); PG8_STAGE(PG8_SB(1, 1), b3 + hstepB, voffB); PG8_STAGE(PG8_SA(1, 0), a3, voffA);
;             PG8_WAIT_V(8); PG8_WAIT_L(0); PG8_BAR; PG8_MMA(1, 0, At, B0); PG8_MMA(1, 1, At, B1); PG8_BAR; PG8_SCHED;
	ds_read_b128 v[2:5], v191
	ds_read_b128 v[6:9], v191 offset:16
	ds_read_b128 v[10:13], v191 offset:2048
	ds_read_b128 v[14:17], v191 offset:2064
	ds_read_b128 v[18:21], v192
	ds_read_b128 v[22:25], v192 offset:16
	ds_read_b128 v[26:29], v192 offset:2048
	ds_read_b128 v[30:33], v192 offset:2064
	s_add_u32 s28, s36, 0xb0000
	s_addc_u32 s29, s37, 0
	s_mov_b32 m0, s49
	ds_read_b128 v[34:37], v189 offset:32768
	ds_read_b128 v[38:41], v189 offset:32784
	ds_read_b128 v[42:45], v189 offset:34816
	ds_read_b128 v[46:49], v189 offset:34832
	ds_read_b128 v[50:53], v189 offset:36864
	ds_read_b128 v[54:57], v189 offset:36880
	ds_read_b128 v[58:61], v189 offset:38912
	ds_read_b128 v[62:65], v189 offset:38928
	global_load_lds_dwordx4 v162, s[28:29]
	s_mov_b32 m0, s50
	s_nop 0
	global_load_lds_dwordx4 v166, s[28:29]
	s_waitcnt vmcnt(8) lgkmcnt(0)
	s_barrier
	s_setprio 1
	v_mfma_scale_f32_16x16x128_f8f6f4 v[158:161], v[2:9], v[34:41], v[158:161], v190, v190 op_sel_hi:[0,0,0]
	v_mfma_scale_f32_16x16x128_f8f6f4 v[154:157], v[10:17], v[34:41], v[154:157], v190, v190 op_sel_hi:[0,0,0]
	v_mfma_scale_f32_16x16x128_f8f6f4 v[150:153], v[2:9], v[42:49], v[150:153], v190, v190 op_sel_hi:[0,0,0]
	v_mfma_scale_f32_16x16x128_f8f6f4 v[146:149], v[10:17], v[42:49], v[146:149], v190, v190 op_sel_hi:[0,0,0]
	v_mfma_scale_f32_16x16x128_f8f6f4 v[126:129], v[2:9], v[50:57], v[126:129], v190, v190 op_sel_hi:[0,0,0]
	v_mfma_scale_f32_16x16x128_f8f6f4 v[122:125], v[10:17], v[50:57], v[122:125], v190, v190 op_sel_hi:[0,0,0]
	v_mfma_scale_f32_16x16x128_f8f6f4 v[118:121], v[2:9], v[58:65], v[118:121], v190, v190 op_sel_hi:[0,0,0]
	v_mfma_scale_f32_16x16x128_f8f6f4 v[110:113], v[10:17], v[58:65], v[110:113], v190, v190 op_sel_hi:[0,0,0]
	s_setprio 0
	s_setprio 1
	v_mfma_scale_f32_16x16x128_f8f6f4 v[142:145], v[18:25], v[34:41], v[142:145], v190, v190 op_sel_hi:[0,0,0]
	v_mfma_scale_f32_16x16x128_f8f6f4 v[138:141], v[26:33], v[34:41], v[138:141], v190, v190 op_sel_hi:[0,0,0]
	v_mfma_scale_f32_16x16x128_f8f6f4 v[134:137], v[18:25], v[42:49], v[134:137], v190, v190 op_sel_hi:[0,0,0]
	v_mfma_scale_f32_16x16x128_f8f6f4 v[130:133], v[26:33], v[42:49], v[130:133], v190, v190 op_sel_hi:[0,0,0]
	v_mfma_scale_f32_16x16x128_f8f6f4 v[114:117], v[18:25], v[50:57], v[114:117], v190, v190 op_sel_hi:[0,0,0]
	v_mfma_scale_f32_16x16x128_f8f6f4 v[106:109], v[26:33], v[50:57], v[106:109], v190, v190 op_sel_hi:[0,0,0]
	v_mfma_scale_f32_16x16x128_f8f6f4 v[102:105], v[18:25], v[58:65], v[102:105], v190, v190 op_sel_hi:[0,0,0]
	v_mfma_scale_f32_16x16x128_f8f6f4 v[98:101], v[26:33], v[58:65], v[98:101], v190, v190 op_sel_hi:[0,0,0]
	s_setprio 0
	s_barrier
	s_mov_b32 m0, s53
	s_add_u32 s28, s34, 0xb0080
	ds_read_b128 v[34:37], v189 offset:49152
	ds_read_b128 v[38:41], v189 offset:49168
	ds_read_b128 v[50:53], v189 offset:51200
	ds_read_b128 v[54:57], v189 offset:51216
	ds_read_b128 v[194:197], v189 offset:53248
	ds_read_b128 v[198:201], v189 offset:53264
	ds_read_b128 v[202:205], v189 offset:55296
	ds_read_b128 v[206:209], v189 offset:55312
	global_load_lds_dwordx4 v164, s[98:99]
	s_mov_b32 m0, s54
	s_addc_u32 s29, s35, 0
	global_load_lds_dwordx4 v168, s[98:99]
	s_mov_b32 m0, s57
	s_nop 0
	global_load_lds_dwordx4 v164, s[28:29]
	s_mov_b32 m0, s58
	s_nop 0
	global_load_lds_dwordx4 v168, s[28:29]
	s_mov_b32 m0, s55
	s_nop 0
	global_load_lds_dwordx4 v162, s[100:101]
	s_mov_b32 m0, s56
	s_nop 0
	global_load_lds_dwordx4 v166, s[100:101]
	s_waitcnt vmcnt(8) lgkmcnt(0)
	s_barrier
	s_setprio 1
	v_mfma_scale_f32_16x16x128_f8f6f4 v[94:97], v[2:9], v[34:41], v[94:97], v190, v190 op_sel_hi:[0,0,0]
	v_mfma_scale_f32_16x16x128_f8f6f4 v[90:93], v[10:17], v[34:41], v[90:93], v190, v190 op_sel_hi:[0,0,0]
	v_mfma_scale_f32_16x16x128_f8f6f4 v[78:81], v[2:9], v[50:57], v[78:81], v190, v190 op_sel_hi:[0,0,0]
	v_mfma_scale_f32_16x16x128_f8f6f4 v[74:77], v[10:17], v[50:57], v[74:77], v190, v190 op_sel_hi:[0,0,0]
	v_mfma_scale_f32_16x16x128_f8f6f4 v[62:65], v[2:9], v[194:201], v[226:229], v190, v190 op_sel_hi:[0,0,0]
	v_mfma_scale_f32_16x16x128_f8f6f4 v[58:61], v[10:17], v[194:201], v[230:233], v190, v190 op_sel_hi:[0,0,0]
	v_mfma_scale_f32_16x16x128_f8f6f4 v[46:49], v[2:9], v[202:209], v[234:237], v190, v190 op_sel_hi:[0,0,0]
	v_mfma_scale_f32_16x16x128_f8f6f4 v[42:45], v[10:17], v[202:209], v[238:241], v190, v190 op_sel_hi:[0,0,0]
	s_setprio 0
	s_setprio 1
	v_mfma_scale_f32_16x16x128_f8f6f4 v[86:89], v[18:25], v[34:41], v[86:89], v190, v190 op_sel_hi:[0,0,0]
	v_mfma_scale_f32_16x16x128_f8f6f4 v[82:85], v[26:33], v[34:41], v[82:85], v190, v190 op_sel_hi:[0,0,0]
	v_mfma_scale_f32_16x16x128_f8f6f4 v[70:73], v[18:25], v[50:57], v[70:73], v190, v190 op_sel_hi:[0,0,0]
	v_mfma_scale_f32_16x16x128_f8f6f4 v[66:69], v[26:33], v[50:57], v[66:69], v190, v190 op_sel_hi:[0,0,0]
	v_mfma_scale_f32_16x16x128_f8f6f4 v[54:57], v[18:25], v[194:201], v[242:245], v190, v190 op_sel_hi:[0,0,0]
	v_mfma_scale_f32_16x16x128_f8f6f4 v[50:53], v[26:33], v[194:201], v[210:213], v190, v190 op_sel_hi:[0,0,0]
	v_mfma_scale_f32_16x16x128_f8f6f4 v[38:41], v[18:25], v[202:209], v[214:217], v190, v190 op_sel_hi:[0,0,0]
	v_mfma_scale_f32_16x16x128_f8f6f4 v[34:37], v[26:33], v[202:209], v[218:221], v190, v190 op_sel_hi:[0,0,0]
	s_setprio 0
	s_barrier
	s_add_u32 s66, s66, 0x100
	s_addc_u32 s67, s67, 0
	s_cmp_ge_i32 s68, s52
	s_mov_b64 s[28:29], s[30:31]
	s_mov_b32 s34, s68
	s_cbranch_scc0 .LBB0_4217
	s_branch .LBB0_4218

;     __device__ bool next(int i, Unit& u) const { if (!b.next(i, u)) return false; const int seg = u.pn < 24 ? (u.pn >> 3) : u.pn - 21; u.pm += ((0x541320 >> (4 * seg)) & 7) * MROWS_TILES; return true; }
;     __device__ bool next(int i, Unit& u) const { if (!b.next(i, u)) return false; u.pm += (u.pn >> 3) * MROWS_TILES; return true; }
; #define PG8_STAGE(bufoff, gbase, voff) do { _Pragma("unroll") for (int _i = 0; _i < 2; ++_i) \
;         __builtin_amdgcn_global_load_lds((const unsigned*)((const char*)(gbase) + (voff)[_i]), (PG8_LAS unsigned*)(lds + (bufoff) + ldsw + _i * 8192), 16, 0, 0); } while (0)
; #define PG8_LDA(dst, b, h) do { if constexpr (DT != 1) { _Pragma("unroll") for (int m = 0; m < 4; ++m) _Pragma("unroll") for (int k = 0; k < 2; ++k) dst[m][k] = *(const PG8_LAS bf16x8*)(lds + PG8_SA(b, h) + aoff + m * 2048 + k * 1024); } \
;         else { _Pragma("unroll") for (int m = 0; m < 4; ++m) dst##8[m] = ld32(lds + PG8_SA(b, h) + aoff + m * 2048); } } while (0)
; #define PG8_WAIT_V(n) asm volatile("s_waitcnt vmcnt(" #n ")" ::: "memory")
; #define PG8_WAIT_L(n) asm volatile("s_waitcnt lgkmcnt(" #n ")" ::: "memory")
; #define PG8_BAR __builtin_amdgcn_s_barrier()
;     ...
;     for (;;) {
;         const bool has_next = S.next(ui + 1, nxt);
;         const char* nA = has_next ? (const char*)g.A + (size_t)nxt.pm * tstepA : cA; const char* nB = has_next ? (const char*)g.Bt + (size_t)nxt.pn * tstepB : cB;
;         for (int t = 0; t < nt; t += 2) {
;             const bool last = (t == nt - 2);
;             const char* a1 = cA + (size_t)(t + 1) * kstep;
;             const char* a2 = last ? nA : cA + (size_t)(t + 2) * kstep; const char* b2 = last ? nB : cB + (size_t)(t + 2) * kstep;
;             const char* a3 = a2 + kstep; const char* b3 = b2 + kstep;
;             if (last && has_next) S.a_ready(nxt);
;             if constexpr (SP2) {
;             PG8_LDB(B0, 0, 0); PG8_LDB(B1, 0, 1); PG8_SCHED; PG8_LDA(At, 0, 0); PG8_STAGE(PG8_SA(1, 1), a1 + hstepA, voffA);
;             PG8_WAIT_V(8); PG8_WAIT_L(0); PG8_BAR; PG8_MMA(0, 0, At, B0); PG8_MMA(0, 1, At, B1); PG8_BAR; PG8_SCHED;
;             PG8_LDA(At, 0, 1); PG8_STAGE(PG8_SB(0, 0), b2, voffB); PG8_STAGE(PG8_SB(0, 1), b2 + hstepB, voffB); PG8_STAGE(PG8_SA(0, 0), a2, voffA);
;             PG8_WAIT_V(8); PG8_WAIT_L(0); PG8_BAR; PG8_MMA(1, 0, At, B0); PG8_MMA(1, 1, At, B1); PG8_BAR; PG8_SCHED;
.LBB0_4348:
	s_ashr_i32 s19, s18, 31
	s_lshl_b64 s[20:21], s[18:19], 19
	s_add_u32 s20, s39, s20
	s_addc_u32 s21, s40, s21
	s_ashr_i32 s17, s16, 31
	s_lshl_b64 s[22:23], s[16:17], 19
	s_add_u32 s22, s41, s22
	v_mov_b32_e32 v161, 0
	s_addc_u32 s23, s42, s23
	s_andn2_b64 vcc, exec, s[10:11]
	v_mov_b32_e32 v160, 0
	v_mov_b32_e32 v167, 0
	v_mov_b32_e32 v166, v161
	v_mov_b32_e32 v165, 0
	v_mov_b32_e32 v164, 0
	v_mov_b32_e32 v163, 0
	v_mov_b32_e32 v162, v161
	v_mov_b32_e32 v155, 0
	v_mov_b32_e32 v154, 0
	v_mov_b32_e32 v153, 0
	v_mov_b32_e32 v152, v161
	v_mov_b32_e32 v159, 0
	v_mov_b32_e32 v158, 0
	v_mov_b32_e32 v157, 0
	v_mov_b32_e32 v156, v161
	v_mov_b32_e32 v113, 0
	v_mov_b32_e32 v112, 0
	v_mov_b32_e32 v111, 0
	v_mov_b32_e32 v110, v161
	v_mov_b32_e32 v109, 0
	v_mov_b32_e32 v108, 0
	v_mov_b32_e32 v107, 0
	v_mov_b32_e32 v106, v161
	v_mov_b32_e32 v105, 0
	v_mov_b32_e32 v104, 0
	v_mov_b32_e32 v103, 0
	v_mov_b32_e32 v102, v161
	v_mov_b32_e32 v101, 0
	v_mov_b32_e32 v100, 0
	v_mov_b32_e32 v99, 0
	v_mov_b32_e32 v98, v161
	v_mov_b32_e32 v117, 0
	v_mov_b32_e32 v116, 0
	v_mov_b32_e32 v115, 0
	v_mov_b32_e32 v114, 0
	v_mov_b32_e32 v121, 0
	v_mov_b32_e32 v120, 0
	v_mov_b32_e32 v119, 0
	v_mov_b32_e32 v118, 0
	v_mov_b32_e32 v125, 0
	v_mov_b32_e32 v124, 0
	v_mov_b32_e32 v123, 0
	v_mov_b32_e32 v122, 0
	v_mov_b32_e32 v129, 0
	v_mov_b32_e32 v128, 0
	v_mov_b32_e32 v127, 0
	v_mov_b32_e32 v126, 0
	v_mov_b32_e32 v97, 0
	v_mov_b32_e32 v96, 0
	v_mov_b32_e32 v89, 0
	v_mov_b32_e32 v88, 0
	v_mov_b32_e32 v95, 0
	v_mov_b32_e32 v94, 0
	v_mov_b32_e32 v87, 0
	v_mov_b32_e32 v86, 0
	v_mov_b32_e32 v81, 0
	v_mov_b32_e32 v80, 0
	v_mov_b32_e32 v73, 0
	v_mov_b32_e32 v72, 0
	v_mov_b32_e32 v79, 0
	v_mov_b32_e32 v78, 0
	v_mov_b32_e32 v71, 0
	v_mov_b32_e32 v70, 0
	v_mov_b32_e32 v93, 0
	v_mov_b32_e32 v92, 0
	v_mov_b32_e32 v91, 0
	v_mov_b32_e32 v90, v161
	v_mov_b32_e32 v85, 0
	v_mov_b32_e32 v84, 0
	v_mov_b32_e32 v83, 0
	v_mov_b32_e32 v82, v161
	v_mov_b32_e32 v77, 0
	v_mov_b32_e32 v76, 0
	v_mov_b32_e32 v75, 0
	v_mov_b32_e32 v74, v161
	v_mov_b32_e32 v69, 0
	v_mov_b32_e32 v68, 0
	v_mov_b32_e32 v67, 0
	v_mov_b32_e32 v66, v161
	v_mov_b32_e32 v61, 0
	v_mov_b32_e32 v60, 0
	v_mov_b32_e32 v59, 0
	v_mov_b32_e32 v58, v161
	v_mov_b32_e32 v53, 0
	v_mov_b32_e32 v52, 0
	v_mov_b32_e32 v51, 0
	v_mov_b32_e32 v50, v161
	v_mov_b32_e32 v45, 0
	v_mov_b32_e32 v44, 0
	v_mov_b32_e32 v43, 0
	v_mov_b32_e32 v42, v161
	v_mov_b32_e32 v37, 0
	v_mov_b32_e32 v36, 0
	v_mov_b32_e32 v35, 0
	v_mov_b32_e32 v34, v161
	v_mov_b32_e32 v65, 0
	v_mov_b32_e32 v64, 0
	v_mov_b32_e32 v57, 0
	v_mov_b32_e32 v56, 0
	v_mov_b32_e32 v63, 0
	v_mov_b32_e32 v62, 0
	v_mov_b32_e32 v55, 0
	v_mov_b32_e32 v54, 0
	v_mov_b32_e32 v49, 0
	v_mov_b32_e32 v48, 0
	v_mov_b32_e32 v41, 0
	v_mov_b32_e32 v40, 0
	v_mov_b32_e32 v47, 0
	v_mov_b32_e32 v46, 0
	v_mov_b32_e32 v39, 0
	v_mov_b32_e32 v38, 0
	v_mov_b32_e32 v33, 0
	v_mov_b32_e32 v32, 0
	v_mov_b32_e32 v29, 0
	v_mov_b32_e32 v28, 0
	v_mov_b32_e32 v31, 0
	v_mov_b32_e32 v30, 0
	v_mov_b32_e32 v27, 0
	v_mov_b32_e32 v26, 0
	v_mov_b32_e32 v25, 0
	v_mov_b32_e32 v24, 0
	v_mov_b32_e32 v21, 0
	v_mov_b32_e32 v20, 0
	v_mov_b32_e32 v23, 0
	v_mov_b32_e32 v22, 0
	v_mov_b32_e32 v19, 0
	v_mov_b32_e32 v18, 0
	s_cbranch_vccnz .LBB0_4352
	s_and_b64 s[30:31], s[0:1], exec
	s_cselect_b32 s17, s21, s29
	s_cselect_b32 s19, s20, s28
	s_cselect_b32 s66, s23, s27
	s_cselect_b32 s67, s22, s26
	s_add_u32 s68, s26, 0x100
	s_addc_u32 s69, s27, 0
	s_add_u32 s26, s28, 0x40080
	s_addc_u32 s27, s29, 0
	s_mov_b32 s28, 0
	s_waitcnt vmcnt(0)
	v_add_u32_e32 v164, s37, v170
	v_add_u32_e32 v168, s38, v170
	ds_read_b128 v[152:155], v164
	ds_read_b128 v[156:159], v164 offset:1024
	ds_read_b128 v[160:163], v164 offset:2048
	ds_read_b128 v[164:167], v164 offset:3072
	ds_read_b128 v[180:183], v168
	ds_read_b128 v[184:187], v168 offset:1024
	ds_read_b128 v[188:191], v168 offset:2048
	ds_read_b128 v[192:195], v168 offset:3072
	s_add_i32 s70, s28, 2
	s_add_u32 s29, s26, 0xfffc0080
	s_addc_u32 s30, s27, -1
	s_cmp_eq_u32 s64, s28
	s_cselect_b32 s28, s67, s68
	s_cselect_b32 s31, s17, s30
	s_cselect_b32 s30, s19, s29
	s_cselect_b32 s29, s66, s69
	s_add_i32 m0, s49, 0xc000
	ds_read_b128 v[196:199], v179
	ds_read_b128 v[200:203], v179 offset:1024
	ds_read_b128 v[204:207], v179 offset:2048
	ds_read_b128 v[208:211], v179 offset:3072
	ds_read_b128 v[212:215], v179 offset:4096
	ds_read_b128 v[216:219], v179 offset:5120
	ds_read_b128 v[220:223], v179 offset:6144
	ds_read_b128 v[224:227], v179 offset:7168
	global_load_lds_dwordx4 v146, s[26:27]
	s_add_i32 m0, s49, 0xe000
	s_nop 0
	global_load_lds_dwordx4 v144, s[26:27]
	s_waitcnt vmcnt(8) lgkmcnt(0)
	s_barrier
; #define PG8_STAGE(bufoff, gbase, voff) do { _Pragma("unroll") for (int _i = 0; _i < 2; ++_i) \
;         __builtin_amdgcn_global_load_lds((const unsigned*)((const char*)(gbase) + (voff)[_i]), (PG8_LAS unsigned*)(lds + (bufoff) + ldsw + _i * 8192), 16, 0, 0); } while (0)
; #define PG8_LDA(dst, b, h) do { if constexpr (DT != 1) { _Pragma("unroll") for (int m = 0; m < 4; ++m) _Pragma("unroll") for (int k = 0; k < 2; ++k) dst[m][k] = *(const PG8_LAS bf16x8*)(lds + PG8_SA(b, h) + aoff + m * 2048 + k * 1024); } \
;         else { _Pragma("unroll") for (int m = 0; m < 4; ++m) dst##8[m] = ld32(lds + PG8_SA(b, h) + aoff + m * 2048); } } while (0)
; #define PG8_WAIT_V(n) asm volatile("s_waitcnt vmcnt(" #n ")" ::: "memory")
; #define PG8_WAIT_L(n) asm volatile("s_waitcnt lgkmcnt(" #n ")" ::: "memory")
; #define PG8_BAR __builtin_amdgcn_s_barrier()
; #define PG8_SCHED __builtin_amdgcn_sched_barrier(0)
;     ...
;             PG8_WAIT_V(8); PG8_WAIT_L(0); PG8_BAR; PG8_MMA(0, 0, At, B0); PG8_MMA(0, 1, At, B1); PG8_BAR; PG8_SCHED;
;             PG8_LDA(At, 0, 1); PG8_STAGE(PG8_SB(0, 0), b2, voffB); PG8_STAGE(PG8_SB(0, 1), b2 + hstepB, voffB); PG8_STAGE(PG8_SA(0, 0), a2, voffA);
;             PG8_WAIT_V(8); PG8_WAIT_L(0); PG8_BAR; PG8_MMA(1, 0, At, B0); PG8_MMA(1, 1, At, B1); PG8_BAR; PG8_SCHED;
	s_setprio 1
	v_mfma_i32_16x16x64_i8 v[126:129], v[152:155], v[196:199], 0
	v_mfma_i32_16x16x64_i8 v[122:125], v[160:163], v[196:199], 0
	v_mfma_i32_16x16x64_i8 v[118:121], v[152:155], v[204:207], 0
	v_mfma_i32_16x16x64_i8 v[114:117], v[160:163], v[204:207], 0
	v_mfma_i32_16x16x64_i8 v[110:113], v[152:155], v[212:215], 0
	v_mfma_i32_16x16x64_i8 v[106:109], v[160:163], v[212:215], 0
	v_mfma_i32_16x16x64_i8 v[102:105], v[152:155], v[220:223], 0
	v_mfma_i32_16x16x64_i8 v[98:101], v[160:163], v[220:223], 0
	v_mfma_i32_16x16x64_i8 v[126:129], v[156:159], v[200:203], v[126:129]
	v_mfma_i32_16x16x64_i8 v[122:125], v[164:167], v[200:203], v[122:125]
	v_mfma_i32_16x16x64_i8 v[118:121], v[156:159], v[208:211], v[118:121]
	v_mfma_i32_16x16x64_i8 v[114:117], v[164:167], v[208:211], v[114:117]
	v_mfma_i32_16x16x64_i8 v[110:113], v[156:159], v[216:219], v[110:113]
	v_mfma_i32_16x16x64_i8 v[106:109], v[164:167], v[216:219], v[106:109]
	v_mfma_i32_16x16x64_i8 v[102:105], v[156:159], v[224:227], v[102:105]
	v_mfma_i32_16x16x64_i8 v[98:101], v[164:167], v[224:227], v[98:101]
	s_setprio 0
	s_setprio 1
	v_mfma_i32_16x16x64_i8 v[94:97], v[180:183], v[196:199], 0
	v_mfma_i32_16x16x64_i8 v[86:89], v[188:191], v[196:199], 0
	v_mfma_i32_16x16x64_i8 v[78:81], v[180:183], v[204:207], 0
	v_mfma_i32_16x16x64_i8 v[70:73], v[188:191], v[204:207], 0
	v_mfma_i32_16x16x64_i8 v[62:65], v[180:183], v[212:215], 0
	v_mfma_i32_16x16x64_i8 v[54:57], v[188:191], v[212:215], 0
	v_mfma_i32_16x16x64_i8 v[46:49], v[180:183], v[220:223], 0
	v_mfma_i32_16x16x64_i8 v[38:41], v[188:191], v[220:223], 0
	v_mfma_i32_16x16x64_i8 v[94:97], v[184:187], v[200:203], v[94:97]
	v_mfma_i32_16x16x64_i8 v[86:89], v[192:195], v[200:203], v[86:89]
	v_mfma_i32_16x16x64_i8 v[78:81], v[184:187], v[208:211], v[78:81]
	v_mfma_i32_16x16x64_i8 v[70:73], v[192:195], v[208:211], v[70:73]
	v_mfma_i32_16x16x64_i8 v[62:65], v[184:187], v[216:219], v[62:65]
	v_mfma_i32_16x16x64_i8 v[54:57], v[192:195], v[216:219], v[54:57]
	v_mfma_i32_16x16x64_i8 v[46:49], v[184:187], v[224:227], v[46:49]
	v_mfma_i32_16x16x64_i8 v[38:41], v[192:195], v[224:227], v[38:41]
	s_setprio 0
	s_barrier
	s_mov_b32 m0, s45
	s_add_u32 s98, s28, 0x80
	s_addc_u32 s99, s29, 0
	s_add_u32 s72, s28, 0x40000
	ds_read_b128 v[196:199], v179 offset:16384
	ds_read_b128 v[200:203], v179 offset:17408
	ds_read_b128 v[204:207], v179 offset:18432
	ds_read_b128 v[208:211], v179 offset:19456
	ds_read_b128 v[212:215], v179 offset:20480
	ds_read_b128 v[216:219], v179 offset:21504
	ds_read_b128 v[220:223], v179 offset:22528
	ds_read_b128 v[224:227], v179 offset:23552
	global_load_lds_dwordx4 v132, s[28:29]
	s_mov_b32 m0, s46
	s_addc_u32 s73, s29, 0
	global_load_lds_dwordx4 v136, s[28:29]
	s_mov_b32 m0, s47
	s_nop 0
	global_load_lds_dwordx4 v132, s[72:73]
	s_mov_b32 m0, s48
	s_nop 0
	global_load_lds_dwordx4 v136, s[72:73]
	s_add_u32 s100, s30, 0x80
	s_addc_u32 s101, s31, 0
	s_mov_b32 m0, s49
	s_nop 0
	global_load_lds_dwordx4 v130, s[30:31]
	s_mov_b32 m0, s50
	s_nop 0
	global_load_lds_dwordx4 v134, s[30:31]
	s_waitcnt vmcnt(8) lgkmcnt(0)
	s_barrier
	s_setprio 1
	v_mfma_i32_16x16x64_i8 v[90:93], v[152:155], v[196:199], 0
	v_mfma_i32_16x16x64_i8 v[82:85], v[160:163], v[196:199], 0
	v_mfma_i32_16x16x64_i8 v[74:77], v[152:155], v[204:207], 0
	v_mfma_i32_16x16x64_i8 v[66:69], v[160:163], v[204:207], 0
	v_mfma_i32_16x16x64_i8 v[58:61], v[152:155], v[212:215], 0
	v_mfma_i32_16x16x64_i8 v[50:53], v[160:163], v[212:215], 0
	v_mfma_i32_16x16x64_i8 v[42:45], v[152:155], v[220:223], 0
	v_mfma_i32_16x16x64_i8 v[34:37], v[160:163], v[220:223], 0
	v_mfma_i32_16x16x64_i8 v[90:93], v[156:159], v[200:203], v[90:93]
	v_mfma_i32_16x16x64_i8 v[82:85], v[164:167], v[200:203], v[82:85]
	v_mfma_i32_16x16x64_i8 v[74:77], v[156:159], v[208:211], v[74:77]
	v_mfma_i32_16x16x64_i8 v[66:69], v[164:167], v[208:211], v[66:69]
	v_mfma_i32_16x16x64_i8 v[58:61], v[156:159], v[216:219], v[58:61]
	v_mfma_i32_16x16x64_i8 v[50:53], v[164:167], v[216:219], v[50:53]
	v_mfma_i32_16x16x64_i8 v[42:45], v[156:159], v[224:227], v[42:45]
	v_mfma_i32_16x16x64_i8 v[34:37], v[164:167], v[224:227], v[34:37]
	s_setprio 0
	s_setprio 1
	v_mfma_i32_16x16x64_i8 v[30:33], v[180:183], v[196:199], 0
	v_mfma_i32_16x16x64_i8 v[26:29], v[188:191], v[196:199], 0
	v_mfma_i32_16x16x64_i8 v[22:25], v[180:183], v[204:207], 0
	v_mfma_i32_16x16x64_i8 v[18:21], v[188:191], v[204:207], 0
	v_mfma_i32_16x16x64_i8 v[14:17], v[180:183], v[212:215], 0
	v_mfma_i32_16x16x64_i8 v[10:13], v[188:191], v[212:215], 0
	v_mfma_i32_16x16x64_i8 v[6:9], v[180:183], v[220:223], 0
	v_mfma_i32_16x16x64_i8 v[2:5], v[188:191], v[220:223], 0
	v_mfma_i32_16x16x64_i8 v[30:33], v[184:187], v[200:203], v[30:33]
	v_mfma_i32_16x16x64_i8 v[26:29], v[192:195], v[200:203], v[26:29]
	v_mfma_i32_16x16x64_i8 v[22:25], v[184:187], v[208:211], v[22:25]
	v_mfma_i32_16x16x64_i8 v[18:21], v[192:195], v[208:211], v[18:21]
	v_mfma_i32_16x16x64_i8 v[14:17], v[184:187], v[216:219], v[14:17]
	v_mfma_i32_16x16x64_i8 v[10:13], v[192:195], v[216:219], v[10:13]
	v_mfma_i32_16x16x64_i8 v[6:9], v[184:187], v[224:227], v[6:9]
	v_mfma_i32_16x16x64_i8 v[2:5], v[192:195], v[224:227], v[2:5]
	s_setprio 0
	s_barrier
; #define PG8_STAGE(bufoff, gbase, voff) do { _Pragma("unroll") for (int _i = 0; _i < 2; ++_i) \
;         __builtin_amdgcn_global_load_lds((const unsigned*)((const char*)(gbase) + (voff)[_i]), (PG8_LAS unsigned*)(lds + (bufoff) + ldsw + _i * 8192), 16, 0, 0); } while (0)
; #define PG8_LDA(dst, b, h) do { if constexpr (DT != 1) { _Pragma("unroll") for (int m = 0; m < 4; ++m) _Pragma("unroll") for (int k = 0; k < 2; ++k) dst[m][k] = *(const PG8_LAS bf16x8*)(lds + PG8_SA(b, h) + aoff + m * 2048 + k * 1024); } \
;         else { _Pragma("unroll") for (int m = 0; m < 4; ++m) dst##8[m] = ld32(lds + PG8_SA(b, h) + aoff + m * 2048); } } while (0)
; #define PG8_LDB(dst, b, h) do { if constexpr (DT != 1) { _Pragma("unroll") for (int n = 0; n < 2; ++n) _Pragma("unroll") for (int k = 0; k < 2; ++k) dst[n][k] = *(const PG8_LAS bf16x8*)(lds + PG8_SB(b, h) + boff + n * 2048 + k * 1024); } \
;         else { _Pragma("unroll") for (int n = 0; n < 2; ++n) dst##8[n] = ld32(lds + PG8_SB(b, h) + boff + n * 2048); } } while (0)
; #define PG8_WAIT_V(n) asm volatile("s_waitcnt vmcnt(" #n ")" ::: "memory")
; #define PG8_WAIT_L(n) asm volatile("s_waitcnt lgkmcnt(" #n ")" ::: "memory")
; #define PG8_BAR __builtin_amdgcn_s_barrier()
; #define PG8_SCHED __builtin_amdgcn_sched_barrier(0)
;     ...
;             PG8_LDB(B0, 1, 0); PG8_LDB(B1, 1, 1); PG8_SCHED; PG8_LDA(At, 1, 0); PG8_STAGE(PG8_SA(0, 1), a2 + hstepA, voffA);
;             PG8_WAIT_V(8); PG8_WAIT_L(0); PG8_BAR; PG8_MMA(0, 0, At, B0); PG8_MMA(0, 1, At, B1); PG8_BAR; PG8_SCHED;
;             PG8_LDA(At, 1, 1); PG8_STAGE(PG8_SB(1, 0), b3, voffB); PG8_STAGE(PG8_SB(1, 1), b3 + hstepB, voffB); PG8_STAGE(PG8_SA(1, 0), a3, voffA);
;             PG8_WAIT_V(8); PG8_WAIT_L(0); PG8_BAR; PG8_MMA(1, 0, At, B0); PG8_MMA(1, 1, At, B1); PG8_BAR; PG8_SCHED;
	v_add_u32_e32 v164, s54, v170
	v_add_u32_e32 v192, s55, v170
	ds_read_b128 v[152:155], v164
	ds_read_b128 v[156:159], v164 offset:1024
	ds_read_b128 v[160:163], v164 offset:2048
	ds_read_b128 v[164:167], v164 offset:3072
	ds_read_b128 v[180:183], v192
	ds_read_b128 v[184:187], v192 offset:1024
	ds_read_b128 v[188:191], v192 offset:2048
	ds_read_b128 v[192:195], v192 offset:3072
	s_add_u32 s30, s30, 0x40000
	s_addc_u32 s31, s31, 0
	s_mov_b32 m0, s51
	ds_read_b128 v[196:199], v179 offset:32768
	ds_read_b128 v[200:203], v179 offset:33792
	ds_read_b128 v[204:207], v179 offset:34816
	ds_read_b128 v[208:211], v179 offset:35840
	ds_read_b128 v[212:215], v179 offset:36864
	ds_read_b128 v[216:219], v179 offset:37888
	ds_read_b128 v[220:223], v179 offset:38912
	ds_read_b128 v[224:227], v179 offset:39936
	global_load_lds_dwordx4 v130, s[30:31]
	s_mov_b32 m0, s52
	s_nop 0
	global_load_lds_dwordx4 v134, s[30:31]
	s_waitcnt vmcnt(8) lgkmcnt(0)
	s_barrier
	s_setprio 1
	v_mfma_i32_16x16x64_i8 v[126:129], v[152:155], v[196:199], v[126:129]
	v_mfma_i32_16x16x64_i8 v[122:125], v[160:163], v[196:199], v[122:125]
	v_mfma_i32_16x16x64_i8 v[118:121], v[152:155], v[204:207], v[118:121]
	v_mfma_i32_16x16x64_i8 v[114:117], v[160:163], v[204:207], v[114:117]
	v_mfma_i32_16x16x64_i8 v[110:113], v[152:155], v[212:215], v[110:113]
	v_mfma_i32_16x16x64_i8 v[106:109], v[160:163], v[212:215], v[106:109]
	v_mfma_i32_16x16x64_i8 v[102:105], v[152:155], v[220:223], v[102:105]
	v_mfma_i32_16x16x64_i8 v[98:101], v[160:163], v[220:223], v[98:101]
	v_mfma_i32_16x16x64_i8 v[126:129], v[156:159], v[200:203], v[126:129]
	v_mfma_i32_16x16x64_i8 v[122:125], v[164:167], v[200:203], v[122:125]
	v_mfma_i32_16x16x64_i8 v[118:121], v[156:159], v[208:211], v[118:121]
	v_mfma_i32_16x16x64_i8 v[114:117], v[164:167], v[208:211], v[114:117]
	v_mfma_i32_16x16x64_i8 v[110:113], v[156:159], v[216:219], v[110:113]
	v_mfma_i32_16x16x64_i8 v[106:109], v[164:167], v[216:219], v[106:109]
	v_mfma_i32_16x16x64_i8 v[102:105], v[156:159], v[224:227], v[102:105]
	v_mfma_i32_16x16x64_i8 v[98:101], v[164:167], v[224:227], v[98:101]
	s_setprio 0
	s_setprio 1
	v_mfma_i32_16x16x64_i8 v[94:97], v[180:183], v[196:199], v[94:97]
	v_mfma_i32_16x16x64_i8 v[86:89], v[188:191], v[196:199], v[86:89]
	v_mfma_i32_16x16x64_i8 v[78:81], v[180:183], v[204:207], v[78:81]
	v_mfma_i32_16x16x64_i8 v[70:73], v[188:191], v[204:207], v[70:73]
	v_mfma_i32_16x16x64_i8 v[62:65], v[180:183], v[212:215], v[62:65]
	v_mfma_i32_16x16x64_i8 v[54:57], v[188:191], v[212:215], v[54:57]
	v_mfma_i32_16x16x64_i8 v[46:49], v[180:183], v[220:223], v[46:49]
	v_mfma_i32_16x16x64_i8 v[38:41], v[188:191], v[220:223], v[38:41]
	v_mfma_i32_16x16x64_i8 v[94:97], v[184:187], v[200:203], v[94:97]
	v_mfma_i32_16x16x64_i8 v[86:89], v[192:195], v[200:203], v[86:89]
	v_mfma_i32_16x16x64_i8 v[78:81], v[184:187], v[208:211], v[78:81]
	v_mfma_i32_16x16x64_i8 v[70:73], v[192:195], v[208:211], v[70:73]
	v_mfma_i32_16x16x64_i8 v[62:65], v[184:187], v[216:219], v[62:65]
	v_mfma_i32_16x16x64_i8 v[54:57], v[192:195], v[216:219], v[54:57]
	v_mfma_i32_16x16x64_i8 v[46:49], v[184:187], v[224:227], v[46:49]
	v_mfma_i32_16x16x64_i8 v[38:41], v[192:195], v[224:227], v[38:41]
	s_setprio 0
	s_barrier
	s_mov_b32 m0, s58
	s_add_u32 s28, s28, 0x40080
	ds_read_b128 v[196:199], v179 offset:49152
	ds_read_b128 v[200:203], v179 offset:50176
	ds_read_b128 v[204:207], v179 offset:51200
	ds_read_b128 v[208:211], v179 offset:52224
	ds_read_b128 v[212:215], v179 offset:53248
	ds_read_b128 v[216:219], v179 offset:54272
	ds_read_b128 v[220:223], v179 offset:55296
	ds_read_b128 v[224:227], v179 offset:56320
	global_load_lds_dwordx4 v132, s[98:99]
	s_mov_b32 m0, s59
	s_addc_u32 s29, s29, 0
	global_load_lds_dwordx4 v136, s[98:99]
	s_mov_b32 m0, s62
	s_nop 0
	global_load_lds_dwordx4 v132, s[28:29]
	s_mov_b32 m0, s63
	s_nop 0
	global_load_lds_dwordx4 v136, s[28:29]
	s_mov_b32 m0, s60
	s_nop 0
	global_load_lds_dwordx4 v130, s[100:101]
	s_mov_b32 m0, s61
	s_nop 0
	global_load_lds_dwordx4 v134, s[100:101]
	s_waitcnt vmcnt(8) lgkmcnt(0)
	s_barrier
	s_setprio 1
	v_mfma_i32_16x16x64_i8 v[90:93], v[152:155], v[196:199], v[90:93]
	v_mfma_i32_16x16x64_i8 v[82:85], v[160:163], v[196:199], v[82:85]
	v_mfma_i32_16x16x64_i8 v[74:77], v[152:155], v[204:207], v[74:77]
	v_mfma_i32_16x16x64_i8 v[66:69], v[160:163], v[204:207], v[66:69]
	v_mfma_i32_16x16x64_i8 v[58:61], v[152:155], v[212:215], v[58:61]
	v_mfma_i32_16x16x64_i8 v[50:53], v[160:163], v[212:215], v[50:53]
	v_mfma_i32_16x16x64_i8 v[42:45], v[152:155], v[220:223], v[42:45]
	v_mfma_i32_16x16x64_i8 v[34:37], v[160:163], v[220:223], v[34:37]
	v_mfma_i32_16x16x64_i8 v[90:93], v[156:159], v[200:203], v[90:93]
	v_mfma_i32_16x16x64_i8 v[82:85], v[164:167], v[200:203], v[82:85]
	v_mfma_i32_16x16x64_i8 v[74:77], v[156:159], v[208:211], v[74:77]
	v_mfma_i32_16x16x64_i8 v[66:69], v[164:167], v[208:211], v[66:69]
	v_mfma_i32_16x16x64_i8 v[58:61], v[156:159], v[216:219], v[58:61]
	v_mfma_i32_16x16x64_i8 v[50:53], v[164:167], v[216:219], v[50:53]
	v_mfma_i32_16x16x64_i8 v[42:45], v[156:159], v[224:227], v[42:45]
	v_mfma_i32_16x16x64_i8 v[34:37], v[164:167], v[224:227], v[34:37]
	s_setprio 0
	s_setprio 1
	v_mfma_i32_16x16x64_i8 v[30:33], v[180:183], v[196:199], v[30:33]
	v_mfma_i32_16x16x64_i8 v[26:29], v[188:191], v[196:199], v[26:29]
	v_mfma_i32_16x16x64_i8 v[22:25], v[180:183], v[204:207], v[22:25]
	v_mfma_i32_16x16x64_i8 v[18:21], v[188:191], v[204:207], v[18:21]
	v_mfma_i32_16x16x64_i8 v[14:17], v[180:183], v[212:215], v[14:17]
	v_mfma_i32_16x16x64_i8 v[10:13], v[188:191], v[212:215], v[10:13]
	v_mfma_i32_16x16x64_i8 v[6:9], v[180:183], v[220:223], v[6:9]
	v_mfma_i32_16x16x64_i8 v[2:5], v[188:191], v[220:223], v[2:5]
	v_mfma_i32_16x16x64_i8 v[30:33], v[184:187], v[200:203], v[30:33]
	v_mfma_i32_16x16x64_i8 v[26:29], v[192:195], v[200:203], v[26:29]
	v_mfma_i32_16x16x64_i8 v[22:25], v[184:187], v[208:211], v[22:25]
	v_mfma_i32_16x16x64_i8 v[18:21], v[192:195], v[208:211], v[18:21]
	v_mfma_i32_16x16x64_i8 v[14:17], v[184:187], v[216:219], v[14:17]
	v_mfma_i32_16x16x64_i8 v[10:13], v[192:195], v[216:219], v[10:13]
	v_mfma_i32_16x16x64_i8 v[6:9], v[184:187], v[224:227], v[6:9]
	v_mfma_i32_16x16x64_i8 v[2:5], v[192:195], v[224:227], v[2:5]
	s_setprio 0
	s_barrier
	s_add_u32 s68, s68, 0x100
	s_addc_u32 s69, s69, 0
	s_add_u32 s26, s26, 0x100
	s_addc_u32 s27, s27, 0
	s_cmp_ge_i32 s70, s57
	s_mov_b32 s28, s70
	s_cbranch_scc0 .LBB0_4350
	s_branch .Lpx_21

; __device__ __forceinline__ f32x4 i32bits_to_f32(f32x4 v) { return (f32x4){(float)__float_as_int(v.x), (float)__float_as_int(v.y), (float)__float_as_int(v.z), (float)__float_as_int(v.w)}; }
;     __device__ __forceinline__ void operator()(const f32x4 (&acc)[2][2][4][2], const Unit& u, int wr, int wc, int fr, int fq) const {
;     ...
;                 for (int bj = 0; bj < 2; ++bj) { f32x4 v0 = acc[ai][bj][m][0], v1 = acc[ai][bj][m][1];
;                     if (IN8) { v0 = i32bits_to_f32(v0) * cs[bj][0] * rs; v1 = i32bits_to_f32(v1) * cs[bj][1] * rs; }
.Lpx_21:
	v_cvt_f32_i32_e32 v166, v126
	v_cvt_f32_i32_e32 v167, v127
	v_cvt_f32_i32_e32 v160, v128
	v_cvt_f32_i32_e32 v161, v129
	v_cvt_f32_i32_e32 v162, v122
	v_cvt_f32_i32_e32 v163, v123
	v_cvt_f32_i32_e32 v164, v124
	v_cvt_f32_i32_e32 v165, v125
	v_cvt_f32_i32_e32 v152, v118
	v_cvt_f32_i32_e32 v153, v119
	v_cvt_f32_i32_e32 v154, v120
	v_cvt_f32_i32_e32 v155, v121
	v_cvt_f32_i32_e32 v156, v114
	v_cvt_f32_i32_e32 v157, v115
	v_cvt_f32_i32_e32 v158, v116
	v_cvt_f32_i32_e32 v159, v117
	v_cvt_f32_i32_e32 v110, v110
	v_cvt_f32_i32_e32 v111, v111
	v_cvt_f32_i32_e32 v112, v112
	v_cvt_f32_i32_e32 v113, v113
	v_cvt_f32_i32_e32 v106, v106
	v_cvt_f32_i32_e32 v107, v107
	v_cvt_f32_i32_e32 v108, v108
	v_cvt_f32_i32_e32 v109, v109
	v_cvt_f32_i32_e32 v102, v102
	v_cvt_f32_i32_e32 v103, v103
	v_cvt_f32_i32_e32 v104, v104
	v_cvt_f32_i32_e32 v105, v105
	v_cvt_f32_i32_e32 v98, v98
	v_cvt_f32_i32_e32 v99, v99
	v_cvt_f32_i32_e32 v100, v100
	v_cvt_f32_i32_e32 v101, v101
	v_cvt_f32_i32_e32 v90, v90
	v_cvt_f32_i32_e32 v91, v91
	v_cvt_f32_i32_e32 v92, v92
	v_cvt_f32_i32_e32 v93, v93
	v_cvt_f32_i32_e32 v82, v82
	v_cvt_f32_i32_e32 v83, v83
	v_cvt_f32_i32_e32 v84, v84
	v_cvt_f32_i32_e32 v85, v85
	v_cvt_f32_i32_e32 v74, v74
	v_cvt_f32_i32_e32 v75, v75
	v_cvt_f32_i32_e32 v76, v76
	v_cvt_f32_i32_e32 v77, v77
	v_cvt_f32_i32_e32 v66, v66
	v_cvt_f32_i32_e32 v67, v67
	v_cvt_f32_i32_e32 v68, v68
	v_cvt_f32_i32_e32 v69, v69
	v_cvt_f32_i32_e32 v58, v58
	v_cvt_f32_i32_e32 v59, v59
	v_cvt_f32_i32_e32 v60, v60
	v_cvt_f32_i32_e32 v61, v61
	v_cvt_f32_i32_e32 v50, v50
	v_cvt_f32_i32_e32 v51, v51
	v_cvt_f32_i32_e32 v52, v52
	v_cvt_f32_i32_e32 v53, v53
	v_cvt_f32_i32_e32 v42, v42
	v_cvt_f32_i32_e32 v43, v43
	v_cvt_f32_i32_e32 v44, v44
	v_cvt_f32_i32_e32 v45, v45
	v_cvt_f32_i32_e32 v34, v34
	v_cvt_f32_i32_e32 v35, v35
	v_cvt_f32_i32_e32 v36, v36
	v_cvt_f32_i32_e32 v37, v37
	v_cvt_f32_i32_e32 v114, v94
	v_cvt_f32_i32_e32 v115, v95
	v_cvt_f32_i32_e32 v116, v96
	v_cvt_f32_i32_e32 v117, v97
	v_cvt_f32_i32_e32 v118, v86
	v_cvt_f32_i32_e32 v119, v87
	v_cvt_f32_i32_e32 v120, v88
	v_cvt_f32_i32_e32 v121, v89
	v_cvt_f32_i32_e32 v122, v78
	v_cvt_f32_i32_e32 v123, v79
	v_cvt_f32_i32_e32 v124, v80
	v_cvt_f32_i32_e32 v125, v81
	v_cvt_f32_i32_e32 v126, v70
	v_cvt_f32_i32_e32 v127, v71
	v_cvt_f32_i32_e32 v128, v72
	v_cvt_f32_i32_e32 v129, v73
	v_cvt_f32_i32_e32 v88, v62
	v_cvt_f32_i32_e32 v89, v63
	v_cvt_f32_i32_e32 v96, v64
	v_cvt_f32_i32_e32 v97, v65
	v_cvt_f32_i32_e32 v86, v54
	v_cvt_f32_i32_e32 v87, v55
	v_cvt_f32_i32_e32 v94, v56
	v_cvt_f32_i32_e32 v95, v57
	v_cvt_f32_i32_e32 v72, v46
	v_cvt_f32_i32_e32 v73, v47
	v_cvt_f32_i32_e32 v80, v48
	v_cvt_f32_i32_e32 v81, v49
	v_cvt_f32_i32_e32 v70, v38
	v_cvt_f32_i32_e32 v71, v39
	v_cvt_f32_i32_e32 v78, v40
	v_cvt_f32_i32_e32 v79, v41
	v_cvt_f32_i32_e32 v56, v30
	v_cvt_f32_i32_e32 v57, v31
	v_cvt_f32_i32_e32 v64, v32
	v_cvt_f32_i32_e32 v65, v33
	v_cvt_f32_i32_e32 v54, v26
	v_cvt_f32_i32_e32 v55, v27
	v_cvt_f32_i32_e32 v62, v28
	v_cvt_f32_i32_e32 v63, v29
	v_cvt_f32_i32_e32 v40, v22
	v_cvt_f32_i32_e32 v41, v23
	v_cvt_f32_i32_e32 v48, v24
	v_cvt_f32_i32_e32 v49, v25
	v_cvt_f32_i32_e32 v38, v18
	v_cvt_f32_i32_e32 v39, v19
	v_cvt_f32_i32_e32 v46, v20
	v_cvt_f32_i32_e32 v47, v21
	v_cvt_f32_i32_e32 v28, v14
	v_cvt_f32_i32_e32 v29, v15
	v_cvt_f32_i32_e32 v32, v16
	v_cvt_f32_i32_e32 v33, v17
	v_cvt_f32_i32_e32 v26, v10
	v_cvt_f32_i32_e32 v27, v11
	v_cvt_f32_i32_e32 v30, v12
	v_cvt_f32_i32_e32 v31, v13
	v_cvt_f32_i32_e32 v20, v6
	v_cvt_f32_i32_e32 v21, v7
	v_cvt_f32_i32_e32 v24, v8
	v_cvt_f32_i32_e32 v25, v9
	v_cvt_f32_i32_e32 v18, v2
	v_cvt_f32_i32_e32 v19, v3
	v_cvt_f32_i32_e32 v22, v4
	v_cvt_f32_i32_e32 v23, v5

; #define PG8_STAGE(bufoff, gbase, voff) do { _Pragma("unroll") for (int _i = 0; _i < 2; ++_i) \
;         __builtin_amdgcn_global_load_lds((const unsigned*)((const char*)(gbase) + (voff)[_i]), (PG8_LAS unsigned*)(lds + (bufoff) + ldsw + _i * 8192), 16, 0, 0); } while (0)
; #define PG8_LDA(dst, b, h) do { if constexpr (DT != 1) { _Pragma("unroll") for (int m = 0; m < 4; ++m) _Pragma("unroll") for (int k = 0; k < 2; ++k) dst[m][k] = *(const PG8_LAS bf16x8*)(lds + PG8_SA(b, h) + aoff + m * 2048 + k * 1024); } \
;         else { _Pragma("unroll") for (int m = 0; m < 4; ++m) dst##8[m] = ld32(lds + PG8_SA(b, h) + aoff + m * 2048); } } while (0)
; #define PG8_LDB(dst, b, h) do { if constexpr (DT != 1) { _Pragma("unroll") for (int n = 0; n < 2; ++n) _Pragma("unroll") for (int k = 0; k < 2; ++k) dst[n][k] = *(const PG8_LAS bf16x8*)(lds + PG8_SB(b, h) + boff + n * 2048 + k * 1024); } \
;         else { _Pragma("unroll") for (int n = 0; n < 2; ++n) dst##8[n] = ld32(lds + PG8_SB(b, h) + boff + n * 2048); } } while (0)
; #define PG8_WAIT_V(n) asm volatile("s_waitcnt vmcnt(" #n ")" ::: "memory")
; #define PG8_WAIT_L(n) asm volatile("s_waitcnt lgkmcnt(" #n ")" ::: "memory")
; #define PG8_BAR __builtin_amdgcn_s_barrier()
; #define PG8_SCHED __builtin_amdgcn_sched_barrier(0)
;     ...
;         for (int t = 0; t < nt; t += 2) {
;             const bool last = (t == nt - 2);
;             const char* a1 = cA + (size_t)(t + 1) * kstep;
;             const char* a2 = last ? nA : cA + (size_t)(t + 2) * kstep; const char* b2 = last ? nB : cB + (size_t)(t + 2) * kstep;
;             const char* a3 = a2 + kstep; const char* b3 = b2 + kstep;
;             if (last && has_next) S.a_ready(nxt);
;             if constexpr (SP2) {
;             PG8_LDB(B0, 0, 0); PG8_LDB(B1, 0, 1); PG8_SCHED; PG8_LDA(At, 0, 0); PG8_STAGE(PG8_SA(1, 1), a1 + hstepA, voffA);
;             PG8_WAIT_V(8); PG8_WAIT_L(0); PG8_BAR; PG8_MMA(0, 0, At, B0); PG8_MMA(0, 1, At, B1); PG8_BAR; PG8_SCHED;
;             PG8_LDA(At, 0, 1); PG8_STAGE(PG8_SB(0, 0), b2, voffB); PG8_STAGE(PG8_SB(0, 1), b2 + hstepB, voffB); PG8_STAGE(PG8_SA(0, 0), a2, voffA);
;             PG8_WAIT_V(8); PG8_WAIT_L(0); PG8_BAR; PG8_MMA(1, 0, At, B0); PG8_MMA(1, 1, At, B1); PG8_BAR; PG8_SCHED;
.Lzs_15:
	s_cbranch_vccnz .LBB0_4647
	s_and_b64 s[40:41], s[0:1], exec
	s_cselect_b32 s25, s29, s39
	s_cselect_b32 s27, s28, s38
	s_cselect_b32 s67, s31, s37
	s_cselect_b32 s68, s30, s36
	s_add_u32 s69, s36, 0x100
	s_addc_u32 s70, s37, 0
	s_add_u32 s36, s38, 0x80080
	s_addc_u32 s37, s39, 0
	s_mov_b32 s38, 0
	ds_read_b128 v[146:149], v157
	ds_read_b128 v[150:153], v157 offset:1024
	ds_read_b128 v[162:165], v157 offset:2048
	ds_read_b128 v[166:169], v157 offset:3072
	ds_read_b128 v[170:173], v158
	ds_read_b128 v[174:177], v158 offset:1024
	ds_read_b128 v[178:181], v158 offset:2048
	ds_read_b128 v[182:185], v158 offset:3072
	s_add_i32 s71, s38, 2
	s_add_u32 s39, s36, 0xfff80080
	s_addc_u32 s40, s37, -1
	s_cmp_eq_u32 s63, s38
	s_cselect_b32 s38, s68, s69
	s_cselect_b32 s41, s25, s40
	s_cselect_b32 s40, s27, s39
	s_cselect_b32 s39, s67, s70
	s_add_i32 m0, s51, 0xc000
	ds_read_b128 v[186:189], v159
	ds_read_b128 v[190:193], v159 offset:1024
	ds_read_b128 v[194:197], v159 offset:2048
	ds_read_b128 v[198:201], v159 offset:3072
	ds_read_b128 v[202:205], v159 offset:4096
	ds_read_b128 v[206:209], v159 offset:5120
	ds_read_b128 v[210:213], v159 offset:6144
	ds_read_b128 v[214:217], v159 offset:7168
	global_load_lds_dwordx4 v140, s[36:37]
	s_add_i32 m0, s51, 0xe000
	s_nop 0
	global_load_lds_dwordx4 v138, s[36:37]
	s_waitcnt vmcnt(8) lgkmcnt(0)
	s_barrier
	s_setprio 1
	v_mfma_f32_16x16x32_bf16 v[122:125], v[146:149], v[186:189], 0
	v_mfma_f32_16x16x32_bf16 v[126:129], v[162:165], v[186:189], 0
	v_mfma_f32_16x16x32_bf16 v[110:113], v[146:149], v[194:197], 0
	v_mfma_f32_16x16x32_bf16 v[106:109], v[162:165], v[194:197], 0
	v_mfma_f32_16x16x32_bf16 v[94:97], v[146:149], v[202:205], 0
	v_mfma_f32_16x16x32_bf16 v[90:93], v[162:165], v[202:205], 0
	v_mfma_f32_16x16x32_bf16 v[78:81], v[146:149], v[210:213], 0
	v_mfma_f32_16x16x32_bf16 v[74:77], v[162:165], v[210:213], 0
	v_mfma_f32_16x16x32_bf16 v[122:125], v[150:153], v[190:193], v[122:125]
	v_mfma_f32_16x16x32_bf16 v[126:129], v[166:169], v[190:193], v[126:129]
	v_mfma_f32_16x16x32_bf16 v[110:113], v[150:153], v[198:201], v[110:113]
	v_mfma_f32_16x16x32_bf16 v[106:109], v[166:169], v[198:201], v[106:109]
	v_mfma_f32_16x16x32_bf16 v[94:97], v[150:153], v[206:209], v[94:97]
	v_mfma_f32_16x16x32_bf16 v[90:93], v[166:169], v[206:209], v[90:93]
	v_mfma_f32_16x16x32_bf16 v[78:81], v[150:153], v[214:217], v[78:81]
	v_mfma_f32_16x16x32_bf16 v[74:77], v[166:169], v[214:217], v[74:77]
	s_setprio 0
	s_setprio 1
	v_mfma_f32_16x16x32_bf16 v[118:121], v[170:173], v[186:189], 0
	v_mfma_f32_16x16x32_bf16 v[114:117], v[178:181], v[186:189], 0
	v_mfma_f32_16x16x32_bf16 v[102:105], v[170:173], v[194:197], 0
	v_mfma_f32_16x16x32_bf16 v[98:101], v[178:181], v[194:197], 0
	v_mfma_f32_16x16x32_bf16 v[86:89], v[170:173], v[202:205], 0
	v_mfma_f32_16x16x32_bf16 v[82:85], v[178:181], v[202:205], 0
	v_mfma_f32_16x16x32_bf16 v[70:73], v[170:173], v[210:213], 0
	v_mfma_f32_16x16x32_bf16 v[66:69], v[178:181], v[210:213], 0
	v_mfma_f32_16x16x32_bf16 v[118:121], v[174:177], v[190:193], v[118:121]
	v_mfma_f32_16x16x32_bf16 v[114:117], v[182:185], v[190:193], v[114:117]
	v_mfma_f32_16x16x32_bf16 v[102:105], v[174:177], v[198:201], v[102:105]
	v_mfma_f32_16x16x32_bf16 v[98:101], v[182:185], v[198:201], v[98:101]
	v_mfma_f32_16x16x32_bf16 v[86:89], v[174:177], v[206:209], v[86:89]
	v_mfma_f32_16x16x32_bf16 v[82:85], v[182:185], v[206:209], v[82:85]
	v_mfma_f32_16x16x32_bf16 v[70:73], v[174:177], v[214:217], v[70:73]
	v_mfma_f32_16x16x32_bf16 v[66:69], v[182:185], v[214:217], v[66:69]
	s_setprio 0
	s_barrier
	s_mov_b32 m0, s35
	s_add_u32 s98, s38, 0x80
	s_addc_u32 s99, s39, 0
	s_add_u32 s72, s38, 0x80000
	ds_read_b128 v[186:189], v159 offset:16384
	ds_read_b128 v[190:193], v159 offset:17408
	ds_read_b128 v[194:197], v159 offset:18432
	ds_read_b128 v[198:201], v159 offset:19456
	ds_read_b128 v[202:205], v159 offset:20480
	ds_read_b128 v[206:209], v159 offset:21504
	ds_read_b128 v[210:213], v159 offset:22528
	ds_read_b128 v[214:217], v159 offset:23552
	global_load_lds_dwordx4 v132, s[38:39]
	s_mov_b32 m0, s48
	s_addc_u32 s73, s39, 0
	global_load_lds_dwordx4 v136, s[38:39]
	s_mov_b32 m0, s49
	s_nop 0
	global_load_lds_dwordx4 v132, s[72:73]
	s_mov_b32 m0, s50
	s_nop 0
	global_load_lds_dwordx4 v136, s[72:73]
	s_add_u32 s100, s40, 0x80
	s_addc_u32 s101, s41, 0
	s_mov_b32 m0, s51
	s_nop 0
	global_load_lds_dwordx4 v130, s[40:41]
	s_mov_b32 m0, s52
	s_nop 0
	global_load_lds_dwordx4 v134, s[40:41]
	s_waitcnt vmcnt(8) lgkmcnt(0)
	s_barrier
	s_setprio 1
	v_mfma_f32_16x16x32_bf16 v[62:65], v[146:149], v[186:189], 0
	v_mfma_f32_16x16x32_bf16 v[58:61], v[162:165], v[186:189], 0
	v_mfma_f32_16x16x32_bf16 v[46:49], v[146:149], v[194:197], 0
	v_mfma_f32_16x16x32_bf16 v[42:45], v[162:165], v[194:197], 0
	v_mfma_f32_16x16x32_bf16 v[30:33], v[146:149], v[202:205], 0
	v_mfma_f32_16x16x32_bf16 v[26:29], v[162:165], v[202:205], 0
	v_mfma_f32_16x16x32_bf16 v[14:17], v[146:149], v[210:213], 0
	v_mfma_f32_16x16x32_bf16 v[10:13], v[162:165], v[210:213], 0
	v_mfma_f32_16x16x32_bf16 v[62:65], v[150:153], v[190:193], v[62:65]
	v_mfma_f32_16x16x32_bf16 v[58:61], v[166:169], v[190:193], v[58:61]
	v_mfma_f32_16x16x32_bf16 v[46:49], v[150:153], v[198:201], v[46:49]
	v_mfma_f32_16x16x32_bf16 v[42:45], v[166:169], v[198:201], v[42:45]
	v_mfma_f32_16x16x32_bf16 v[30:33], v[150:153], v[206:209], v[30:33]
	v_mfma_f32_16x16x32_bf16 v[26:29], v[166:169], v[206:209], v[26:29]
	v_mfma_f32_16x16x32_bf16 v[14:17], v[150:153], v[214:217], v[14:17]
	v_mfma_f32_16x16x32_bf16 v[10:13], v[166:169], v[214:217], v[10:13]
	s_setprio 0
	s_setprio 1
	v_mfma_f32_16x16x32_bf16 v[54:57], v[170:173], v[186:189], 0
	v_mfma_f32_16x16x32_bf16 v[50:53], v[178:181], v[186:189], 0
	v_mfma_f32_16x16x32_bf16 v[38:41], v[170:173], v[194:197], 0
	v_mfma_f32_16x16x32_bf16 v[34:37], v[178:181], v[194:197], 0
	v_mfma_f32_16x16x32_bf16 v[22:25], v[170:173], v[202:205], 0
	v_mfma_f32_16x16x32_bf16 v[18:21], v[178:181], v[202:205], 0
	v_mfma_f32_16x16x32_bf16 v[6:9], v[170:173], v[210:213], 0
	v_mfma_f32_16x16x32_bf16 v[2:5], v[178:181], v[210:213], 0
	v_mfma_f32_16x16x32_bf16 v[54:57], v[174:177], v[190:193], v[54:57]
	v_mfma_f32_16x16x32_bf16 v[50:53], v[182:185], v[190:193], v[50:53]
	v_mfma_f32_16x16x32_bf16 v[38:41], v[174:177], v[198:201], v[38:41]
	v_mfma_f32_16x16x32_bf16 v[34:37], v[182:185], v[198:201], v[34:37]
	v_mfma_f32_16x16x32_bf16 v[22:25], v[174:177], v[206:209], v[22:25]
	v_mfma_f32_16x16x32_bf16 v[18:21], v[182:185], v[206:209], v[18:21]
	v_mfma_f32_16x16x32_bf16 v[6:9], v[174:177], v[214:217], v[6:9]
	v_mfma_f32_16x16x32_bf16 v[2:5], v[182:185], v[214:217], v[2:5]
	s_setprio 0
	s_barrier
; #define PG8_STAGE(bufoff, gbase, voff) do { _Pragma("unroll") for (int _i = 0; _i < 2; ++_i) \
;         __builtin_amdgcn_global_load_lds((const unsigned*)((const char*)(gbase) + (voff)[_i]), (PG8_LAS unsigned*)(lds + (bufoff) + ldsw + _i * 8192), 16, 0, 0); } while (0)
; #define PG8_LDA(dst, b, h) do { if constexpr (DT != 1) { _Pragma("unroll") for (int m = 0; m < 4; ++m) _Pragma("unroll") for (int k = 0; k < 2; ++k) dst[m][k] = *(const PG8_LAS bf16x8*)(lds + PG8_SA(b, h) + aoff + m * 2048 + k * 1024); } \
;         else { _Pragma("unroll") for (int m = 0; m < 4; ++m) dst##8[m] = ld32(lds + PG8_SA(b, h) + aoff + m * 2048); } } while (0)
; #define PG8_LDB(dst, b, h) do { if constexpr (DT != 1) { _Pragma("unroll") for (int n = 0; n < 2; ++n) _Pragma("unroll") for (int k = 0; k < 2; ++k) dst[n][k] = *(const PG8_LAS bf16x8*)(lds + PG8_SB(b, h) + boff + n * 2048 + k * 1024); } \
;         else { _Pragma("unroll") for (int n = 0; n < 2; ++n) dst##8[n] = ld32(lds + PG8_SB(b, h) + boff + n * 2048); } } while (0)
; #define PG8_WAIT_V(n) asm volatile("s_waitcnt vmcnt(" #n ")" ::: "memory")
; #define PG8_WAIT_L(n) asm volatile("s_waitcnt lgkmcnt(" #n ")" ::: "memory")
; #define PG8_BAR __builtin_amdgcn_s_barrier()
; #define PG8_SCHED __builtin_amdgcn_sched_barrier(0)
;     ...
;             PG8_LDB(B0, 1, 0); PG8_LDB(B1, 1, 1); PG8_SCHED; PG8_LDA(At, 1, 0); PG8_STAGE(PG8_SA(0, 1), a2 + hstepA, voffA);
;             PG8_WAIT_V(8); PG8_WAIT_L(0); PG8_BAR; PG8_MMA(0, 0, At, B0); PG8_MMA(0, 1, At, B1); PG8_BAR; PG8_SCHED;
;             PG8_LDA(At, 1, 1); PG8_STAGE(PG8_SB(1, 0), b3, voffB); PG8_STAGE(PG8_SB(1, 1), b3 + hstepB, voffB); PG8_STAGE(PG8_SA(1, 0), a3, voffA);
;             PG8_WAIT_V(8); PG8_WAIT_L(0); PG8_BAR; PG8_MMA(1, 0, At, B0); PG8_MMA(1, 1, At, B1); PG8_BAR; PG8_SCHED;
	ds_read_b128 v[146:149], v160
	ds_read_b128 v[150:153], v160 offset:1024
	ds_read_b128 v[162:165], v160 offset:2048
	ds_read_b128 v[166:169], v160 offset:3072
	ds_read_b128 v[170:173], v161
	ds_read_b128 v[174:177], v161 offset:1024
	ds_read_b128 v[178:181], v161 offset:2048
	ds_read_b128 v[182:185], v161 offset:3072
	s_add_u32 s40, s40, 0x80000
	s_addc_u32 s41, s41, 0
	s_mov_b32 m0, s53
	ds_read_b128 v[186:189], v159 offset:32768
	ds_read_b128 v[190:193], v159 offset:33792
	ds_read_b128 v[194:197], v159 offset:34816
	ds_read_b128 v[198:201], v159 offset:35840
	ds_read_b128 v[202:205], v159 offset:36864
	ds_read_b128 v[206:209], v159 offset:37888
	ds_read_b128 v[210:213], v159 offset:38912
	ds_read_b128 v[214:217], v159 offset:39936
	global_load_lds_dwordx4 v130, s[40:41]
	s_mov_b32 m0, s54
	s_nop 0
	global_load_lds_dwordx4 v134, s[40:41]
	s_waitcnt vmcnt(8) lgkmcnt(0)
	s_barrier
	s_setprio 1
	v_mfma_f32_16x16x32_bf16 v[122:125], v[146:149], v[186:189], v[122:125]
	v_mfma_f32_16x16x32_bf16 v[126:129], v[162:165], v[186:189], v[126:129]
	v_mfma_f32_16x16x32_bf16 v[110:113], v[146:149], v[194:197], v[110:113]
	v_mfma_f32_16x16x32_bf16 v[106:109], v[162:165], v[194:197], v[106:109]
	v_mfma_f32_16x16x32_bf16 v[94:97], v[146:149], v[202:205], v[94:97]
	v_mfma_f32_16x16x32_bf16 v[90:93], v[162:165], v[202:205], v[90:93]
	v_mfma_f32_16x16x32_bf16 v[78:81], v[146:149], v[210:213], v[78:81]
	v_mfma_f32_16x16x32_bf16 v[74:77], v[162:165], v[210:213], v[74:77]
	v_mfma_f32_16x16x32_bf16 v[122:125], v[150:153], v[190:193], v[122:125]
	v_mfma_f32_16x16x32_bf16 v[126:129], v[166:169], v[190:193], v[126:129]
	v_mfma_f32_16x16x32_bf16 v[110:113], v[150:153], v[198:201], v[110:113]
	v_mfma_f32_16x16x32_bf16 v[106:109], v[166:169], v[198:201], v[106:109]
	v_mfma_f32_16x16x32_bf16 v[94:97], v[150:153], v[206:209], v[94:97]
	v_mfma_f32_16x16x32_bf16 v[90:93], v[166:169], v[206:209], v[90:93]
	v_mfma_f32_16x16x32_bf16 v[78:81], v[150:153], v[214:217], v[78:81]
	v_mfma_f32_16x16x32_bf16 v[74:77], v[166:169], v[214:217], v[74:77]
	s_setprio 0
	s_setprio 1
	v_mfma_f32_16x16x32_bf16 v[118:121], v[170:173], v[186:189], v[118:121]
	v_mfma_f32_16x16x32_bf16 v[114:117], v[178:181], v[186:189], v[114:117]
	v_mfma_f32_16x16x32_bf16 v[102:105], v[170:173], v[194:197], v[102:105]
	v_mfma_f32_16x16x32_bf16 v[98:101], v[178:181], v[194:197], v[98:101]
	v_mfma_f32_16x16x32_bf16 v[86:89], v[170:173], v[202:205], v[86:89]
	v_mfma_f32_16x16x32_bf16 v[82:85], v[178:181], v[202:205], v[82:85]
	v_mfma_f32_16x16x32_bf16 v[70:73], v[170:173], v[210:213], v[70:73]
	v_mfma_f32_16x16x32_bf16 v[66:69], v[178:181], v[210:213], v[66:69]
	v_mfma_f32_16x16x32_bf16 v[118:121], v[174:177], v[190:193], v[118:121]
	v_mfma_f32_16x16x32_bf16 v[114:117], v[182:185], v[190:193], v[114:117]
	v_mfma_f32_16x16x32_bf16 v[102:105], v[174:177], v[198:201], v[102:105]
	v_mfma_f32_16x16x32_bf16 v[98:101], v[182:185], v[198:201], v[98:101]
	v_mfma_f32_16x16x32_bf16 v[86:89], v[174:177], v[206:209], v[86:89]
	v_mfma_f32_16x16x32_bf16 v[82:85], v[182:185], v[206:209], v[82:85]
	v_mfma_f32_16x16x32_bf16 v[70:73], v[174:177], v[214:217], v[70:73]
	v_mfma_f32_16x16x32_bf16 v[66:69], v[182:185], v[214:217], v[66:69]
	s_setprio 0
	s_barrier
	s_mov_b32 m0, s57
	s_add_u32 s38, s38, 0x80080
	ds_read_b128 v[186:189], v159 offset:49152
	ds_read_b128 v[190:193], v159 offset:50176
	ds_read_b128 v[194:197], v159 offset:51200
	ds_read_b128 v[198:201], v159 offset:52224
	ds_read_b128 v[202:205], v159 offset:53248
	ds_read_b128 v[206:209], v159 offset:54272
	ds_read_b128 v[210:213], v159 offset:55296
	ds_read_b128 v[214:217], v159 offset:56320
	global_load_lds_dwordx4 v132, s[98:99]
	s_mov_b32 m0, s58
	s_addc_u32 s39, s39, 0
	global_load_lds_dwordx4 v136, s[98:99]
	s_mov_b32 m0, s61
	s_nop 0
	global_load_lds_dwordx4 v132, s[38:39]
	s_mov_b32 m0, s62
	s_nop 0
	global_load_lds_dwordx4 v136, s[38:39]
	s_mov_b32 m0, s59
	s_nop 0
	global_load_lds_dwordx4 v130, s[100:101]
	s_mov_b32 m0, s60
	s_nop 0
	global_load_lds_dwordx4 v134, s[100:101]
	s_waitcnt vmcnt(8) lgkmcnt(0)
	s_barrier
	s_setprio 1
	v_mfma_f32_16x16x32_bf16 v[62:65], v[146:149], v[186:189], v[62:65]
	v_mfma_f32_16x16x32_bf16 v[58:61], v[162:165], v[186:189], v[58:61]
	v_mfma_f32_16x16x32_bf16 v[46:49], v[146:149], v[194:197], v[46:49]
	v_mfma_f32_16x16x32_bf16 v[42:45], v[162:165], v[194:197], v[42:45]
	v_mfma_f32_16x16x32_bf16 v[30:33], v[146:149], v[202:205], v[30:33]
	v_mfma_f32_16x16x32_bf16 v[26:29], v[162:165], v[202:205], v[26:29]
	v_mfma_f32_16x16x32_bf16 v[14:17], v[146:149], v[210:213], v[14:17]
	v_mfma_f32_16x16x32_bf16 v[10:13], v[162:165], v[210:213], v[10:13]
	v_mfma_f32_16x16x32_bf16 v[62:65], v[150:153], v[190:193], v[62:65]
	v_mfma_f32_16x16x32_bf16 v[58:61], v[166:169], v[190:193], v[58:61]
	v_mfma_f32_16x16x32_bf16 v[46:49], v[150:153], v[198:201], v[46:49]
	v_mfma_f32_16x16x32_bf16 v[42:45], v[166:169], v[198:201], v[42:45]
	v_mfma_f32_16x16x32_bf16 v[30:33], v[150:153], v[206:209], v[30:33]
	v_mfma_f32_16x16x32_bf16 v[26:29], v[166:169], v[206:209], v[26:29]
	v_mfma_f32_16x16x32_bf16 v[14:17], v[150:153], v[214:217], v[14:17]
	v_mfma_f32_16x16x32_bf16 v[10:13], v[166:169], v[214:217], v[10:13]
	s_setprio 0
	s_setprio 1
	v_mfma_f32_16x16x32_bf16 v[54:57], v[170:173], v[186:189], v[54:57]
	v_mfma_f32_16x16x32_bf16 v[50:53], v[178:181], v[186:189], v[50:53]
	v_mfma_f32_16x16x32_bf16 v[38:41], v[170:173], v[194:197], v[38:41]
	v_mfma_f32_16x16x32_bf16 v[34:37], v[178:181], v[194:197], v[34:37]
	v_mfma_f32_16x16x32_bf16 v[22:25], v[170:173], v[202:205], v[22:25]
	v_mfma_f32_16x16x32_bf16 v[18:21], v[178:181], v[202:205], v[18:21]
	v_mfma_f32_16x16x32_bf16 v[6:9], v[170:173], v[210:213], v[6:9]
	v_mfma_f32_16x16x32_bf16 v[2:5], v[178:181], v[210:213], v[2:5]
	v_mfma_f32_16x16x32_bf16 v[54:57], v[174:177], v[190:193], v[54:57]
	v_mfma_f32_16x16x32_bf16 v[50:53], v[182:185], v[190:193], v[50:53]
	v_mfma_f32_16x16x32_bf16 v[38:41], v[174:177], v[198:201], v[38:41]
	v_mfma_f32_16x16x32_bf16 v[34:37], v[182:185], v[198:201], v[34:37]
	v_mfma_f32_16x16x32_bf16 v[22:25], v[174:177], v[206:209], v[22:25]
	v_mfma_f32_16x16x32_bf16 v[18:21], v[182:185], v[206:209], v[18:21]
	v_mfma_f32_16x16x32_bf16 v[6:9], v[174:177], v[214:217], v[6:9]
	v_mfma_f32_16x16x32_bf16 v[2:5], v[182:185], v[214:217], v[2:5]
	s_setprio 0
	s_barrier
	s_add_u32 s69, s69, 0x100
	s_addc_u32 s70, s70, 0
	s_add_u32 s36, s36, 0x100
	s_addc_u32 s37, s37, 0
	s_cmp_ge_i32 s71, s56
	s_mov_b32 s38, s71
	s_cbranch_scc0 .LBB0_4646
	s_branch .LBB0_4647

; #define PG8_STAGE(bufoff, gbase, voff) do { _Pragma("unroll") for (int _i = 0; _i < 2; ++_i) \
;         __builtin_amdgcn_global_load_lds((const unsigned*)((const char*)(gbase) + (voff)[_i]), (PG8_LAS unsigned*)(lds + (bufoff) + ldsw + _i * 8192), 16, 0, 0); } while (0)
; #define PG8_LDA(dst, b, h) do { if constexpr (DT != 1) { _Pragma("unroll") for (int m = 0; m < 4; ++m) _Pragma("unroll") for (int k = 0; k < 2; ++k) dst[m][k] = *(const PG8_LAS bf16x8*)(lds + PG8_SA(b, h) + aoff + m * 2048 + k * 1024); } \
;         else { _Pragma("unroll") for (int m = 0; m < 4; ++m) dst##8[m] = ld32(lds + PG8_SA(b, h) + aoff + m * 2048); } } while (0)
; #define PG8_LDB(dst, b, h) do { if constexpr (DT != 1) { _Pragma("unroll") for (int n = 0; n < 2; ++n) _Pragma("unroll") for (int k = 0; k < 2; ++k) dst[n][k] = *(const PG8_LAS bf16x8*)(lds + PG8_SB(b, h) + boff + n * 2048 + k * 1024); } \
;         else { _Pragma("unroll") for (int n = 0; n < 2; ++n) dst##8[n] = ld32(lds + PG8_SB(b, h) + boff + n * 2048); } } while (0)
; #define PG8_WAIT_V(n) asm volatile("s_waitcnt vmcnt(" #n ")" ::: "memory")
; #define PG8_WAIT_L(n) asm volatile("s_waitcnt lgkmcnt(" #n ")" ::: "memory")
; #define PG8_BAR __builtin_amdgcn_s_barrier()
; #define PG8_SCHED __builtin_amdgcn_sched_barrier(0)
;     ...
;         for (int t = 0; t < nt; t += 2) {
;             const bool last = (t == nt - 2);
;             const char* a1 = cA + (size_t)(t + 1) * kstep;
;             const char* a2 = last ? nA : cA + (size_t)(t + 2) * kstep; const char* b2 = last ? nB : cB + (size_t)(t + 2) * kstep;
;             const char* a3 = a2 + kstep; const char* b3 = b2 + kstep;
;             if (last && has_next) S.a_ready(nxt);
;             if constexpr (SP2) {
;             PG8_LDB(B0, 0, 0); PG8_LDB(B1, 0, 1); PG8_SCHED; PG8_LDA(At, 0, 0); PG8_STAGE(PG8_SA(1, 1), a1 + hstepA, voffA);
;             PG8_WAIT_V(8); PG8_WAIT_L(0); PG8_BAR; PG8_MMA(0, 0, At, B0); PG8_MMA(0, 1, At, B1); PG8_BAR; PG8_SCHED;
;             PG8_LDA(At, 0, 1); PG8_STAGE(PG8_SB(0, 0), b2, voffB); PG8_STAGE(PG8_SB(0, 1), b2 + hstepB, voffB); PG8_STAGE(PG8_SA(0, 0), a2, voffA);
;             PG8_WAIT_V(8); PG8_WAIT_L(0); PG8_BAR; PG8_MMA(1, 0, At, B0); PG8_MMA(1, 1, At, B1); PG8_BAR; PG8_SCHED;
.Lzs_17:
	s_cbranch_vccnz .LBB0_4856
	s_add_u32 s59, s24, 0x100
	s_addc_u32 s60, s25, 0
	s_mov_b32 s26, 0
	ds_read_b128 v[16:19], v186
	ds_read_b128 v[20:23], v186 offset:16
	ds_read_b128 v[24:27], v186 offset:2048
	ds_read_b128 v[28:31], v186 offset:2064
	ds_read_b128 v[0:3], v187
	ds_read_b128 v[4:7], v187 offset:16
	ds_read_b128 v[8:11], v187 offset:2048
	ds_read_b128 v[12:15], v187 offset:2064
	s_add_i32 s61, s26, 2
	s_add_u32 s24, s22, 0x100
	s_addc_u32 s25, s23, 0
	s_cmp_eq_u32 s52, s26
	s_cselect_b32 s26, s20, s59
	s_cselect_b32 s29, s3, s25
	s_cselect_b32 s28, s2, s24
	s_cselect_b32 s27, s21, s60
	v_lshl_add_u64 v[216:217], s[22:23], 0, v[170:171]
	s_add_i32 m0, s40, 0xc000
	ds_read_b128 v[176:179], v188
	ds_read_b128 v[180:183], v188 offset:16
	ds_read_b128 v[192:195], v188 offset:2048
	ds_read_b128 v[196:199], v188 offset:2064
	ds_read_b128 v[200:203], v188 offset:4096
	ds_read_b128 v[204:207], v188 offset:4112
	ds_read_b128 v[208:211], v188 offset:6144
	ds_read_b128 v[212:215], v188 offset:6160
	global_load_lds_dwordx4 v[216:217], off
	v_lshl_add_u64 v[216:217], s[22:23], 0, v[168:169]
	s_add_i32 m0, s40, 0xe000
	s_nop 0
	global_load_lds_dwordx4 v[216:217], off
	s_waitcnt vmcnt(8) lgkmcnt(0)
	s_barrier
	s_setprio 1
	v_mfma_scale_f32_16x16x128_f8f6f4 v[156:159], v[16:23], v[176:183], 0, v189, v189 op_sel_hi:[0,0,0]
	v_mfma_scale_f32_16x16x128_f8f6f4 v[152:155], v[24:31], v[176:183], 0, v189, v189 op_sel_hi:[0,0,0]
	v_mfma_scale_f32_16x16x128_f8f6f4 v[148:151], v[16:23], v[192:199], 0, v189, v189 op_sel_hi:[0,0,0]
	v_mfma_scale_f32_16x16x128_f8f6f4 v[144:147], v[24:31], v[192:199], 0, v189, v189 op_sel_hi:[0,0,0]
	v_mfma_scale_f32_16x16x128_f8f6f4 v[128:131], v[16:23], v[200:207], 0, v189, v189 op_sel_hi:[0,0,0]
	v_mfma_scale_f32_16x16x128_f8f6f4 v[120:123], v[24:31], v[200:207], 0, v189, v189 op_sel_hi:[0,0,0]
	v_mfma_scale_f32_16x16x128_f8f6f4 v[108:111], v[16:23], v[208:215], 0, v189, v189 op_sel_hi:[0,0,0]
	v_mfma_scale_f32_16x16x128_f8f6f4 v[104:107], v[24:31], v[208:215], 0, v189, v189 op_sel_hi:[0,0,0]
	s_setprio 0
	s_setprio 1
	v_mfma_scale_f32_16x16x128_f8f6f4 v[140:143], v[0:7], v[176:183], 0, v189, v189 op_sel_hi:[0,0,0]
	v_mfma_scale_f32_16x16x128_f8f6f4 v[136:139], v[8:15], v[176:183], 0, v189, v189 op_sel_hi:[0,0,0]
	v_mfma_scale_f32_16x16x128_f8f6f4 v[132:135], v[0:7], v[192:199], 0, v189, v189 op_sel_hi:[0,0,0]
	v_mfma_scale_f32_16x16x128_f8f6f4 v[124:127], v[8:15], v[192:199], 0, v189, v189 op_sel_hi:[0,0,0]
	v_mfma_scale_f32_16x16x128_f8f6f4 v[116:119], v[0:7], v[200:207], 0, v189, v189 op_sel_hi:[0,0,0]
	v_mfma_scale_f32_16x16x128_f8f6f4 v[112:115], v[8:15], v[200:207], 0, v189, v189 op_sel_hi:[0,0,0]
	v_mfma_scale_f32_16x16x128_f8f6f4 v[100:103], v[0:7], v[208:215], 0, v189, v189 op_sel_hi:[0,0,0]
	v_mfma_scale_f32_16x16x128_f8f6f4 v[96:99], v[8:15], v[208:215], 0, v189, v189 op_sel_hi:[0,0,0]
	s_setprio 0
	s_barrier
	s_mov_b32 m0, s36
	s_add_u32 s98, s26, 0x80
	s_addc_u32 s99, s27, 0
	s_add_u32 s22, s26, 0xb0000
	ds_read_b128 v[192:195], v188 offset:16384
	ds_read_b128 v[196:199], v188 offset:16400
	ds_read_b128 v[200:203], v188 offset:18432
	ds_read_b128 v[204:207], v188 offset:18448
	ds_read_b128 v[208:211], v188 offset:20480
	ds_read_b128 v[212:215], v188 offset:20496
	ds_read_b128 v[216:219], v188 offset:22528
	ds_read_b128 v[220:223], v188 offset:22544
	global_load_lds_dwordx4 v162, s[26:27]
	s_mov_b32 m0, s37
	s_addc_u32 s23, s27, 0
	global_load_lds_dwordx4 v166, s[26:27]
	s_mov_b32 m0, s38
	s_nop 0
	global_load_lds_dwordx4 v162, s[22:23]
	s_mov_b32 m0, s39
	s_nop 0
	global_load_lds_dwordx4 v166, s[22:23]
	s_add_u32 s100, s28, 0x80
	s_addc_u32 s101, s29, 0
	s_mov_b32 m0, s40
	s_nop 0
	global_load_lds_dwordx4 v160, s[28:29]
	s_mov_b32 m0, s41
	s_nop 0
	global_load_lds_dwordx4 v164, s[28:29]
	s_waitcnt vmcnt(8) lgkmcnt(0)
	s_barrier
	s_setprio 1
	v_mfma_scale_f32_16x16x128_f8f6f4 v[92:95], v[16:23], v[192:199], 0, v189, v189 op_sel_hi:[0,0,0]
	v_mfma_scale_f32_16x16x128_f8f6f4 v[88:91], v[24:31], v[192:199], 0, v189, v189 op_sel_hi:[0,0,0]
	v_mfma_scale_f32_16x16x128_f8f6f4 v[76:79], v[16:23], v[200:207], 0, v189, v189 op_sel_hi:[0,0,0]
	v_mfma_scale_f32_16x16x128_f8f6f4 v[72:75], v[24:31], v[200:207], 0, v189, v189 op_sel_hi:[0,0,0]
	v_mfma_scale_f32_16x16x128_f8f6f4 v[224:227], v[16:23], v[208:215], 0, v189, v189 op_sel_hi:[0,0,0]
	v_mfma_scale_f32_16x16x128_f8f6f4 v[228:231], v[24:31], v[208:215], 0, v189, v189 op_sel_hi:[0,0,0]
	v_mfma_scale_f32_16x16x128_f8f6f4 v[232:235], v[16:23], v[216:223], 0, v189, v189 op_sel_hi:[0,0,0]
	v_mfma_scale_f32_16x16x128_f8f6f4 v[236:239], v[24:31], v[216:223], 0, v189, v189 op_sel_hi:[0,0,0]
	s_setprio 0
	s_setprio 1
	v_mfma_scale_f32_16x16x128_f8f6f4 v[84:87], v[0:7], v[192:199], 0, v189, v189 op_sel_hi:[0,0,0]
	v_mfma_scale_f32_16x16x128_f8f6f4 v[80:83], v[8:15], v[192:199], 0, v189, v189 op_sel_hi:[0,0,0]
	v_mfma_scale_f32_16x16x128_f8f6f4 v[68:71], v[0:7], v[200:207], 0, v189, v189 op_sel_hi:[0,0,0]
	v_mfma_scale_f32_16x16x128_f8f6f4 v[64:67], v[8:15], v[200:207], 0, v189, v189 op_sel_hi:[0,0,0]
	v_mfma_scale_f32_16x16x128_f8f6f4 v[240:243], v[0:7], v[208:215], 0, v189, v189 op_sel_hi:[0,0,0]
	v_mfma_scale_f32_16x16x128_f8f6f4 v[208:211], v[8:15], v[208:215], 0, v189, v189 op_sel_hi:[0,0,0]
	v_mfma_scale_f32_16x16x128_f8f6f4 v[212:215], v[0:7], v[216:223], 0, v189, v189 op_sel_hi:[0,0,0]
	v_mfma_scale_f32_16x16x128_f8f6f4 v[216:219], v[8:15], v[216:223], 0, v189, v189 op_sel_hi:[0,0,0]
	s_setprio 0
	s_barrier
; #define PG8_STAGE(bufoff, gbase, voff) do { _Pragma("unroll") for (int _i = 0; _i < 2; ++_i) \
;         __builtin_amdgcn_global_load_lds((const unsigned*)((const char*)(gbase) + (voff)[_i]), (PG8_LAS unsigned*)(lds + (bufoff) + ldsw + _i * 8192), 16, 0, 0); } while (0)
; #define PG8_LDA(dst, b, h) do { if constexpr (DT != 1) { _Pragma("unroll") for (int m = 0; m < 4; ++m) _Pragma("unroll") for (int k = 0; k < 2; ++k) dst[m][k] = *(const PG8_LAS bf16x8*)(lds + PG8_SA(b, h) + aoff + m * 2048 + k * 1024); } \
;         else { _Pragma("unroll") for (int m = 0; m < 4; ++m) dst##8[m] = ld32(lds + PG8_SA(b, h) + aoff + m * 2048); } } while (0)
; #define PG8_LDB(dst, b, h) do { if constexpr (DT != 1) { _Pragma("unroll") for (int n = 0; n < 2; ++n) _Pragma("unroll") for (int k = 0; k < 2; ++k) dst[n][k] = *(const PG8_LAS bf16x8*)(lds + PG8_SB(b, h) + boff + n * 2048 + k * 1024); } \
;         else { _Pragma("unroll") for (int n = 0; n < 2; ++n) dst##8[n] = ld32(lds + PG8_SB(b, h) + boff + n * 2048); } } while (0)
; #define PG8_WAIT_V(n) asm volatile("s_waitcnt vmcnt(" #n ")" ::: "memory")
; #define PG8_WAIT_L(n) asm volatile("s_waitcnt lgkmcnt(" #n ")" ::: "memory")
; #define PG8_BAR __builtin_amdgcn_s_barrier()
; #define PG8_SCHED __builtin_amdgcn_sched_barrier(0)
;     ...
;             if constexpr (SP2) {
;             PG8_LDB(B0, 0, 0); PG8_LDB(B1, 0, 1); PG8_SCHED; PG8_LDA(At, 0, 0); PG8_STAGE(PG8_SA(1, 1), a1 + hstepA, voffA);
;             PG8_WAIT_V(8); PG8_WAIT_L(0); PG8_BAR; PG8_MMA(0, 0, At, B0); PG8_MMA(0, 1, At, B1); PG8_BAR; PG8_SCHED;
;             PG8_LDA(At, 0, 1); PG8_STAGE(PG8_SB(0, 0), b2, voffB); PG8_STAGE(PG8_SB(0, 1), b2 + hstepB, voffB); PG8_STAGE(PG8_SA(0, 0), a2, voffA);
;             PG8_WAIT_V(8); PG8_WAIT_L(0); PG8_BAR; PG8_MMA(1, 0, At, B0); PG8_MMA(1, 1, At, B1); PG8_BAR; PG8_SCHED;
;             PG8_LDB(B0, 1, 0); PG8_LDB(B1, 1, 1); PG8_SCHED; PG8_LDA(At, 1, 0); PG8_STAGE(PG8_SA(0, 1), a2 + hstepA, voffA);
;             PG8_WAIT_V(8); PG8_WAIT_L(0); PG8_BAR; PG8_MMA(0, 0, At, B0); PG8_MMA(0, 1, At, B1); PG8_BAR; PG8_SCHED;
;             PG8_LDA(At, 1, 1); PG8_STAGE(PG8_SB(1, 0), b3, voffB); PG8_STAGE(PG8_SB(1, 1), b3 + hstepB, voffB); PG8_STAGE(PG8_SA(1, 0), a3, voffA);
;             PG8_WAIT_V(8); PG8_WAIT_L(0); PG8_BAR; PG8_MMA(1, 0, At, B0); PG8_MMA(1, 1, At, B1); PG8_BAR; PG8_SCHED;
	ds_read_b128 v[0:3], v190
	ds_read_b128 v[4:7], v190 offset:16
	ds_read_b128 v[8:11], v190 offset:2048
	ds_read_b128 v[12:15], v190 offset:2064
	ds_read_b128 v[16:19], v191
	ds_read_b128 v[20:23], v191 offset:16
	ds_read_b128 v[24:27], v191 offset:2048
	ds_read_b128 v[28:31], v191 offset:2064
	s_add_u32 s22, s28, 0xb0000
	s_addc_u32 s23, s29, 0
	s_mov_b32 m0, s42
	ds_read_b128 v[32:35], v188 offset:32768
	ds_read_b128 v[36:39], v188 offset:32784
	ds_read_b128 v[40:43], v188 offset:34816
	ds_read_b128 v[44:47], v188 offset:34832
	ds_read_b128 v[48:51], v188 offset:36864
	ds_read_b128 v[52:55], v188 offset:36880
	ds_read_b128 v[56:59], v188 offset:38912
	ds_read_b128 v[60:63], v188 offset:38928
	global_load_lds_dwordx4 v160, s[22:23]
	s_mov_b32 m0, s43
	s_nop 0
	global_load_lds_dwordx4 v164, s[22:23]
	s_waitcnt vmcnt(8) lgkmcnt(0)
	s_barrier
	s_setprio 1
	v_mfma_scale_f32_16x16x128_f8f6f4 v[156:159], v[0:7], v[32:39], v[156:159], v189, v189 op_sel_hi:[0,0,0]
	v_mfma_scale_f32_16x16x128_f8f6f4 v[152:155], v[8:15], v[32:39], v[152:155], v189, v189 op_sel_hi:[0,0,0]
	v_mfma_scale_f32_16x16x128_f8f6f4 v[148:151], v[0:7], v[40:47], v[148:151], v189, v189 op_sel_hi:[0,0,0]
	v_mfma_scale_f32_16x16x128_f8f6f4 v[144:147], v[8:15], v[40:47], v[144:147], v189, v189 op_sel_hi:[0,0,0]
	v_mfma_scale_f32_16x16x128_f8f6f4 v[128:131], v[0:7], v[48:55], v[128:131], v189, v189 op_sel_hi:[0,0,0]
	v_mfma_scale_f32_16x16x128_f8f6f4 v[120:123], v[8:15], v[48:55], v[120:123], v189, v189 op_sel_hi:[0,0,0]
	v_mfma_scale_f32_16x16x128_f8f6f4 v[108:111], v[0:7], v[56:63], v[108:111], v189, v189 op_sel_hi:[0,0,0]
	v_mfma_scale_f32_16x16x128_f8f6f4 v[104:107], v[8:15], v[56:63], v[104:107], v189, v189 op_sel_hi:[0,0,0]
	s_setprio 0
	s_setprio 1
	v_mfma_scale_f32_16x16x128_f8f6f4 v[140:143], v[16:23], v[32:39], v[140:143], v189, v189 op_sel_hi:[0,0,0]
	v_mfma_scale_f32_16x16x128_f8f6f4 v[136:139], v[24:31], v[32:39], v[136:139], v189, v189 op_sel_hi:[0,0,0]
	v_mfma_scale_f32_16x16x128_f8f6f4 v[132:135], v[16:23], v[40:47], v[132:135], v189, v189 op_sel_hi:[0,0,0]
	v_mfma_scale_f32_16x16x128_f8f6f4 v[124:127], v[24:31], v[40:47], v[124:127], v189, v189 op_sel_hi:[0,0,0]
	v_mfma_scale_f32_16x16x128_f8f6f4 v[116:119], v[16:23], v[48:55], v[116:119], v189, v189 op_sel_hi:[0,0,0]
	v_mfma_scale_f32_16x16x128_f8f6f4 v[112:115], v[24:31], v[48:55], v[112:115], v189, v189 op_sel_hi:[0,0,0]
	v_mfma_scale_f32_16x16x128_f8f6f4 v[100:103], v[16:23], v[56:63], v[100:103], v189, v189 op_sel_hi:[0,0,0]
	v_mfma_scale_f32_16x16x128_f8f6f4 v[96:99], v[24:31], v[56:63], v[96:99], v189, v189 op_sel_hi:[0,0,0]
	s_setprio 0
	s_barrier
	s_mov_b32 m0, s46
	s_add_u32 s22, s26, 0xb0080
	ds_read_b128 v[32:35], v188 offset:49152
	ds_read_b128 v[36:39], v188 offset:49168
	ds_read_b128 v[48:51], v188 offset:51200
	ds_read_b128 v[52:55], v188 offset:51216
	ds_read_b128 v[192:195], v188 offset:53248
	ds_read_b128 v[196:199], v188 offset:53264
	ds_read_b128 v[200:203], v188 offset:55296
	ds_read_b128 v[204:207], v188 offset:55312
	global_load_lds_dwordx4 v162, s[98:99]
	s_mov_b32 m0, s47
	s_addc_u32 s23, s27, 0
	global_load_lds_dwordx4 v166, s[98:99]
	s_mov_b32 m0, s50
	s_nop 0
	global_load_lds_dwordx4 v162, s[22:23]
	s_mov_b32 m0, s51
	s_nop 0
	global_load_lds_dwordx4 v166, s[22:23]
	s_mov_b32 m0, s48
	s_nop 0
	global_load_lds_dwordx4 v160, s[100:101]
	s_mov_b32 m0, s49
	s_nop 0
	global_load_lds_dwordx4 v164, s[100:101]
	s_waitcnt vmcnt(8) lgkmcnt(0)
	s_barrier
	s_setprio 1
	v_mfma_scale_f32_16x16x128_f8f6f4 v[92:95], v[0:7], v[32:39], v[92:95], v189, v189 op_sel_hi:[0,0,0]
	v_mfma_scale_f32_16x16x128_f8f6f4 v[88:91], v[8:15], v[32:39], v[88:91], v189, v189 op_sel_hi:[0,0,0]
	v_mfma_scale_f32_16x16x128_f8f6f4 v[76:79], v[0:7], v[48:55], v[76:79], v189, v189 op_sel_hi:[0,0,0]
	v_mfma_scale_f32_16x16x128_f8f6f4 v[72:75], v[8:15], v[48:55], v[72:75], v189, v189 op_sel_hi:[0,0,0]
	v_mfma_scale_f32_16x16x128_f8f6f4 v[60:63], v[0:7], v[192:199], v[224:227], v189, v189 op_sel_hi:[0,0,0]
	v_mfma_scale_f32_16x16x128_f8f6f4 v[56:59], v[8:15], v[192:199], v[228:231], v189, v189 op_sel_hi:[0,0,0]
	v_mfma_scale_f32_16x16x128_f8f6f4 v[44:47], v[0:7], v[200:207], v[232:235], v189, v189 op_sel_hi:[0,0,0]
	v_mfma_scale_f32_16x16x128_f8f6f4 v[40:43], v[8:15], v[200:207], v[236:239], v189, v189 op_sel_hi:[0,0,0]
	s_setprio 0
	s_setprio 1
	v_mfma_scale_f32_16x16x128_f8f6f4 v[84:87], v[16:23], v[32:39], v[84:87], v189, v189 op_sel_hi:[0,0,0]
	v_mfma_scale_f32_16x16x128_f8f6f4 v[80:83], v[24:31], v[32:39], v[80:83], v189, v189 op_sel_hi:[0,0,0]
	v_mfma_scale_f32_16x16x128_f8f6f4 v[68:71], v[16:23], v[48:55], v[68:71], v189, v189 op_sel_hi:[0,0,0]
	v_mfma_scale_f32_16x16x128_f8f6f4 v[64:67], v[24:31], v[48:55], v[64:67], v189, v189 op_sel_hi:[0,0,0]
	v_mfma_scale_f32_16x16x128_f8f6f4 v[52:55], v[16:23], v[192:199], v[240:243], v189, v189 op_sel_hi:[0,0,0]
	v_mfma_scale_f32_16x16x128_f8f6f4 v[48:51], v[24:31], v[192:199], v[208:211], v189, v189 op_sel_hi:[0,0,0]
	v_mfma_scale_f32_16x16x128_f8f6f4 v[36:39], v[16:23], v[200:207], v[212:215], v189, v189 op_sel_hi:[0,0,0]
	v_mfma_scale_f32_16x16x128_f8f6f4 v[32:35], v[24:31], v[200:207], v[216:219], v189, v189 op_sel_hi:[0,0,0]
	s_setprio 0
	s_barrier
	s_add_u32 s59, s59, 0x100
	s_addc_u32 s60, s60, 0
	s_cmp_ge_i32 s61, s45
	s_mov_b64 s[22:23], s[24:25]
	s_mov_b32 s26, s61
	s_cbranch_scc0 .LBB0_4855
	s_branch .LBB0_4856
